# hoist loop-invariant lane staging offset chains out of 11 GEMM K-loops; P1a vmcnt(0) moved to preheader
# speedup vs baseline: 1.0296x; 1.0296x over previous
; __device__ __forceinline__ int lane_id() { int l; asm volatile("v_mbcnt_lo_u32_b32 %0, -1, 0\n\tv_mbcnt_hi_u32_b32 %0, -1, %0" : "=v"(l)); return l; }
; #define G_STAGE(bufoff, gbase, voff) do { _Pragma("unroll") for (int _i = 0; _i < 2; ++_i) \
;         __builtin_amdgcn_global_load_lds((const unsigned*)((const char*)(gbase) + (voff)[_i]), (LAS unsigned*)(lds + (bufoff) + ldsw + _i * 8192), 16, 0, 0); } while (0)
; #define G_LDA(dst, b, h) do { _Pragma("unroll") for (int m = 0; m < 4; ++m) G_LD8(dst[m], lds + G_SA(b, h) + aoff + m * 2048); } while (0)
; #define G_LDB(dst, b, h) do { _Pragma("unroll") for (int n = 0; n < 2; ++n) G_LD8(dst[n], lds + G_SB(b, h) + boff + n * 2048); } while (0)
; #define G_SCHED __builtin_amdgcn_sched_barrier(0)
;     ...
;         for (int t = 0; t < nt; t += 2) {
;             const bool last = (t == nt - 2);
;             { const int tz_ = wid * 64 + lane_id();
; #pragma unroll
;               for (int i = 0; i < 2; ++i) { int R, C; stage_rc(tz_ * 16 + i * 8192, R, C); const int Rb = Epi::PERM ? ((R & ~31) + perm32(R & 31)) : R;
;                   voffA[i] = (unsigned)(R * S.multA * S.pitchA + C) * 2u; voffB[i] = (unsigned)(Rb * S.multB * S.pitchB + C) * 2u; } }
;             if constexpr (GATHER) asm volatile("" : "+v"(gc0[0]), "+v"(gc0[1]), "+v"(gc1[0]), "+v"(gc1[1]));
;             if constexpr (PREF) { if (t == nt - 4) S.prefetch(nxt, lds); }
;             const char* a11 = cur.a1 + (size_t)(t + 1) * kstep;
;             const char* a02 = last ? nxt.a0 : cur.a0 + (size_t)(t + 2) * kstep; const char* a12 = last ? nxt.a1 : cur.a1 + (size_t)(t + 2) * kstep;
;             const char* b02 = last ? nxt.b0 : cur.b0 + (size_t)(t + 2) * kstep; const char* b12 = last ? nxt.b1 : cur.b1 + (size_t)(t + 2) * kstep;
;             G_LDB(B0, 0, 0); G_LDB(B1, 0, 1); G_SCHED; G_LDA(At, 0, 0); G_STAGE(G_SA(1, 1), a11, vA1);
;     ...
;         for (int a = 0; a < 2; ++a)
; #pragma unroll
;             for (int b = 0; b < 2; ++b)
; #pragma unroll
;                 for (int m = 0; m < 4; ++m)
; #pragma unroll
;                     for (int n = 0; n < 2; ++n) acc[a][b][m][n] = (acc_t){0, 0, 0, 0};
;         cur = nxt; ++ui;
.LBB0_178:
	s_add_u32 s0, s80, 0x100
	s_addc_u32 s2, s81, 0
	s_add_u32 s5, s78, 0x100
	s_addc_u32 s6, s79, 0
	s_add_u32 s19, s76, 0x100
	s_addc_u32 s33, s77, 0
	s_add_u32 s74, s74, 0x80
	s_addc_u32 s75, s75, 0
	s_mov_b32 s59, 0
	v_mov_b32_e32 v0, 0
	v_mov_b32_e32 v1, 0
	v_mov_b32_e32 v2, 0
	v_mov_b32_e32 v3, 0
	v_mov_b32_e32 v8, 0
	v_mov_b32_e32 v9, 0
	v_mov_b32_e32 v10, 0
	v_mov_b32_e32 v11, 0
	v_mov_b32_e32 v16, 0
	v_mov_b32_e32 v17, 0
	v_mov_b32_e32 v18, 0
	v_mov_b32_e32 v19, 0
	v_mov_b32_e32 v24, 0
	v_mov_b32_e32 v25, 0
	v_mov_b32_e32 v26, 0
	v_mov_b32_e32 v27, 0
	v_mov_b32_e32 v48, 0
	v_mov_b32_e32 v49, 0
	v_mov_b32_e32 v50, 0
	v_mov_b32_e32 v51, 0
	v_mov_b32_e32 v56, 0
	v_mov_b32_e32 v57, 0
	v_mov_b32_e32 v58, 0
	v_mov_b32_e32 v59, 0
	v_mov_b32_e32 v64, 0
	v_mov_b32_e32 v65, 0
	v_mov_b32_e32 v66, 0
	v_mov_b32_e32 v67, 0
	v_mov_b32_e32 v72, 0
	v_mov_b32_e32 v73, 0
	v_mov_b32_e32 v74, 0
	v_mov_b32_e32 v75, 0
	v_mov_b32_e32 v4, 0
	v_mov_b32_e32 v5, 0
	v_mov_b32_e32 v6, 0
	v_mov_b32_e32 v7, 0
	v_mov_b32_e32 v12, 0
	v_mov_b32_e32 v13, 0
	v_mov_b32_e32 v14, 0
	v_mov_b32_e32 v15, 0
	v_mov_b32_e32 v20, 0
	v_mov_b32_e32 v21, 0
	v_mov_b32_e32 v22, 0
	v_mov_b32_e32 v23, 0
	v_mov_b32_e32 v28, 0
	v_mov_b32_e32 v29, 0
	v_mov_b32_e32 v30, 0
	v_mov_b32_e32 v31, 0
	v_mov_b32_e32 v52, 0
	v_mov_b32_e32 v53, 0
	v_mov_b32_e32 v54, 0
	v_mov_b32_e32 v55, 0
	v_mov_b32_e32 v60, 0
	v_mov_b32_e32 v61, 0
	v_mov_b32_e32 v62, 0
	v_mov_b32_e32 v63, 0
	v_mov_b32_e32 v68, 0
	v_mov_b32_e32 v69, 0
	v_mov_b32_e32 v70, 0
	v_mov_b32_e32 v71, 0
	v_mov_b32_e32 v76, 0
	v_mov_b32_e32 v77, 0
	v_mov_b32_e32 v78, 0
	v_mov_b32_e32 v79, 0
	v_mov_b32_e32 v80, 0
	v_mov_b32_e32 v81, 0
	v_mov_b32_e32 v82, 0
	v_mov_b32_e32 v83, 0
	v_mov_b32_e32 v88, 0
	v_mov_b32_e32 v89, 0
	v_mov_b32_e32 v90, 0
	v_mov_b32_e32 v91, 0
	v_mov_b32_e32 v96, 0
	v_mov_b32_e32 v97, 0
	v_mov_b32_e32 v98, 0
	v_mov_b32_e32 v99, 0
	v_mov_b32_e32 v104, 0
	v_mov_b32_e32 v105, 0
	v_mov_b32_e32 v106, 0
	v_mov_b32_e32 v107, 0
	v_mov_b32_e32 v112, 0
	v_mov_b32_e32 v113, 0
	v_mov_b32_e32 v114, 0
	v_mov_b32_e32 v115, 0
	v_mov_b32_e32 v120, 0
	v_mov_b32_e32 v121, 0
	v_mov_b32_e32 v122, 0
	v_mov_b32_e32 v123, 0
	v_mov_b32_e32 v128, 0
	v_mov_b32_e32 v129, 0
	v_mov_b32_e32 v130, 0
	v_mov_b32_e32 v131, 0
	v_mov_b32_e32 v136, 0
	v_mov_b32_e32 v137, 0
	v_mov_b32_e32 v138, 0
	v_mov_b32_e32 v139, 0
	v_mov_b32_e32 v84, 0
	v_mov_b32_e32 v85, 0
	v_mov_b32_e32 v86, 0
	v_mov_b32_e32 v87, 0
	v_mov_b32_e32 v92, 0
	v_mov_b32_e32 v93, 0
	v_mov_b32_e32 v94, 0
	v_mov_b32_e32 v95, 0
	v_mov_b32_e32 v100, 0
	v_mov_b32_e32 v101, 0
	v_mov_b32_e32 v102, 0
	v_mov_b32_e32 v103, 0
	v_mov_b32_e32 v108, 0
	v_mov_b32_e32 v109, 0
	v_mov_b32_e32 v110, 0
	v_mov_b32_e32 v111, 0
	v_mov_b32_e32 v116, 0
	v_mov_b32_e32 v117, 0
	v_mov_b32_e32 v118, 0
	v_mov_b32_e32 v119, 0
	v_mov_b32_e32 v124, 0
	v_mov_b32_e32 v125, 0
	v_mov_b32_e32 v126, 0
	v_mov_b32_e32 v127, 0
	v_mov_b32_e32 v132, 0
	v_mov_b32_e32 v133, 0
	v_mov_b32_e32 v134, 0
	v_mov_b32_e32 v135, 0
	v_mov_b32_e32 v140, 0
	v_mov_b32_e32 v141, 0
	v_mov_b32_e32 v142, 0
	v_mov_b32_e32 v143, 0
	s_waitcnt vmcnt(0)
	v_mbcnt_lo_u32_b32 v248, -1, 0
	v_mbcnt_hi_u32_b32 v248, -1, v248
	v_mov_b32_e32 v249, s88
	v_lshrrev_b32_e32 v249, 6, v249
	v_and_b32_e32 v250, 3, v248
	v_lshlrev_b32_e32 v250, 4, v250
	v_and_b32_e32 v251, 32, v248
	v_xor_b32_e32 v250, v250, v251
	v_and_b32_e32 v251, 1, v249
	v_lshl_add_u32 v250, v251, 6, v250
	v_lshrrev_b32_e32 v251, 1, v249
	v_lshrrev_b32_e32 v252, 2, v248
	v_lshl_add_u32 v251, v251, 4, v252
	v_mov_b32_e32 v253, 0x800
	v_mad_u32_u24 v240, v251, v253, v250
	v_add_u32_e32 v242, 0x20000, v240
	v_lshrrev_b32_e32 v251, 2, v249
	v_lshlrev_b32_e32 v251, 5, v251
	v_lshrrev_b32_e32 v252, 4, v248
	v_lshl_add_u32 v251, v252, 3, v251
	v_bfe_u32 v252, v249, 1, 1
	v_lshl_add_u32 v251, v252, 2, v251
	v_bfe_u32 v252, v248, 2, 2
	v_add_u32_e32 v251, v251, v252
	v_mov_b32_e32 v253, 0x800
	v_mad_u32_u24 v244, v251, v253, v250
	v_add_u32_e32 v246, 0x20000, v244
	v_mov_b32_e32 v241, 0
	v_mov_b32_e32 v243, 0
	v_mov_b32_e32 v245, 0
	v_mov_b32_e32 v247, 0
.LBB0_179:
	v_add_u32_e32 v144, s91, v163
	v_add_u32_e32 v170, s3, v163
	ds_read_b128 v[34:37], v144
	ds_read_b128 v[38:41], v144 offset:1024
	ds_read_b128 v[42:45], v144 offset:2048
	ds_read_b128 v[144:147], v144 offset:3072
	ds_read_b128 v[150:153], v170
	ds_read_b128 v[154:157], v170 offset:1024
	ds_read_b128 v[166:169], v170 offset:2048
	ds_read_b128 v[170:173], v170 offset:3072
	s_add_i32 s63, s59, 2
	s_add_u32 s73, s74, 0x80
	s_addc_u32 s76, s75, 0
	s_add_i32 s83, s91, s97
	s_add_i32 m0, s22, 0xc000
	s_add_i32 s82, s22, 0xe000
	s_add_i32 s89, s83, 0x2000
	s_cmp_eq_u32 s20, s59
	s_cselect_b32 s79, s65, s33
	s_cselect_b32 s78, s64, s19
	s_cselect_b32 s81, s69, s2
	s_cselect_b32 s80, s68, s0
	s_cselect_b32 s77, s67, s76
	s_cselect_b32 s76, s66, s73
	ds_read_b128 v[174:177], v164
	ds_read_b128 v[178:181], v164 offset:1024
	ds_read_b128 v[182:185], v164 offset:2048
	ds_read_b128 v[186:189], v164 offset:3072
	ds_read_b128 v[190:193], v164 offset:4096
	ds_read_b128 v[194:197], v164 offset:5120
	ds_read_b128 v[198:201], v164 offset:6144
	ds_read_b128 v[202:205], v164 offset:7168
	global_load_lds_dwordx4 v240, s[74:75]
	s_mov_b32 m0, s82
	s_nop 0
	global_load_lds_dwordx4 v242, s[74:75]
	s_waitcnt lgkmcnt(0)
	v_mov_b32_e32 v33, v149
	s_barrier
; #define G_STAGE(bufoff, gbase, voff) do { _Pragma("unroll") for (int _i = 0; _i < 2; ++_i) \
;         __builtin_amdgcn_global_load_lds((const unsigned*)((const char*)(gbase) + (voff)[_i]), (LAS unsigned*)(lds + (bufoff) + ldsw + _i * 8192), 16, 0, 0); } while (0)
; #define G_LDA(dst, b, h) do { _Pragma("unroll") for (int m = 0; m < 4; ++m) G_LD8(dst[m], lds + G_SA(b, h) + aoff + m * 2048); } while (0)
; #define G_WAIT_V(n) asm volatile("s_waitcnt vmcnt(" #n ")" ::: "memory")
; #define G_WAIT_L(n) asm volatile("s_waitcnt lgkmcnt(" #n ")" ::: "memory")
; #define G_BAR __builtin_amdgcn_s_barrier()
; #define G_SCHED __builtin_amdgcn_sched_barrier(0)
;     ...
;             G_WAIT_L(0); G_BAR; G_MMA(0, 0, At, B0); G_MMA(0, 1, At, B1); G_WAIT_V(8); G_BAR; G_SCHED;
;             G_LDA(At, 0, 1); G_STAGE(G_SB(0, 0), b02, voffB); G_STAGE(G_SB(0, 1), b12, voffB); G_STAGE(G_SA(0, 0), a02, vA0);
;             G_WAIT_L(0); G_BAR; G_MMA(1, 0, At, B0); G_MMA(1, 1, At, B1); G_WAIT_V(8); G_BAR; G_SCHED;
	s_setprio 1
	s_waitcnt lgkmcnt(0)
	v_mfma_i32_16x16x64_i8 v[140:143], v[34:37], v[174:177], v[140:143]
	v_mfma_i32_16x16x64_i8 v[132:135], v[42:45], v[174:177], v[132:135]
	v_mfma_i32_16x16x64_i8 v[124:127], v[34:37], v[182:185], v[124:127]
	v_mfma_i32_16x16x64_i8 v[116:119], v[42:45], v[182:185], v[116:119]
	v_mfma_i32_16x16x64_i8 v[108:111], v[34:37], v[190:193], v[108:111]
	v_mfma_i32_16x16x64_i8 v[100:103], v[42:45], v[190:193], v[100:103]
	v_mfma_i32_16x16x64_i8 v[92:95], v[34:37], v[198:201], v[92:95]
	v_mfma_i32_16x16x64_i8 v[84:87], v[42:45], v[198:201], v[84:87]
	v_mfma_i32_16x16x64_i8 v[140:143], v[38:41], v[178:181], v[140:143]
	v_mfma_i32_16x16x64_i8 v[132:135], v[144:147], v[178:181], v[132:135]
	v_mfma_i32_16x16x64_i8 v[124:127], v[38:41], v[186:189], v[124:127]
	v_mfma_i32_16x16x64_i8 v[116:119], v[144:147], v[186:189], v[116:119]
	v_mfma_i32_16x16x64_i8 v[108:111], v[38:41], v[194:197], v[108:111]
	v_mfma_i32_16x16x64_i8 v[100:103], v[144:147], v[194:197], v[100:103]
	v_mfma_i32_16x16x64_i8 v[92:95], v[38:41], v[202:205], v[92:95]
	v_mfma_i32_16x16x64_i8 v[84:87], v[144:147], v[202:205], v[84:87]
	s_setprio 0
	s_setprio 1
	v_mfma_i32_16x16x64_i8 v[136:139], v[150:153], v[174:177], v[136:139]
	v_mfma_i32_16x16x64_i8 v[128:131], v[166:169], v[174:177], v[128:131]
	v_mfma_i32_16x16x64_i8 v[120:123], v[150:153], v[182:185], v[120:123]
	v_mfma_i32_16x16x64_i8 v[112:115], v[166:169], v[182:185], v[112:115]
	v_mfma_i32_16x16x64_i8 v[104:107], v[150:153], v[190:193], v[104:107]
	v_mfma_i32_16x16x64_i8 v[96:99], v[166:169], v[190:193], v[96:99]
	v_mfma_i32_16x16x64_i8 v[88:91], v[150:153], v[198:201], v[88:91]
	v_mfma_i32_16x16x64_i8 v[80:83], v[166:169], v[198:201], v[80:83]
	v_mfma_i32_16x16x64_i8 v[136:139], v[154:157], v[178:181], v[136:139]
	v_mfma_i32_16x16x64_i8 v[128:131], v[170:173], v[178:181], v[128:131]
	v_mfma_i32_16x16x64_i8 v[120:123], v[154:157], v[186:189], v[120:123]
	v_mfma_i32_16x16x64_i8 v[112:115], v[170:173], v[186:189], v[112:115]
	v_mfma_i32_16x16x64_i8 v[104:107], v[154:157], v[194:197], v[104:107]
	v_mfma_i32_16x16x64_i8 v[96:99], v[170:173], v[194:197], v[96:99]
	v_mfma_i32_16x16x64_i8 v[88:91], v[154:157], v[202:205], v[88:91]
	v_mfma_i32_16x16x64_i8 v[80:83], v[170:173], v[202:205], v[80:83]
	s_setprio 0
	s_waitcnt vmcnt(8)
	s_barrier
	s_mov_b32 m0, s83
	ds_read_b128 v[174:177], v164 offset:16384
	ds_read_b128 v[178:181], v164 offset:17408
	ds_read_b128 v[182:185], v164 offset:18432
	ds_read_b128 v[186:189], v164 offset:19456
	ds_read_b128 v[190:193], v164 offset:20480
	ds_read_b128 v[194:197], v164 offset:21504
	ds_read_b128 v[198:201], v164 offset:22528
	ds_read_b128 v[202:205], v164 offset:23552
	v_mov_b32_e32 v47, v149
	global_load_lds_dwordx4 v244, s[80:81]
	v_mov_b32_e32 v159, v149
	s_mov_b32 m0, s89
	v_lshl_add_u64 v[206:207], s[80:81], 0, v[244:245]
	v_lshl_add_u64 v[208:209], s[80:81], 0, v[246:247]
	global_load_lds_dwordx4 v246, s[80:81]
	s_cselect_b32 s81, s71, s6
	s_cselect_b32 s80, s70, s5
	s_add_i32 s59, s3, s97
	s_mov_b32 m0, s59
	v_lshl_add_u64 v[210:211], s[80:81], 0, v[244:245]
	global_load_lds_dwordx4 v244, s[80:81]
	s_add_i32 m0, s59, 0x2000
	v_lshl_add_u64 v[212:213], s[80:81], 0, v[246:247]
	global_load_lds_dwordx4 v246, s[80:81]
	s_mov_b32 m0, s22
	v_lshl_add_u64 v[158:159], s[78:79], 0, v[240:241]
	global_load_lds_dwordx4 v240, s[78:79]
	s_mov_b32 m0, s23
	v_lshl_add_u64 v[214:215], s[78:79], 0, v[242:243]
	global_load_lds_dwordx4 v242, s[78:79]
	s_waitcnt lgkmcnt(0)
	s_barrier
	s_setprio 1
	s_waitcnt lgkmcnt(0)
	v_mfma_i32_16x16x64_i8 v[76:79], v[34:37], v[174:177], v[76:79]
	v_mfma_i32_16x16x64_i8 v[68:71], v[42:45], v[174:177], v[68:71]
	v_mfma_i32_16x16x64_i8 v[60:63], v[34:37], v[182:185], v[60:63]
	v_mfma_i32_16x16x64_i8 v[52:55], v[42:45], v[182:185], v[52:55]
	v_mfma_i32_16x16x64_i8 v[28:31], v[34:37], v[190:193], v[28:31]
	v_mfma_i32_16x16x64_i8 v[20:23], v[42:45], v[190:193], v[20:23]
	v_mfma_i32_16x16x64_i8 v[12:15], v[34:37], v[198:201], v[12:15]
	v_mfma_i32_16x16x64_i8 v[4:7], v[42:45], v[198:201], v[4:7]
	v_mfma_i32_16x16x64_i8 v[76:79], v[38:41], v[178:181], v[76:79]
	v_mfma_i32_16x16x64_i8 v[68:71], v[144:147], v[178:181], v[68:71]
	v_mfma_i32_16x16x64_i8 v[60:63], v[38:41], v[186:189], v[60:63]
	v_mfma_i32_16x16x64_i8 v[52:55], v[144:147], v[186:189], v[52:55]
	v_mfma_i32_16x16x64_i8 v[28:31], v[38:41], v[194:197], v[28:31]
	v_mfma_i32_16x16x64_i8 v[20:23], v[144:147], v[194:197], v[20:23]
	v_mfma_i32_16x16x64_i8 v[12:15], v[38:41], v[202:205], v[12:15]
	v_mfma_i32_16x16x64_i8 v[4:7], v[144:147], v[202:205], v[4:7]
	s_setprio 0
	s_setprio 1
	v_mfma_i32_16x16x64_i8 v[46:49], v[166:169], v[182:185], v[48:51]
	v_mfma_i32_16x16x64_i8 v[24:27], v[150:153], v[190:193], v[24:27]
	v_mfma_i32_16x16x64_i8 v[16:19], v[166:169], v[190:193], v[16:19]
	v_mfma_i32_16x16x64_i8 v[8:11], v[150:153], v[198:201], v[8:11]
	v_mfma_i32_16x16x64_i8 v[0:3], v[166:169], v[198:201], v[0:3]
	v_mfma_i32_16x16x64_i8 v[34:37], v[150:153], v[174:177], v[72:75]
	v_mfma_i32_16x16x64_i8 v[38:41], v[166:169], v[174:177], v[64:67]
	v_mfma_i32_16x16x64_i8 v[42:45], v[150:153], v[182:185], v[56:59]
	v_mfma_i32_16x16x64_i8 v[46:49], v[170:173], v[186:189], v[46:49]
	v_mfma_i32_16x16x64_i8 v[24:27], v[154:157], v[194:197], v[24:27]
	v_mfma_i32_16x16x64_i8 v[16:19], v[170:173], v[194:197], v[16:19]
	v_mfma_i32_16x16x64_i8 v[8:11], v[154:157], v[202:205], v[8:11]
	v_mfma_i32_16x16x64_i8 v[0:3], v[170:173], v[202:205], v[0:3]
	v_mfma_i32_16x16x64_i8 v[34:37], v[154:157], v[178:181], v[34:37]
	v_mfma_i32_16x16x64_i8 v[38:41], v[170:173], v[178:181], v[38:41]
	v_mfma_i32_16x16x64_i8 v[42:45], v[154:157], v[186:189], v[42:45]
	s_setprio 0
	s_waitcnt vmcnt(8)
	s_barrier
; #define G_STAGE(bufoff, gbase, voff) do { _Pragma("unroll") for (int _i = 0; _i < 2; ++_i) \
;         __builtin_amdgcn_global_load_lds((const unsigned*)((const char*)(gbase) + (voff)[_i]), (LAS unsigned*)(lds + (bufoff) + ldsw + _i * 8192), 16, 0, 0); } while (0)
; #define G_LDA(dst, b, h) do { _Pragma("unroll") for (int m = 0; m < 4; ++m) G_LD8(dst[m], lds + G_SA(b, h) + aoff + m * 2048); } while (0)
; #define G_LDB(dst, b, h) do { _Pragma("unroll") for (int n = 0; n < 2; ++n) G_LD8(dst[n], lds + G_SB(b, h) + boff + n * 2048); } while (0)
; #define G_WAIT_V(n) asm volatile("s_waitcnt vmcnt(" #n ")" ::: "memory")
; #define G_WAIT_L(n) asm volatile("s_waitcnt lgkmcnt(" #n ")" ::: "memory")
; #define G_BAR __builtin_amdgcn_s_barrier()
; #define G_SCHED __builtin_amdgcn_sched_barrier(0)
;     ...
;             G_LDB(B0, 1, 0); G_LDB(B1, 1, 1); G_SCHED; G_LDA(At, 1, 0); G_STAGE(G_SA(0, 1), a12, vA1);
;             G_WAIT_L(0); G_BAR; G_MMA(0, 0, At, B0); G_MMA(0, 1, At, B1); G_WAIT_V(8); G_BAR; G_SCHED;
;             G_LDA(At, 1, 1); G_STAGE(G_SB(1, 0), b02 + kstep, voffB); G_STAGE(G_SB(1, 1), b12 + kstep, voffB); G_STAGE(G_SA(1, 0), a02 + kstep, vA0);
;             G_WAIT_L(0); G_BAR; G_MMA(1, 0, At, B0); G_MMA(1, 1, At, B1); G_WAIT_V(8); G_BAR; G_SCHED;
;         }
	s_add_i32 s59, 0, 0x18000
	v_add_u32_e32 v33, s59, v163
	s_add_i32 s73, 0, 0x1c000
	ds_read_b128 v[56:59], v33
	ds_read_b128 v[64:67], v33 offset:1024
	ds_read_b128 v[72:75], v33 offset:2048
	ds_read_b128 v[144:147], v33 offset:3072
	v_add_u32_e32 v33, s73, v163
	ds_read_b128 v[150:153], v33
	ds_read_b128 v[154:157], v33 offset:1024
	ds_read_b128 v[166:169], v33 offset:2048
	ds_read_b128 v[170:173], v33 offset:3072
	s_mov_b32 m0, s55
	ds_read_b128 v[174:177], v164 offset:32768
	ds_read_b128 v[178:181], v164 offset:33792
	ds_read_b128 v[182:185], v164 offset:34816
	ds_read_b128 v[186:189], v164 offset:35840
	ds_read_b128 v[190:193], v164 offset:36864
	ds_read_b128 v[194:197], v164 offset:37888
	ds_read_b128 v[198:201], v164 offset:38912
	ds_read_b128 v[202:205], v164 offset:39936
	global_load_lds_dwordx4 v240, s[76:77]
	s_mov_b32 m0, s84
	s_nop 0
	global_load_lds_dwordx4 v242, s[76:77]
	s_waitcnt lgkmcnt(0)
	s_barrier
	s_setprio 1
	s_waitcnt lgkmcnt(0)
	v_mfma_i32_16x16x64_i8 v[140:143], v[56:59], v[174:177], v[140:143]
	v_mfma_i32_16x16x64_i8 v[132:135], v[72:75], v[174:177], v[132:135]
	v_mfma_i32_16x16x64_i8 v[124:127], v[56:59], v[182:185], v[124:127]
	v_mfma_i32_16x16x64_i8 v[116:119], v[72:75], v[182:185], v[116:119]
	v_mfma_i32_16x16x64_i8 v[108:111], v[56:59], v[190:193], v[108:111]
	v_mfma_i32_16x16x64_i8 v[100:103], v[72:75], v[190:193], v[100:103]
	v_mfma_i32_16x16x64_i8 v[92:95], v[56:59], v[198:201], v[92:95]
	v_mfma_i32_16x16x64_i8 v[84:87], v[72:75], v[198:201], v[84:87]
	v_mfma_i32_16x16x64_i8 v[140:143], v[64:67], v[178:181], v[140:143]
	v_mfma_i32_16x16x64_i8 v[132:135], v[144:147], v[178:181], v[132:135]
	v_mfma_i32_16x16x64_i8 v[124:127], v[64:67], v[186:189], v[124:127]
	v_mfma_i32_16x16x64_i8 v[116:119], v[144:147], v[186:189], v[116:119]
	v_mfma_i32_16x16x64_i8 v[108:111], v[64:67], v[194:197], v[108:111]
	v_mfma_i32_16x16x64_i8 v[100:103], v[144:147], v[194:197], v[100:103]
	v_mfma_i32_16x16x64_i8 v[92:95], v[64:67], v[202:205], v[92:95]
	v_mfma_i32_16x16x64_i8 v[84:87], v[144:147], v[202:205], v[84:87]
	s_setprio 0
	s_setprio 1
	v_mfma_i32_16x16x64_i8 v[136:139], v[150:153], v[174:177], v[136:139]
	v_mfma_i32_16x16x64_i8 v[128:131], v[166:169], v[174:177], v[128:131]
	v_mfma_i32_16x16x64_i8 v[120:123], v[150:153], v[182:185], v[120:123]
	v_mfma_i32_16x16x64_i8 v[112:115], v[166:169], v[182:185], v[112:115]
	v_mfma_i32_16x16x64_i8 v[104:107], v[150:153], v[190:193], v[104:107]
	v_mfma_i32_16x16x64_i8 v[96:99], v[166:169], v[190:193], v[96:99]
	v_mfma_i32_16x16x64_i8 v[88:91], v[150:153], v[198:201], v[88:91]
	v_mfma_i32_16x16x64_i8 v[80:83], v[166:169], v[198:201], v[80:83]
	v_mfma_i32_16x16x64_i8 v[136:139], v[154:157], v[178:181], v[136:139]
	v_mfma_i32_16x16x64_i8 v[128:131], v[170:173], v[178:181], v[128:131]
	v_mfma_i32_16x16x64_i8 v[120:123], v[154:157], v[186:189], v[120:123]
	v_mfma_i32_16x16x64_i8 v[112:115], v[170:173], v[186:189], v[112:115]
	v_mfma_i32_16x16x64_i8 v[104:107], v[154:157], v[194:197], v[104:107]
	v_mfma_i32_16x16x64_i8 v[96:99], v[170:173], v[194:197], v[96:99]
	v_mfma_i32_16x16x64_i8 v[88:91], v[154:157], v[202:205], v[88:91]
	v_mfma_i32_16x16x64_i8 v[80:83], v[170:173], v[202:205], v[80:83]
	s_setprio 0
	s_waitcnt vmcnt(8)
	s_barrier
	s_add_i32 s59, s59, s97
	v_lshl_add_u64 v[32:33], v[206:207], 0, s[46:47]
	s_mov_b32 m0, s59
	ds_read_b128 v[174:177], v164 offset:49152
	ds_read_b128 v[178:181], v164 offset:50176
	ds_read_b128 v[182:185], v164 offset:51200
	ds_read_b128 v[186:189], v164 offset:52224
	ds_read_b128 v[190:193], v164 offset:53248
	ds_read_b128 v[194:197], v164 offset:54272
	ds_read_b128 v[198:201], v164 offset:55296
	ds_read_b128 v[202:205], v164 offset:56320
	global_load_lds_dwordx4 v[32:33], off
	v_lshl_add_u64 v[32:33], v[208:209], 0, s[46:47]
	s_add_i32 m0, s59, 0x2000
	s_add_i32 s59, s73, s97
	global_load_lds_dwordx4 v[32:33], off
	v_lshl_add_u64 v[32:33], v[210:211], 0, s[46:47]
	s_mov_b32 m0, s59
	s_nop 0
	global_load_lds_dwordx4 v[32:33], off
	v_lshl_add_u64 v[32:33], v[212:213], 0, s[46:47]
	s_add_i32 m0, s59, 0x2000
	s_nop 0
	global_load_lds_dwordx4 v[32:33], off
	v_lshl_add_u64 v[32:33], v[158:159], 0, s[46:47]
	s_mov_b32 m0, s86
	s_nop 0
	global_load_lds_dwordx4 v[32:33], off
	v_lshl_add_u64 v[32:33], v[214:215], 0, s[46:47]
	s_mov_b32 m0, s87
	s_nop 0
	global_load_lds_dwordx4 v[32:33], off
	s_waitcnt lgkmcnt(0)
	s_barrier
	s_setprio 1
	s_waitcnt lgkmcnt(0)
	v_mfma_i32_16x16x64_i8 v[76:79], v[56:59], v[174:177], v[76:79]
	v_mfma_i32_16x16x64_i8 v[68:71], v[72:75], v[174:177], v[68:71]
	v_mfma_i32_16x16x64_i8 v[60:63], v[56:59], v[182:185], v[60:63]
	v_mfma_i32_16x16x64_i8 v[50:53], v[72:75], v[182:185], v[52:55]
	v_mfma_i32_16x16x64_i8 v[28:31], v[56:59], v[190:193], v[28:31]
	v_mfma_i32_16x16x64_i8 v[20:23], v[72:75], v[190:193], v[20:23]
	v_mfma_i32_16x16x64_i8 v[12:15], v[56:59], v[198:201], v[12:15]
	v_mfma_i32_16x16x64_i8 v[4:7], v[72:75], v[198:201], v[4:7]
	v_mfma_i32_16x16x64_i8 v[76:79], v[64:67], v[178:181], v[76:79]
	v_mfma_i32_16x16x64_i8 v[68:71], v[144:147], v[178:181], v[68:71]
	v_mfma_i32_16x16x64_i8 v[60:63], v[64:67], v[186:189], v[60:63]
	v_mfma_i32_16x16x64_i8 v[52:55], v[144:147], v[186:189], v[50:53]
	v_mfma_i32_16x16x64_i8 v[28:31], v[64:67], v[194:197], v[28:31]
	v_mfma_i32_16x16x64_i8 v[20:23], v[144:147], v[194:197], v[20:23]
	v_mfma_i32_16x16x64_i8 v[12:15], v[64:67], v[202:205], v[12:15]
	v_mfma_i32_16x16x64_i8 v[4:7], v[144:147], v[202:205], v[4:7]
	s_setprio 0
	s_setprio 1
	v_mfma_i32_16x16x64_i8 v[32:35], v[150:153], v[174:177], v[34:37]
	v_mfma_i32_16x16x64_i8 v[72:75], v[154:157], v[178:181], v[32:35]
	v_mfma_i32_16x16x64_i8 v[32:35], v[166:169], v[174:177], v[38:41]
	v_mfma_i32_16x16x64_i8 v[64:67], v[170:173], v[178:181], v[32:35]
	v_mfma_i32_16x16x64_i8 v[32:35], v[150:153], v[182:185], v[42:45]
	v_mfma_i32_16x16x64_i8 v[56:59], v[154:157], v[186:189], v[32:35]
	v_mfma_i32_16x16x64_i8 v[32:35], v[166:169], v[182:185], v[46:49]
	v_mfma_i32_16x16x64_i8 v[24:27], v[150:153], v[190:193], v[24:27]
	v_mfma_i32_16x16x64_i8 v[16:19], v[166:169], v[190:193], v[16:19]
	v_mfma_i32_16x16x64_i8 v[8:11], v[150:153], v[198:201], v[8:11]
	v_mfma_i32_16x16x64_i8 v[0:3], v[166:169], v[198:201], v[0:3]
	v_mfma_i32_16x16x64_i8 v[48:51], v[170:173], v[186:189], v[32:35]
	v_mfma_i32_16x16x64_i8 v[24:27], v[154:157], v[194:197], v[24:27]
	v_mfma_i32_16x16x64_i8 v[16:19], v[170:173], v[194:197], v[16:19]
	v_mfma_i32_16x16x64_i8 v[8:11], v[154:157], v[202:205], v[8:11]
	v_mfma_i32_16x16x64_i8 v[0:3], v[170:173], v[202:205], v[0:3]
	s_setprio 0
	s_waitcnt vmcnt(8)
	s_barrier
	s_add_u32 s0, s0, 0x100
	s_addc_u32 s2, s2, 0
	s_add_u32 s5, s5, 0x100
	s_addc_u32 s6, s6, 0
	s_add_u32 s19, s19, 0x100
	s_addc_u32 s33, s33, 0
	s_add_u32 s74, s74, 0x100
	s_addc_u32 s75, s75, 0
	s_cmp_ge_i32 s63, s25
	s_mov_b32 s59, s63
	s_cbranch_scc0 .LBB0_179
	s_and_b64 vcc, exec, s[50:51]
	s_cbranch_vccz .LBB0_182

; __device__ __forceinline__ int lane_id() { int l; asm volatile("v_mbcnt_lo_u32_b32 %0, -1, 0\n\tv_mbcnt_hi_u32_b32 %0, -1, %0" : "=v"(l)); return l; }
; #define G_STAGE(bufoff, gbase, voff) do { _Pragma("unroll") for (int _i = 0; _i < 2; ++_i) \
;         __builtin_amdgcn_global_load_lds((const unsigned*)((const char*)(gbase) + (voff)[_i]), (LAS unsigned*)(lds + (bufoff) + ldsw + _i * 8192), 16, 0, 0); } while (0)
; #define G_LDA(dst, b, h) do { _Pragma("unroll") for (int m = 0; m < 4; ++m) G_LD8(dst[m], lds + G_SA(b, h) + aoff + m * 2048); } while (0)
; #define G_LDB(dst, b, h) do { _Pragma("unroll") for (int n = 0; n < 2; ++n) G_LD8(dst[n], lds + G_SB(b, h) + boff + n * 2048); } while (0)
; #define G_SCHED __builtin_amdgcn_sched_barrier(0)
;     ...
;         for (int t = 0; t < nt; t += 2) {
;             const bool last = (t == nt - 2);
;             { const int tz_ = wid * 64 + lane_id();
; #pragma unroll
;               for (int i = 0; i < 2; ++i) { int R, C; stage_rc(tz_ * 16 + i * 8192, R, C); const int Rb = Epi::PERM ? ((R & ~31) + perm32(R & 31)) : R;
;                   voffA[i] = (unsigned)(R * S.multA * S.pitchA + C) * 2u; voffB[i] = (unsigned)(Rb * S.multB * S.pitchB + C) * 2u; } }
;             if constexpr (GATHER) asm volatile("" : "+v"(gc0[0]), "+v"(gc0[1]), "+v"(gc1[0]), "+v"(gc1[1]));
;             if constexpr (PREF) { if (t == nt - 4) S.prefetch(nxt, lds); }
;             const char* a11 = cur.a1 + (size_t)(t + 1) * kstep;
;             const char* a02 = last ? nxt.a0 : cur.a0 + (size_t)(t + 2) * kstep; const char* a12 = last ? nxt.a1 : cur.a1 + (size_t)(t + 2) * kstep;
;             const char* b02 = last ? nxt.b0 : cur.b0 + (size_t)(t + 2) * kstep; const char* b12 = last ? nxt.b1 : cur.b1 + (size_t)(t + 2) * kstep;
;             G_LDB(B0, 0, 0); G_LDB(B1, 0, 1); G_SCHED; G_LDA(At, 0, 0); G_STAGE(G_SA(1, 1), a11, vA1);
;     ...
;         for (int a = 0; a < 2; ++a)
; #pragma unroll
;             for (int b = 0; b < 2; ++b)
; #pragma unroll
;                 for (int m = 0; m < 4; ++m)
; #pragma unroll
;                     for (int n = 0; n < 2; ++n) acc[a][b][m][n] = (acc_t){0, 0, 0, 0};
;         cur = nxt; ++ui;
.LBB0_248:
	s_add_u32 s43, s60, 0x100
	s_addc_u32 s55, s61, 0
	s_add_u32 s64, s62, 0x100
	s_addc_u32 s65, s63, 0
	s_add_u32 s66, s58, 0x100
	s_addc_u32 s67, s59, 0
	s_add_u32 s56, s56, 0x80
	s_addc_u32 s57, s57, 0
	s_mov_b32 s58, 0
	v_mov_b32_e32 v0, 0
	v_mov_b32_e32 v1, 0
	v_mov_b32_e32 v2, 0
	v_mov_b32_e32 v3, 0
	v_mov_b32_e32 v4, 0
	v_mov_b32_e32 v5, 0
	v_mov_b32_e32 v6, 0
	v_mov_b32_e32 v7, 0
	s_waitcnt vmcnt(0)
	v_mov_b32_e32 v16, 0
	v_mov_b32_e32 v17, 0
	v_mov_b32_e32 v18, 0
	v_mov_b32_e32 v19, 0
	v_mov_b32_e32 v20, 0
	v_mov_b32_e32 v21, 0
	v_mov_b32_e32 v22, 0
	v_mov_b32_e32 v23, 0
	v_mov_b32_e32 v32, 0
	v_mov_b32_e32 v33, 0
	v_mov_b32_e32 v34, 0
	v_mov_b32_e32 v35, 0
	v_mov_b32_e32 v36, 0
	v_mov_b32_e32 v37, 0
	v_mov_b32_e32 v38, 0
	v_mov_b32_e32 v39, 0
	v_mov_b32_e32 v48, 0
	v_mov_b32_e32 v49, 0
	v_mov_b32_e32 v50, 0
	v_mov_b32_e32 v51, 0
	v_mov_b32_e32 v52, 0
	v_mov_b32_e32 v53, 0
	v_mov_b32_e32 v54, 0
	v_mov_b32_e32 v55, 0
	v_mov_b32_e32 v8, 0
	v_mov_b32_e32 v9, 0
	v_mov_b32_e32 v10, 0
	v_mov_b32_e32 v11, 0
	v_mov_b32_e32 v12, 0
	v_mov_b32_e32 v13, 0
	v_mov_b32_e32 v14, 0
	v_mov_b32_e32 v15, 0
	v_mov_b32_e32 v24, 0
	v_mov_b32_e32 v25, 0
	v_mov_b32_e32 v26, 0
	v_mov_b32_e32 v27, 0
	v_mov_b32_e32 v28, 0
	v_mov_b32_e32 v29, 0
	v_mov_b32_e32 v30, 0
	v_mov_b32_e32 v31, 0
	v_mov_b32_e32 v40, 0
	v_mov_b32_e32 v41, 0
	v_mov_b32_e32 v42, 0
	v_mov_b32_e32 v43, 0
	v_mov_b32_e32 v44, 0
	v_mov_b32_e32 v45, 0
	v_mov_b32_e32 v46, 0
	v_mov_b32_e32 v47, 0
	v_mov_b32_e32 v56, 0
	v_mov_b32_e32 v57, 0
	v_mov_b32_e32 v58, 0
	v_mov_b32_e32 v59, 0
	v_mov_b32_e32 v60, 0
	v_mov_b32_e32 v61, 0
	v_mov_b32_e32 v62, 0
	v_mov_b32_e32 v63, 0
	v_mov_b32_e32 v64, 0
	v_mov_b32_e32 v65, 0
	v_mov_b32_e32 v66, 0
	v_mov_b32_e32 v67, 0
	v_mov_b32_e32 v68, 0
	v_mov_b32_e32 v69, 0
	v_mov_b32_e32 v70, 0
	v_mov_b32_e32 v71, 0
	v_mov_b32_e32 v80, 0
	v_mov_b32_e32 v81, 0
	v_mov_b32_e32 v82, 0
	v_mov_b32_e32 v83, 0
	v_mov_b32_e32 v84, 0
	v_mov_b32_e32 v85, 0
	v_mov_b32_e32 v86, 0
	v_mov_b32_e32 v87, 0
	v_mov_b32_e32 v96, 0
	v_mov_b32_e32 v97, 0
	v_mov_b32_e32 v98, 0
	v_mov_b32_e32 v99, 0
	v_mov_b32_e32 v100, 0
	v_mov_b32_e32 v101, 0
	v_mov_b32_e32 v102, 0
	v_mov_b32_e32 v103, 0
	v_mov_b32_e32 v112, 0
	v_mov_b32_e32 v113, 0
	v_mov_b32_e32 v114, 0
	v_mov_b32_e32 v115, 0
	v_mov_b32_e32 v116, 0
	v_mov_b32_e32 v117, 0
	v_mov_b32_e32 v118, 0
	v_mov_b32_e32 v119, 0
	v_mov_b32_e32 v72, 0
	v_mov_b32_e32 v73, 0
	v_mov_b32_e32 v74, 0
	v_mov_b32_e32 v75, 0
	v_mov_b32_e32 v76, 0
	v_mov_b32_e32 v77, 0
	v_mov_b32_e32 v78, 0
	v_mov_b32_e32 v79, 0
	v_mov_b32_e32 v88, 0
	v_mov_b32_e32 v89, 0
	v_mov_b32_e32 v90, 0
	v_mov_b32_e32 v91, 0
	v_mov_b32_e32 v92, 0
	v_mov_b32_e32 v93, 0
	v_mov_b32_e32 v94, 0
	v_mov_b32_e32 v95, 0
	v_mov_b32_e32 v104, 0
	v_mov_b32_e32 v105, 0
	v_mov_b32_e32 v106, 0
	v_mov_b32_e32 v107, 0
	v_mov_b32_e32 v108, 0
	v_mov_b32_e32 v109, 0
	v_mov_b32_e32 v110, 0
	v_mov_b32_e32 v111, 0
	v_mov_b32_e32 v120, 0
	v_mov_b32_e32 v121, 0
	v_mov_b32_e32 v122, 0
	v_mov_b32_e32 v123, 0
	v_mov_b32_e32 v124, 0
	v_mov_b32_e32 v125, 0
	v_mov_b32_e32 v126, 0
	v_mov_b32_e32 v127, 0
	v_mbcnt_lo_u32_b32 v248, -1, 0
	v_mbcnt_hi_u32_b32 v248, -1, v248
	v_mov_b32_e32 v249, s88
	v_lshrrev_b32_e32 v249, 6, v249
	v_and_b32_e32 v250, 3, v248
	v_lshlrev_b32_e32 v250, 4, v250
	v_and_b32_e32 v251, 32, v248
	v_xor_b32_e32 v250, v250, v251
	v_and_b32_e32 v251, 1, v249
	v_lshl_add_u32 v250, v251, 6, v250
	v_lshrrev_b32_e32 v251, 1, v249
	v_lshrrev_b32_e32 v252, 2, v248
	v_lshl_add_u32 v251, v251, 4, v252
	v_mov_b32_e32 v253, 0x800
	v_mad_u32_u24 v240, v251, v253, v250
	v_add_u32_e32 v242, 0x20000, v240
	v_lshrrev_b32_e32 v251, 2, v249
	v_lshlrev_b32_e32 v251, 5, v251
	v_lshrrev_b32_e32 v252, 4, v248
	v_lshl_add_u32 v251, v252, 3, v251
	v_bfe_u32 v252, v249, 1, 1
	v_lshl_add_u32 v251, v252, 2, v251
	v_bfe_u32 v252, v248, 2, 2
	v_add_u32_e32 v251, v251, v252
	v_mov_b32_e32 v253, 0x40000
	v_mad_u32_u24 v244, v251, v253, v250
	v_add_u32_e32 v246, 0x1000000, v244
	v_mov_b32_e32 v241, 0
	v_mov_b32_e32 v243, 0
	v_mov_b32_e32 v245, 0
	v_mov_b32_e32 v247, 0
.LBB0_249:
	v_add_u32_e32 v144, s23, v151
	v_add_u32_e32 v166, s24, v151
	ds_read_b128 v[132:135], v144
	ds_read_b128 v[136:139], v144 offset:1024
	ds_read_b128 v[140:143], v144 offset:2048
	ds_read_b128 v[144:147], v144 offset:3072
	ds_read_b128 v[154:157], v166
	ds_read_b128 v[158:161], v166 offset:1024
	ds_read_b128 v[162:165], v166 offset:2048
	ds_read_b128 v[166:169], v166 offset:3072
	s_add_i32 s68, s58, 2
	s_add_u32 s69, s56, 0x80
	s_addc_u32 s59, s57, 0
	s_add_i32 s71, s23, s97
	s_add_i32 m0, s2, 0xc000
	s_add_i32 s70, s2, 0xe000
	s_add_i32 s72, s71, 0x2000
	s_cmp_eq_u32 s22, s58
	s_cselect_b32 s58, s46, s69
	s_cselect_b32 s61, s45, s67
	s_cselect_b32 s60, s44, s66
	s_cselect_b32 s63, s49, s55
	s_cselect_b32 s62, s48, s43
	s_cselect_b32 s59, s47, s59
	ds_read_b128 v[170:173], v152
	ds_read_b128 v[174:177], v152 offset:1024
	ds_read_b128 v[178:181], v152 offset:2048
	ds_read_b128 v[182:185], v152 offset:3072
	ds_read_b128 v[186:189], v152 offset:4096
	ds_read_b128 v[190:193], v152 offset:5120
	ds_read_b128 v[194:197], v152 offset:6144
	ds_read_b128 v[198:201], v152 offset:7168
	global_load_lds_dwordx4 v240, s[56:57]
	s_mov_b32 m0, s70
	s_nop 0
	global_load_lds_dwordx4 v242, s[56:57]
	s_waitcnt lgkmcnt(0)
	v_mov_b32_e32 v131, v129
	s_barrier
; #define G_STAGE(bufoff, gbase, voff) do { _Pragma("unroll") for (int _i = 0; _i < 2; ++_i) \
;         __builtin_amdgcn_global_load_lds((const unsigned*)((const char*)(gbase) + (voff)[_i]), (LAS unsigned*)(lds + (bufoff) + ldsw + _i * 8192), 16, 0, 0); } while (0)
; #define G_LDA(dst, b, h) do { _Pragma("unroll") for (int m = 0; m < 4; ++m) G_LD8(dst[m], lds + G_SA(b, h) + aoff + m * 2048); } while (0)
; #define G_WAIT_V(n) asm volatile("s_waitcnt vmcnt(" #n ")" ::: "memory")
; #define G_WAIT_L(n) asm volatile("s_waitcnt lgkmcnt(" #n ")" ::: "memory")
; #define G_BAR __builtin_amdgcn_s_barrier()
; #define G_SCHED __builtin_amdgcn_sched_barrier(0)
;     ...
;             G_WAIT_L(0); G_BAR; G_MMA(0, 0, At, B0); G_MMA(0, 1, At, B1); G_WAIT_V(8); G_BAR; G_SCHED;
;             G_LDA(At, 0, 1); G_STAGE(G_SB(0, 0), b02, voffB); G_STAGE(G_SB(0, 1), b12, voffB); G_STAGE(G_SA(0, 0), a02, vA0);
;             G_WAIT_L(0); G_BAR; G_MMA(1, 0, At, B0); G_MMA(1, 1, At, B1); G_WAIT_V(8); G_BAR; G_SCHED;
	s_setprio 1
	s_waitcnt lgkmcnt(0)
	v_mfma_i32_16x16x64_i8 v[124:127], v[132:135], v[170:173], v[124:127]
	v_mfma_i32_16x16x64_i8 v[120:123], v[140:143], v[170:173], v[120:123]
	v_mfma_i32_16x16x64_i8 v[108:111], v[132:135], v[178:181], v[108:111]
	v_mfma_i32_16x16x64_i8 v[104:107], v[140:143], v[178:181], v[104:107]
	v_mfma_i32_16x16x64_i8 v[92:95], v[132:135], v[186:189], v[92:95]
	v_mfma_i32_16x16x64_i8 v[88:91], v[140:143], v[186:189], v[88:91]
	v_mfma_i32_16x16x64_i8 v[76:79], v[132:135], v[194:197], v[76:79]
	v_mfma_i32_16x16x64_i8 v[72:75], v[140:143], v[194:197], v[72:75]
	v_mfma_i32_16x16x64_i8 v[124:127], v[136:139], v[174:177], v[124:127]
	v_mfma_i32_16x16x64_i8 v[120:123], v[144:147], v[174:177], v[120:123]
	v_mfma_i32_16x16x64_i8 v[108:111], v[136:139], v[182:185], v[108:111]
	v_mfma_i32_16x16x64_i8 v[104:107], v[144:147], v[182:185], v[104:107]
	v_mfma_i32_16x16x64_i8 v[92:95], v[136:139], v[190:193], v[92:95]
	v_mfma_i32_16x16x64_i8 v[88:91], v[144:147], v[190:193], v[88:91]
	v_mfma_i32_16x16x64_i8 v[76:79], v[136:139], v[198:201], v[76:79]
	v_mfma_i32_16x16x64_i8 v[72:75], v[144:147], v[198:201], v[72:75]
	s_setprio 0
	s_setprio 1
	v_mfma_i32_16x16x64_i8 v[116:119], v[154:157], v[170:173], v[116:119]
	v_mfma_i32_16x16x64_i8 v[112:115], v[162:165], v[170:173], v[112:115]
	v_mfma_i32_16x16x64_i8 v[100:103], v[154:157], v[178:181], v[100:103]
	v_mfma_i32_16x16x64_i8 v[96:99], v[162:165], v[178:181], v[96:99]
	v_mfma_i32_16x16x64_i8 v[84:87], v[154:157], v[186:189], v[84:87]
	v_mfma_i32_16x16x64_i8 v[80:83], v[162:165], v[186:189], v[80:83]
	v_mfma_i32_16x16x64_i8 v[68:71], v[154:157], v[194:197], v[68:71]
	v_mfma_i32_16x16x64_i8 v[64:67], v[162:165], v[194:197], v[64:67]
	v_mfma_i32_16x16x64_i8 v[116:119], v[158:161], v[174:177], v[116:119]
	v_mfma_i32_16x16x64_i8 v[112:115], v[166:169], v[174:177], v[112:115]
	v_mfma_i32_16x16x64_i8 v[100:103], v[158:161], v[182:185], v[100:103]
	v_mfma_i32_16x16x64_i8 v[96:99], v[166:169], v[182:185], v[96:99]
	v_mfma_i32_16x16x64_i8 v[84:87], v[158:161], v[190:193], v[84:87]
	v_mfma_i32_16x16x64_i8 v[80:83], v[166:169], v[190:193], v[80:83]
	v_mfma_i32_16x16x64_i8 v[68:71], v[158:161], v[198:201], v[68:71]
	v_mfma_i32_16x16x64_i8 v[64:67], v[166:169], v[198:201], v[64:67]
	s_setprio 0
	s_waitcnt vmcnt(8)
	s_barrier
	s_mov_b32 m0, s71
	ds_read_b128 v[170:173], v152 offset:16384
	ds_read_b128 v[174:177], v152 offset:17408
	ds_read_b128 v[178:181], v152 offset:18432
	ds_read_b128 v[182:185], v152 offset:19456
	ds_read_b128 v[186:189], v152 offset:20480
	ds_read_b128 v[190:193], v152 offset:21504
	ds_read_b128 v[194:197], v152 offset:22528
	ds_read_b128 v[198:201], v152 offset:23552
	v_mov_b32_e32 v203, v129
	global_load_lds_dwordx4 v244, s[62:63]
	v_mov_b32_e32 v205, v129
	s_mov_b32 m0, s72
	v_lshl_add_u64 v[206:207], s[62:63], 0, v[244:245]
	v_lshl_add_u64 v[208:209], s[62:63], 0, v[246:247]
	global_load_lds_dwordx4 v246, s[62:63]
	s_cselect_b32 s63, s51, s65
	s_cselect_b32 s62, s50, s64
	s_add_i32 s69, s24, s97
	s_mov_b32 m0, s69
	v_lshl_add_u64 v[210:211], s[62:63], 0, v[244:245]
	global_load_lds_dwordx4 v244, s[62:63]
	s_add_i32 m0, s69, 0x2000
	v_lshl_add_u64 v[202:203], s[62:63], 0, v[246:247]
	global_load_lds_dwordx4 v246, s[62:63]
	s_mov_b32 m0, s2
	v_lshl_add_u64 v[204:205], s[60:61], 0, v[240:241]
	global_load_lds_dwordx4 v240, s[60:61]
	s_mov_b32 m0, s10
	v_lshl_add_u64 v[212:213], s[60:61], 0, v[242:243]
	global_load_lds_dwordx4 v242, s[60:61]
	s_waitcnt lgkmcnt(0)
	s_barrier
	s_setprio 1
	s_waitcnt lgkmcnt(0)
	v_mfma_i32_16x16x64_i8 v[60:63], v[132:135], v[170:173], v[60:63]
	v_mfma_i32_16x16x64_i8 v[56:59], v[140:143], v[170:173], v[56:59]
	v_mfma_i32_16x16x64_i8 v[44:47], v[132:135], v[178:181], v[44:47]
	v_mfma_i32_16x16x64_i8 v[40:43], v[140:143], v[178:181], v[40:43]
	v_mfma_i32_16x16x64_i8 v[28:31], v[132:135], v[186:189], v[28:31]
	v_mfma_i32_16x16x64_i8 v[24:27], v[140:143], v[186:189], v[24:27]
	v_mfma_i32_16x16x64_i8 v[12:15], v[132:135], v[194:197], v[12:15]
	v_mfma_i32_16x16x64_i8 v[8:11], v[140:143], v[194:197], v[8:11]
	v_mfma_i32_16x16x64_i8 v[60:63], v[136:139], v[174:177], v[60:63]
	v_mfma_i32_16x16x64_i8 v[56:59], v[144:147], v[174:177], v[56:59]
	v_mfma_i32_16x16x64_i8 v[44:47], v[136:139], v[182:185], v[44:47]
	v_mfma_i32_16x16x64_i8 v[40:43], v[144:147], v[182:185], v[40:43]
	v_mfma_i32_16x16x64_i8 v[28:31], v[136:139], v[190:193], v[28:31]
	v_mfma_i32_16x16x64_i8 v[24:27], v[144:147], v[190:193], v[24:27]
	v_mfma_i32_16x16x64_i8 v[12:15], v[136:139], v[198:201], v[12:15]
	v_mfma_i32_16x16x64_i8 v[8:11], v[144:147], v[198:201], v[8:11]
	s_setprio 0
	s_setprio 1
	v_mfma_i32_16x16x64_i8 v[52:55], v[154:157], v[170:173], v[52:55]
	v_mfma_i32_16x16x64_i8 v[48:51], v[162:165], v[170:173], v[48:51]
	v_mfma_i32_16x16x64_i8 v[36:39], v[154:157], v[178:181], v[36:39]
	v_mfma_i32_16x16x64_i8 v[32:35], v[162:165], v[178:181], v[32:35]
	v_mfma_i32_16x16x64_i8 v[20:23], v[154:157], v[186:189], v[20:23]
	v_mfma_i32_16x16x64_i8 v[16:19], v[162:165], v[186:189], v[16:19]
	v_mfma_i32_16x16x64_i8 v[4:7], v[154:157], v[194:197], v[4:7]
	v_mfma_i32_16x16x64_i8 v[0:3], v[162:165], v[194:197], v[0:3]
	v_mfma_i32_16x16x64_i8 v[52:55], v[158:161], v[174:177], v[52:55]
	v_mfma_i32_16x16x64_i8 v[48:51], v[166:169], v[174:177], v[48:51]
	v_mfma_i32_16x16x64_i8 v[36:39], v[158:161], v[182:185], v[36:39]
	v_mfma_i32_16x16x64_i8 v[32:35], v[166:169], v[182:185], v[32:35]
	v_mfma_i32_16x16x64_i8 v[20:23], v[158:161], v[190:193], v[20:23]
	v_mfma_i32_16x16x64_i8 v[16:19], v[166:169], v[190:193], v[16:19]
	v_mfma_i32_16x16x64_i8 v[4:7], v[158:161], v[198:201], v[4:7]
	v_mfma_i32_16x16x64_i8 v[0:3], v[166:169], v[198:201], v[0:3]
	s_setprio 0
	s_waitcnt vmcnt(8)
	s_barrier
; #define G_STAGE(bufoff, gbase, voff) do { _Pragma("unroll") for (int _i = 0; _i < 2; ++_i) \
;         __builtin_amdgcn_global_load_lds((const unsigned*)((const char*)(gbase) + (voff)[_i]), (LAS unsigned*)(lds + (bufoff) + ldsw + _i * 8192), 16, 0, 0); } while (0)
; #define G_LDA(dst, b, h) do { _Pragma("unroll") for (int m = 0; m < 4; ++m) G_LD8(dst[m], lds + G_SA(b, h) + aoff + m * 2048); } while (0)
; #define G_LDB(dst, b, h) do { _Pragma("unroll") for (int n = 0; n < 2; ++n) G_LD8(dst[n], lds + G_SB(b, h) + boff + n * 2048); } while (0)
; #define G_WAIT_V(n) asm volatile("s_waitcnt vmcnt(" #n ")" ::: "memory")
; #define G_WAIT_L(n) asm volatile("s_waitcnt lgkmcnt(" #n ")" ::: "memory")
; #define G_BAR __builtin_amdgcn_s_barrier()
; #define G_SCHED __builtin_amdgcn_sched_barrier(0)
;     ...
;             G_LDB(B0, 1, 0); G_LDB(B1, 1, 1); G_SCHED; G_LDA(At, 1, 0); G_STAGE(G_SA(0, 1), a12, vA1);
;             G_WAIT_L(0); G_BAR; G_MMA(0, 0, At, B0); G_MMA(0, 1, At, B1); G_WAIT_V(8); G_BAR; G_SCHED;
;             G_LDA(At, 1, 1); G_STAGE(G_SB(1, 0), b02 + kstep, voffB); G_STAGE(G_SB(1, 1), b12 + kstep, voffB); G_STAGE(G_SA(1, 0), a02 + kstep, vA0);
;             G_WAIT_L(0); G_BAR; G_MMA(1, 0, At, B0); G_MMA(1, 1, At, B1); G_WAIT_V(8); G_BAR; G_SCHED;
;         }
	s_add_i32 s60, 0, 0x18000
	v_add_u32_e32 v131, s60, v151
	s_add_i32 s61, 0, 0x1c000
	ds_read_b128 v[132:135], v131
	ds_read_b128 v[136:139], v131 offset:1024
	ds_read_b128 v[140:143], v131 offset:2048
	ds_read_b128 v[144:147], v131 offset:3072
	v_add_u32_e32 v131, s61, v151
	ds_read_b128 v[154:157], v131
	ds_read_b128 v[158:161], v131 offset:1024
	ds_read_b128 v[162:165], v131 offset:2048
	ds_read_b128 v[166:169], v131 offset:3072
	s_mov_b32 m0, s11
	ds_read_b128 v[170:173], v152 offset:32768
	ds_read_b128 v[174:177], v152 offset:33792
	ds_read_b128 v[178:181], v152 offset:34816
	ds_read_b128 v[182:185], v152 offset:35840
	ds_read_b128 v[186:189], v152 offset:36864
	ds_read_b128 v[190:193], v152 offset:37888
	ds_read_b128 v[194:197], v152 offset:38912
	ds_read_b128 v[198:201], v152 offset:39936
	global_load_lds_dwordx4 v240, s[58:59]
	s_mov_b32 m0, s18
	s_nop 0
	global_load_lds_dwordx4 v242, s[58:59]
	s_waitcnt lgkmcnt(0)
	s_barrier
	s_setprio 1
	s_waitcnt lgkmcnt(0)
	v_mfma_i32_16x16x64_i8 v[124:127], v[132:135], v[170:173], v[124:127]
	v_mfma_i32_16x16x64_i8 v[120:123], v[140:143], v[170:173], v[120:123]
	v_mfma_i32_16x16x64_i8 v[108:111], v[132:135], v[178:181], v[108:111]
	v_mfma_i32_16x16x64_i8 v[104:107], v[140:143], v[178:181], v[104:107]
	v_mfma_i32_16x16x64_i8 v[92:95], v[132:135], v[186:189], v[92:95]
	v_mfma_i32_16x16x64_i8 v[88:91], v[140:143], v[186:189], v[88:91]
	v_mfma_i32_16x16x64_i8 v[76:79], v[132:135], v[194:197], v[76:79]
	v_mfma_i32_16x16x64_i8 v[72:75], v[140:143], v[194:197], v[72:75]
	v_mfma_i32_16x16x64_i8 v[124:127], v[136:139], v[174:177], v[124:127]
	v_mfma_i32_16x16x64_i8 v[120:123], v[144:147], v[174:177], v[120:123]
	v_mfma_i32_16x16x64_i8 v[108:111], v[136:139], v[182:185], v[108:111]
	v_mfma_i32_16x16x64_i8 v[104:107], v[144:147], v[182:185], v[104:107]
	v_mfma_i32_16x16x64_i8 v[92:95], v[136:139], v[190:193], v[92:95]
	v_mfma_i32_16x16x64_i8 v[88:91], v[144:147], v[190:193], v[88:91]
	v_mfma_i32_16x16x64_i8 v[76:79], v[136:139], v[198:201], v[76:79]
	v_mfma_i32_16x16x64_i8 v[72:75], v[144:147], v[198:201], v[72:75]
	s_setprio 0
	s_setprio 1
	v_mfma_i32_16x16x64_i8 v[116:119], v[154:157], v[170:173], v[116:119]
	v_mfma_i32_16x16x64_i8 v[112:115], v[162:165], v[170:173], v[112:115]
	v_mfma_i32_16x16x64_i8 v[100:103], v[154:157], v[178:181], v[100:103]
	v_mfma_i32_16x16x64_i8 v[96:99], v[162:165], v[178:181], v[96:99]
	v_mfma_i32_16x16x64_i8 v[84:87], v[154:157], v[186:189], v[84:87]
	v_mfma_i32_16x16x64_i8 v[80:83], v[162:165], v[186:189], v[80:83]
	v_mfma_i32_16x16x64_i8 v[68:71], v[154:157], v[194:197], v[68:71]
	v_mfma_i32_16x16x64_i8 v[64:67], v[162:165], v[194:197], v[64:67]
	v_mfma_i32_16x16x64_i8 v[116:119], v[158:161], v[174:177], v[116:119]
	v_mfma_i32_16x16x64_i8 v[112:115], v[166:169], v[174:177], v[112:115]
	v_mfma_i32_16x16x64_i8 v[100:103], v[158:161], v[182:185], v[100:103]
	v_mfma_i32_16x16x64_i8 v[96:99], v[166:169], v[182:185], v[96:99]
	v_mfma_i32_16x16x64_i8 v[84:87], v[158:161], v[190:193], v[84:87]
	v_mfma_i32_16x16x64_i8 v[80:83], v[166:169], v[190:193], v[80:83]
	v_mfma_i32_16x16x64_i8 v[68:71], v[158:161], v[198:201], v[68:71]
	v_mfma_i32_16x16x64_i8 v[64:67], v[166:169], v[198:201], v[64:67]
	s_setprio 0
	s_waitcnt vmcnt(8)
	s_barrier
	s_add_i32 s58, s60, s97
	v_lshl_add_u64 v[130:131], v[206:207], 0, s[8:9]
	s_mov_b32 m0, s58
	ds_read_b128 v[170:173], v152 offset:49152
	ds_read_b128 v[174:177], v152 offset:50176
	ds_read_b128 v[178:181], v152 offset:51200
	ds_read_b128 v[182:185], v152 offset:52224
	ds_read_b128 v[186:189], v152 offset:53248
	ds_read_b128 v[190:193], v152 offset:54272
	ds_read_b128 v[194:197], v152 offset:55296
	ds_read_b128 v[198:201], v152 offset:56320
	global_load_lds_dwordx4 v[130:131], off
	v_lshl_add_u64 v[130:131], v[208:209], 0, s[8:9]
	s_add_i32 m0, s58, 0x2000
	s_add_i32 s58, s61, s97
	global_load_lds_dwordx4 v[130:131], off
	v_lshl_add_u64 v[130:131], v[210:211], 0, s[8:9]
	s_mov_b32 m0, s58
	s_nop 0
	global_load_lds_dwordx4 v[130:131], off
	v_lshl_add_u64 v[130:131], v[202:203], 0, s[8:9]
	s_add_i32 m0, s58, 0x2000
	s_nop 0
	global_load_lds_dwordx4 v[130:131], off
	v_lshl_add_u64 v[130:131], v[204:205], 0, s[8:9]
	s_mov_b32 m0, s20
	s_nop 0
	global_load_lds_dwordx4 v[130:131], off
	v_lshl_add_u64 v[130:131], v[212:213], 0, s[8:9]
	s_mov_b32 m0, s21
	s_nop 0
	global_load_lds_dwordx4 v[130:131], off
	s_waitcnt lgkmcnt(0)
	s_barrier
	s_setprio 1
	s_waitcnt lgkmcnt(0)
	v_mfma_i32_16x16x64_i8 v[60:63], v[132:135], v[170:173], v[60:63]
	v_mfma_i32_16x16x64_i8 v[56:59], v[140:143], v[170:173], v[56:59]
	v_mfma_i32_16x16x64_i8 v[44:47], v[132:135], v[178:181], v[44:47]
	v_mfma_i32_16x16x64_i8 v[40:43], v[140:143], v[178:181], v[40:43]
	v_mfma_i32_16x16x64_i8 v[28:31], v[132:135], v[186:189], v[28:31]
	v_mfma_i32_16x16x64_i8 v[24:27], v[140:143], v[186:189], v[24:27]
	v_mfma_i32_16x16x64_i8 v[12:15], v[132:135], v[194:197], v[12:15]
	v_mfma_i32_16x16x64_i8 v[8:11], v[140:143], v[194:197], v[8:11]
	v_mfma_i32_16x16x64_i8 v[60:63], v[136:139], v[174:177], v[60:63]
	v_mfma_i32_16x16x64_i8 v[56:59], v[144:147], v[174:177], v[56:59]
	v_mfma_i32_16x16x64_i8 v[44:47], v[136:139], v[182:185], v[44:47]
	v_mfma_i32_16x16x64_i8 v[40:43], v[144:147], v[182:185], v[40:43]
	v_mfma_i32_16x16x64_i8 v[28:31], v[136:139], v[190:193], v[28:31]
	v_mfma_i32_16x16x64_i8 v[24:27], v[144:147], v[190:193], v[24:27]
	v_mfma_i32_16x16x64_i8 v[12:15], v[136:139], v[198:201], v[12:15]
	v_mfma_i32_16x16x64_i8 v[8:11], v[144:147], v[198:201], v[8:11]
	s_setprio 0
	s_setprio 1
	v_mfma_i32_16x16x64_i8 v[52:55], v[154:157], v[170:173], v[52:55]
	v_mfma_i32_16x16x64_i8 v[48:51], v[162:165], v[170:173], v[48:51]
	v_mfma_i32_16x16x64_i8 v[36:39], v[154:157], v[178:181], v[36:39]
	v_mfma_i32_16x16x64_i8 v[32:35], v[162:165], v[178:181], v[32:35]
	v_mfma_i32_16x16x64_i8 v[20:23], v[154:157], v[186:189], v[20:23]
	v_mfma_i32_16x16x64_i8 v[16:19], v[162:165], v[186:189], v[16:19]
	v_mfma_i32_16x16x64_i8 v[4:7], v[154:157], v[194:197], v[4:7]
	v_mfma_i32_16x16x64_i8 v[0:3], v[162:165], v[194:197], v[0:3]
	v_mfma_i32_16x16x64_i8 v[52:55], v[158:161], v[174:177], v[52:55]
	v_mfma_i32_16x16x64_i8 v[48:51], v[166:169], v[174:177], v[48:51]
	v_mfma_i32_16x16x64_i8 v[36:39], v[158:161], v[182:185], v[36:39]
	v_mfma_i32_16x16x64_i8 v[32:35], v[166:169], v[182:185], v[32:35]
	v_mfma_i32_16x16x64_i8 v[20:23], v[158:161], v[190:193], v[20:23]
	v_mfma_i32_16x16x64_i8 v[16:19], v[166:169], v[190:193], v[16:19]
	v_mfma_i32_16x16x64_i8 v[4:7], v[158:161], v[198:201], v[4:7]
	v_mfma_i32_16x16x64_i8 v[0:3], v[166:169], v[198:201], v[0:3]
	s_setprio 0
	s_waitcnt vmcnt(8)
	s_barrier
	s_add_u32 s43, s43, 0x100
	s_addc_u32 s55, s55, 0
	s_add_u32 s64, s64, 0x100
	s_addc_u32 s65, s65, 0
	s_add_u32 s66, s66, 0x100
	s_addc_u32 s67, s67, 0
	s_add_u32 s56, s56, 0x100
	s_addc_u32 s57, s57, 0
	s_cmp_ge_i32 s68, s0
	s_mov_b32 s58, s68
	s_cbranch_scc0 .LBB0_249
	s_and_b64 vcc, exec, s[40:41]
	s_cbranch_vccz .LBB0_252

; __device__ __forceinline__ int lane_id() { int l; asm volatile("v_mbcnt_lo_u32_b32 %0, -1, 0\n\tv_mbcnt_hi_u32_b32 %0, -1, %0" : "=v"(l)); return l; }
; #define G_STAGE(bufoff, gbase, voff) do { _Pragma("unroll") for (int _i = 0; _i < 2; ++_i) \
;         __builtin_amdgcn_global_load_lds((const unsigned*)((const char*)(gbase) + (voff)[_i]), (LAS unsigned*)(lds + (bufoff) + ldsw + _i * 8192), 16, 0, 0); } while (0)
; #define G_LDA(dst, b, h) do { _Pragma("unroll") for (int m = 0; m < 4; ++m) G_LD8(dst[m], lds + G_SA(b, h) + aoff + m * 2048); } while (0)
; #define G_LDB(dst, b, h) do { _Pragma("unroll") for (int n = 0; n < 2; ++n) G_LD8(dst[n], lds + G_SB(b, h) + boff + n * 2048); } while (0)
; #define G_SCHED __builtin_amdgcn_sched_barrier(0)
;     ...
;         for (int t = 0; t < nt; t += 2) {
;             const bool last = (t == nt - 2);
;             { const int tz_ = wid * 64 + lane_id();
; #pragma unroll
;               for (int i = 0; i < 2; ++i) { int R, C; stage_rc(tz_ * 16 + i * 8192, R, C); const int Rb = Epi::PERM ? ((R & ~31) + perm32(R & 31)) : R;
;                   voffA[i] = (unsigned)(R * S.multA * S.pitchA + C) * 2u; voffB[i] = (unsigned)(Rb * S.multB * S.pitchB + C) * 2u; } }
;             if constexpr (GATHER) asm volatile("" : "+v"(gc0[0]), "+v"(gc0[1]), "+v"(gc1[0]), "+v"(gc1[1]));
;             if constexpr (PREF) { if (t == nt - 4) S.prefetch(nxt, lds); }
;             const char* a11 = cur.a1 + (size_t)(t + 1) * kstep;
;             const char* a02 = last ? nxt.a0 : cur.a0 + (size_t)(t + 2) * kstep; const char* a12 = last ? nxt.a1 : cur.a1 + (size_t)(t + 2) * kstep;
;             const char* b02 = last ? nxt.b0 : cur.b0 + (size_t)(t + 2) * kstep; const char* b12 = last ? nxt.b1 : cur.b1 + (size_t)(t + 2) * kstep;
;             G_LDB(B0, 0, 0); G_LDB(B1, 0, 1); G_SCHED; G_LDA(At, 0, 0); G_STAGE(G_SA(1, 1), a11, vA1);
;     ...
;         for (int a = 0; a < 2; ++a)
; #pragma unroll
;             for (int b = 0; b < 2; ++b)
; #pragma unroll
;                 for (int m = 0; m < 4; ++m)
; #pragma unroll
;                     for (int n = 0; n < 2; ++n) acc[a][b][m][n] = (acc_t){0, 0, 0, 0};
;         cur = nxt; ++ui;
.LBB0_283:
	s_add_u32 s45, s68, 0x100
	s_addc_u32 s59, s69, 0
	s_add_u32 s61, s66, 0x100
	s_addc_u32 s70, s67, 0
	s_add_u32 s71, s64, 0x100
	s_addc_u32 s75, s65, 0
	s_add_u32 s62, s62, 0x80
	s_addc_u32 s63, s63, 0
	s_mov_b32 s64, 0
	v_mov_b32_e32 v0, 0
	v_mov_b32_e32 v1, 0
	v_mov_b32_e32 v2, 0
	v_mov_b32_e32 v3, 0
	v_mov_b32_e32 v4, 0
	v_mov_b32_e32 v5, 0
	v_mov_b32_e32 v6, 0
	v_mov_b32_e32 v7, 0
	s_waitcnt vmcnt(0)
	v_mov_b32_e32 v32, 0
	v_mov_b32_e32 v33, 0
	v_mov_b32_e32 v34, 0
	v_mov_b32_e32 v35, 0
	v_mov_b32_e32 v36, 0
	v_mov_b32_e32 v37, 0
	v_mov_b32_e32 v38, 0
	v_mov_b32_e32 v39, 0
	v_mov_b32_e32 v64, 0
	v_mov_b32_e32 v65, 0
	v_mov_b32_e32 v66, 0
	v_mov_b32_e32 v67, 0
	v_mov_b32_e32 v68, 0
	v_mov_b32_e32 v69, 0
	v_mov_b32_e32 v70, 0
	v_mov_b32_e32 v71, 0
	v_mov_b32_e32 v104, 0
	v_mov_b32_e32 v105, 0
	v_mov_b32_e32 v106, 0
	v_mov_b32_e32 v107, 0
	v_mov_b32_e32 v116, 0
	v_mov_b32_e32 v117, 0
	v_mov_b32_e32 v118, 0
	v_mov_b32_e32 v119, 0
	v_mov_b32_e32 v16, 0
	v_mov_b32_e32 v17, 0
	v_mov_b32_e32 v18, 0
	v_mov_b32_e32 v19, 0
	v_mov_b32_e32 v20, 0
	v_mov_b32_e32 v21, 0
	v_mov_b32_e32 v22, 0
	v_mov_b32_e32 v23, 0
	v_mov_b32_e32 v48, 0
	v_mov_b32_e32 v49, 0
	v_mov_b32_e32 v50, 0
	v_mov_b32_e32 v51, 0
	v_mov_b32_e32 v52, 0
	v_mov_b32_e32 v53, 0
	v_mov_b32_e32 v54, 0
	v_mov_b32_e32 v55, 0
	v_mov_b32_e32 v80, 0
	v_mov_b32_e32 v81, 0
	v_mov_b32_e32 v82, 0
	v_mov_b32_e32 v83, 0
	v_mov_b32_e32 v84, 0
	v_mov_b32_e32 v85, 0
	v_mov_b32_e32 v86, 0
	v_mov_b32_e32 v87, 0
	v_mov_b32_e32 v128, 0
	v_mov_b32_e32 v129, 0
	v_mov_b32_e32 v130, 0
	v_mov_b32_e32 v131, 0
	v_mov_b32_e32 v136, 0
	v_mov_b32_e32 v137, 0
	v_mov_b32_e32 v138, 0
	v_mov_b32_e32 v139, 0
	v_mov_b32_e32 v8, 0
	v_mov_b32_e32 v9, 0
	v_mov_b32_e32 v10, 0
	v_mov_b32_e32 v11, 0
	v_mov_b32_e32 v12, 0
	v_mov_b32_e32 v13, 0
	v_mov_b32_e32 v14, 0
	v_mov_b32_e32 v15, 0
	v_mov_b32_e32 v40, 0
	v_mov_b32_e32 v41, 0
	v_mov_b32_e32 v42, 0
	v_mov_b32_e32 v43, 0
	v_mov_b32_e32 v44, 0
	v_mov_b32_e32 v45, 0
	v_mov_b32_e32 v46, 0
	v_mov_b32_e32 v47, 0
	v_mov_b32_e32 v72, 0
	v_mov_b32_e32 v73, 0
	v_mov_b32_e32 v74, 0
	v_mov_b32_e32 v75, 0
	v_mov_b32_e32 v76, 0
	v_mov_b32_e32 v77, 0
	v_mov_b32_e32 v78, 0
	v_mov_b32_e32 v79, 0
	v_mov_b32_e32 v108, 0
	v_mov_b32_e32 v109, 0
	v_mov_b32_e32 v110, 0
	v_mov_b32_e32 v111, 0
	v_mov_b32_e32 v124, 0
	v_mov_b32_e32 v125, 0
	v_mov_b32_e32 v126, 0
	v_mov_b32_e32 v127, 0
	v_mov_b32_e32 v24, 0
	v_mov_b32_e32 v25, 0
	v_mov_b32_e32 v26, 0
	v_mov_b32_e32 v27, 0
	v_mov_b32_e32 v28, 0
	v_mov_b32_e32 v29, 0
	v_mov_b32_e32 v30, 0
	v_mov_b32_e32 v31, 0
	v_mov_b32_e32 v56, 0
	v_mov_b32_e32 v57, 0
	v_mov_b32_e32 v58, 0
	v_mov_b32_e32 v59, 0
	v_mov_b32_e32 v60, 0
	v_mov_b32_e32 v61, 0
	v_mov_b32_e32 v62, 0
	v_mov_b32_e32 v63, 0
	v_mov_b32_e32 v88, 0
	v_mov_b32_e32 v89, 0
	v_mov_b32_e32 v90, 0
	v_mov_b32_e32 v91, 0
	v_mov_b32_e32 v96, 0
	v_mov_b32_e32 v97, 0
	v_mov_b32_e32 v98, 0
	v_mov_b32_e32 v99, 0
	v_mov_b32_e32 v132, 0
	v_mov_b32_e32 v133, 0
	v_mov_b32_e32 v134, 0
	v_mov_b32_e32 v135, 0
	v_mov_b32_e32 v140, 0
	v_mov_b32_e32 v141, 0
	v_mov_b32_e32 v142, 0
	v_mov_b32_e32 v143, 0
	v_mbcnt_lo_u32_b32 v248, -1, 0
	v_mbcnt_hi_u32_b32 v248, -1, v248
	v_mov_b32_e32 v249, s88
	v_lshrrev_b32_e32 v249, 6, v249
	v_and_b32_e32 v250, 3, v248
	v_lshlrev_b32_e32 v250, 4, v250
	v_and_b32_e32 v251, 32, v248
	v_xor_b32_e32 v250, v250, v251
	v_and_b32_e32 v251, 1, v249
	v_lshl_add_u32 v250, v251, 6, v250
	v_lshrrev_b32_e32 v251, 1, v249
	v_lshrrev_b32_e32 v252, 2, v248
	v_lshl_add_u32 v251, v251, 4, v252
	v_mov_b32_e32 v253, 0x800
	v_mad_u32_u24 v240, v251, v253, v250
	v_add_u32_e32 v242, 0x20000, v240
	v_lshrrev_b32_e32 v251, 2, v249
	v_lshlrev_b32_e32 v251, 5, v251
	v_lshrrev_b32_e32 v252, 4, v248
	v_lshl_add_u32 v251, v252, 3, v251
	v_bfe_u32 v252, v249, 1, 1
	v_lshl_add_u32 v251, v252, 2, v251
	v_bfe_u32 v252, v248, 2, 2
	v_add_u32_e32 v251, v251, v252
	v_mov_b32_e32 v253, 0x800
	v_mad_u32_u24 v244, v251, v253, v250
	v_add_u32_e32 v246, 0x20000, v244
	v_mov_b32_e32 v241, 0
	v_mov_b32_e32 v243, 0
	v_mov_b32_e32 v245, 0
	v_mov_b32_e32 v247, 0
.LBB0_284:
	v_add_u32_e32 v144, s24, v157
	v_add_u32_e32 v168, s25, v157
	ds_read_b128 v[100:103], v144
	ds_read_b128 v[112:115], v144 offset:1024
	ds_read_b128 v[120:123], v144 offset:2048
	ds_read_b128 v[144:147], v144 offset:3072
	ds_read_b128 v[150:153], v168
	ds_read_b128 v[160:163], v168 offset:1024
	ds_read_b128 v[164:167], v168 offset:2048
	ds_read_b128 v[168:171], v168 offset:3072
	s_add_i32 s76, s64, 2
	s_add_u32 s77, s62, 0x80
	s_addc_u32 s65, s63, 0
	s_add_i32 s79, s24, s97
	s_add_i32 m0, s0, 0xc000
	s_add_i32 s78, s0, 0xe000
	s_add_i32 s80, s79, 0x2000
	s_cmp_eq_u32 s23, s64
	s_cselect_b32 s64, s50, s77
	s_cselect_b32 s67, s49, s75
	s_cselect_b32 s66, s48, s71
	s_cselect_b32 s69, s53, s59
	s_cselect_b32 s68, s52, s45
	s_cselect_b32 s65, s51, s65
	ds_read_b128 v[172:175], v158
	ds_read_b128 v[176:179], v158 offset:1024
	ds_read_b128 v[180:183], v158 offset:2048
	ds_read_b128 v[184:187], v158 offset:3072
	ds_read_b128 v[188:191], v158 offset:4096
	ds_read_b128 v[192:195], v158 offset:5120
	ds_read_b128 v[196:199], v158 offset:6144
	ds_read_b128 v[200:203], v158 offset:7168
	global_load_lds_dwordx4 v240, s[62:63]
	s_mov_b32 m0, s78
	s_nop 0
	global_load_lds_dwordx4 v242, s[62:63]
	s_waitcnt lgkmcnt(0)
	v_mov_b32_e32 v93, v149
	s_barrier
; #define G_STAGE(bufoff, gbase, voff) do { _Pragma("unroll") for (int _i = 0; _i < 2; ++_i) \
;         __builtin_amdgcn_global_load_lds((const unsigned*)((const char*)(gbase) + (voff)[_i]), (LAS unsigned*)(lds + (bufoff) + ldsw + _i * 8192), 16, 0, 0); } while (0)
; #define G_LDA(dst, b, h) do { _Pragma("unroll") for (int m = 0; m < 4; ++m) G_LD8(dst[m], lds + G_SA(b, h) + aoff + m * 2048); } while (0)
; #define G_WAIT_V(n) asm volatile("s_waitcnt vmcnt(" #n ")" ::: "memory")
; #define G_WAIT_L(n) asm volatile("s_waitcnt lgkmcnt(" #n ")" ::: "memory")
; #define G_BAR __builtin_amdgcn_s_barrier()
; #define G_SCHED __builtin_amdgcn_sched_barrier(0)
;     ...
;             G_WAIT_L(0); G_BAR; G_MMA(0, 0, At, B0); G_MMA(0, 1, At, B1); G_WAIT_V(8); G_BAR; G_SCHED;
;             G_LDA(At, 0, 1); G_STAGE(G_SB(0, 0), b02, voffB); G_STAGE(G_SB(0, 1), b12, voffB); G_STAGE(G_SA(0, 0), a02, vA0);
;             G_WAIT_L(0); G_BAR; G_MMA(1, 0, At, B0); G_MMA(1, 1, At, B1); G_WAIT_V(8); G_BAR; G_SCHED;
	s_setprio 1
	s_waitcnt lgkmcnt(0)
	v_mfma_i32_16x16x64_i8 v[140:143], v[100:103], v[172:175], v[140:143]
	v_mfma_i32_16x16x64_i8 v[132:135], v[120:123], v[172:175], v[132:135]
	v_mfma_i32_16x16x64_i8 v[94:97], v[100:103], v[180:183], v[96:99]
	v_mfma_i32_16x16x64_i8 v[88:91], v[120:123], v[180:183], v[88:91]
	v_mfma_i32_16x16x64_i8 v[60:63], v[100:103], v[188:191], v[60:63]
	v_mfma_i32_16x16x64_i8 v[56:59], v[120:123], v[188:191], v[56:59]
	v_mfma_i32_16x16x64_i8 v[28:31], v[100:103], v[196:199], v[28:31]
	v_mfma_i32_16x16x64_i8 v[24:27], v[120:123], v[196:199], v[24:27]
	v_mfma_i32_16x16x64_i8 v[140:143], v[112:115], v[176:179], v[140:143]
	v_mfma_i32_16x16x64_i8 v[132:135], v[144:147], v[176:179], v[132:135]
	v_mfma_i32_16x16x64_i8 v[94:97], v[112:115], v[184:187], v[94:97]
	v_mfma_i32_16x16x64_i8 v[88:91], v[144:147], v[184:187], v[88:91]
	v_mfma_i32_16x16x64_i8 v[60:63], v[112:115], v[192:195], v[60:63]
	v_mfma_i32_16x16x64_i8 v[56:59], v[144:147], v[192:195], v[56:59]
	v_mfma_i32_16x16x64_i8 v[28:31], v[112:115], v[200:203], v[28:31]
	v_mfma_i32_16x16x64_i8 v[24:27], v[144:147], v[200:203], v[24:27]
	s_setprio 0
	s_setprio 1
	v_mfma_i32_16x16x64_i8 v[124:127], v[150:153], v[172:175], v[124:127]
	v_mfma_i32_16x16x64_i8 v[108:111], v[164:167], v[172:175], v[108:111]
	v_mfma_i32_16x16x64_i8 v[76:79], v[150:153], v[180:183], v[76:79]
	v_mfma_i32_16x16x64_i8 v[72:75], v[164:167], v[180:183], v[72:75]
	v_mfma_i32_16x16x64_i8 v[44:47], v[150:153], v[188:191], v[44:47]
	v_mfma_i32_16x16x64_i8 v[40:43], v[164:167], v[188:191], v[40:43]
	v_mfma_i32_16x16x64_i8 v[12:15], v[150:153], v[196:199], v[12:15]
	v_mfma_i32_16x16x64_i8 v[8:11], v[164:167], v[196:199], v[8:11]
	v_mfma_i32_16x16x64_i8 v[124:127], v[160:163], v[176:179], v[124:127]
	v_mfma_i32_16x16x64_i8 v[108:111], v[168:171], v[176:179], v[108:111]
	v_mfma_i32_16x16x64_i8 v[76:79], v[160:163], v[184:187], v[76:79]
	v_mfma_i32_16x16x64_i8 v[72:75], v[168:171], v[184:187], v[72:75]
	v_mfma_i32_16x16x64_i8 v[44:47], v[160:163], v[192:195], v[44:47]
	v_mfma_i32_16x16x64_i8 v[40:43], v[168:171], v[192:195], v[40:43]
	v_mfma_i32_16x16x64_i8 v[12:15], v[160:163], v[200:203], v[12:15]
	v_mfma_i32_16x16x64_i8 v[8:11], v[168:171], v[200:203], v[8:11]
	s_setprio 0
	s_waitcnt vmcnt(8)
	s_barrier
	s_mov_b32 m0, s79
	ds_read_b128 v[172:175], v158 offset:16384
	ds_read_b128 v[176:179], v158 offset:17408
	ds_read_b128 v[180:183], v158 offset:18432
	ds_read_b128 v[184:187], v158 offset:19456
	ds_read_b128 v[188:191], v158 offset:20480
	ds_read_b128 v[192:195], v158 offset:21504
	ds_read_b128 v[196:199], v158 offset:22528
	ds_read_b128 v[200:203], v158 offset:23552
	v_mov_b32_e32 v205, v149
	global_load_lds_dwordx4 v244, s[68:69]
	v_mov_b32_e32 v207, v149
	s_mov_b32 m0, s80
	v_lshl_add_u64 v[208:209], s[68:69], 0, v[244:245]
	v_lshl_add_u64 v[210:211], s[68:69], 0, v[246:247]
	global_load_lds_dwordx4 v246, s[68:69]
	s_cselect_b32 s69, s55, s70
	s_cselect_b32 s68, s54, s61
	s_add_i32 s77, s25, s97
	s_mov_b32 m0, s77
	v_lshl_add_u64 v[212:213], s[68:69], 0, v[244:245]
	global_load_lds_dwordx4 v244, s[68:69]
	s_add_i32 m0, s77, 0x2000
	v_lshl_add_u64 v[204:205], s[68:69], 0, v[246:247]
	global_load_lds_dwordx4 v246, s[68:69]
	s_mov_b32 m0, s0
	v_lshl_add_u64 v[206:207], s[66:67], 0, v[240:241]
	global_load_lds_dwordx4 v240, s[66:67]
	s_mov_b32 m0, s11
	v_lshl_add_u64 v[214:215], s[66:67], 0, v[242:243]
	global_load_lds_dwordx4 v242, s[66:67]
	s_waitcnt lgkmcnt(0)
	s_barrier
	s_setprio 1
	s_waitcnt lgkmcnt(0)
	v_mfma_i32_16x16x64_i8 v[136:139], v[100:103], v[172:175], v[136:139]
	v_mfma_i32_16x16x64_i8 v[128:131], v[120:123], v[172:175], v[128:131]
	v_mfma_i32_16x16x64_i8 v[84:87], v[100:103], v[180:183], v[84:87]
	v_mfma_i32_16x16x64_i8 v[80:83], v[120:123], v[180:183], v[80:83]
	v_mfma_i32_16x16x64_i8 v[52:55], v[100:103], v[188:191], v[52:55]
	v_mfma_i32_16x16x64_i8 v[48:51], v[120:123], v[188:191], v[48:51]
	v_mfma_i32_16x16x64_i8 v[20:23], v[100:103], v[196:199], v[20:23]
	v_mfma_i32_16x16x64_i8 v[16:19], v[120:123], v[196:199], v[16:19]
	v_mfma_i32_16x16x64_i8 v[136:139], v[112:115], v[176:179], v[136:139]
	v_mfma_i32_16x16x64_i8 v[128:131], v[144:147], v[176:179], v[128:131]
	v_mfma_i32_16x16x64_i8 v[84:87], v[112:115], v[184:187], v[84:87]
	v_mfma_i32_16x16x64_i8 v[80:83], v[144:147], v[184:187], v[80:83]
	v_mfma_i32_16x16x64_i8 v[52:55], v[112:115], v[192:195], v[52:55]
	v_mfma_i32_16x16x64_i8 v[48:51], v[144:147], v[192:195], v[48:51]
	v_mfma_i32_16x16x64_i8 v[20:23], v[112:115], v[200:203], v[20:23]
	v_mfma_i32_16x16x64_i8 v[16:19], v[144:147], v[200:203], v[16:19]
	s_setprio 0
	s_setprio 1
	v_mfma_i32_16x16x64_i8 v[104:107], v[164:167], v[172:175], v[104:107]
	v_mfma_i32_16x16x64_i8 v[68:71], v[150:153], v[180:183], v[68:71]
	v_mfma_i32_16x16x64_i8 v[64:67], v[164:167], v[180:183], v[64:67]
	v_mfma_i32_16x16x64_i8 v[36:39], v[150:153], v[188:191], v[36:39]
	v_mfma_i32_16x16x64_i8 v[32:35], v[164:167], v[188:191], v[32:35]
	v_mfma_i32_16x16x64_i8 v[4:7], v[150:153], v[196:199], v[4:7]
	v_mfma_i32_16x16x64_i8 v[0:3], v[164:167], v[196:199], v[0:3]
	v_mfma_i32_16x16x64_i8 v[98:101], v[150:153], v[172:175], v[116:119]
	v_mfma_i32_16x16x64_i8 v[104:107], v[168:171], v[176:179], v[104:107]
	v_mfma_i32_16x16x64_i8 v[68:71], v[160:163], v[184:187], v[68:71]
	v_mfma_i32_16x16x64_i8 v[64:67], v[168:171], v[184:187], v[64:67]
	v_mfma_i32_16x16x64_i8 v[36:39], v[160:163], v[192:195], v[36:39]
	v_mfma_i32_16x16x64_i8 v[32:35], v[168:171], v[192:195], v[32:35]
	v_mfma_i32_16x16x64_i8 v[4:7], v[160:163], v[200:203], v[4:7]
	v_mfma_i32_16x16x64_i8 v[0:3], v[168:171], v[200:203], v[0:3]
	v_mfma_i32_16x16x64_i8 v[100:103], v[160:163], v[176:179], v[98:101]
	s_setprio 0
	s_waitcnt vmcnt(8)
	s_barrier
; #define G_STAGE(bufoff, gbase, voff) do { _Pragma("unroll") for (int _i = 0; _i < 2; ++_i) \
;         __builtin_amdgcn_global_load_lds((const unsigned*)((const char*)(gbase) + (voff)[_i]), (LAS unsigned*)(lds + (bufoff) + ldsw + _i * 8192), 16, 0, 0); } while (0)
; #define G_LDA(dst, b, h) do { _Pragma("unroll") for (int m = 0; m < 4; ++m) G_LD8(dst[m], lds + G_SA(b, h) + aoff + m * 2048); } while (0)
; #define G_LDB(dst, b, h) do { _Pragma("unroll") for (int n = 0; n < 2; ++n) G_LD8(dst[n], lds + G_SB(b, h) + boff + n * 2048); } while (0)
; #define G_WAIT_V(n) asm volatile("s_waitcnt vmcnt(" #n ")" ::: "memory")
; #define G_WAIT_L(n) asm volatile("s_waitcnt lgkmcnt(" #n ")" ::: "memory")
; #define G_BAR __builtin_amdgcn_s_barrier()
; #define G_SCHED __builtin_amdgcn_sched_barrier(0)
;     ...
;             G_LDB(B0, 1, 0); G_LDB(B1, 1, 1); G_SCHED; G_LDA(At, 1, 0); G_STAGE(G_SA(0, 1), a12, vA1);
;             G_WAIT_L(0); G_BAR; G_MMA(0, 0, At, B0); G_MMA(0, 1, At, B1); G_WAIT_V(8); G_BAR; G_SCHED;
;             G_LDA(At, 1, 1); G_STAGE(G_SB(1, 0), b02 + kstep, voffB); G_STAGE(G_SB(1, 1), b12 + kstep, voffB); G_STAGE(G_SA(1, 0), a02 + kstep, vA0);
;             G_WAIT_L(0); G_BAR; G_MMA(1, 0, At, B0); G_MMA(1, 1, At, B1); G_WAIT_V(8); G_BAR; G_SCHED;
;         }
	s_add_i32 s66, 0, 0x18000
	v_add_u32_e32 v93, s66, v157
	s_add_i32 s67, 0, 0x1c000
	ds_read_b128 v[112:115], v93
	ds_read_b128 v[116:119], v93 offset:1024
	ds_read_b128 v[120:123], v93 offset:2048
	ds_read_b128 v[144:147], v93 offset:3072
	v_add_u32_e32 v93, s67, v157
	ds_read_b128 v[150:153], v93
	ds_read_b128 v[160:163], v93 offset:1024
	ds_read_b128 v[164:167], v93 offset:2048
	ds_read_b128 v[168:171], v93 offset:3072
	s_mov_b32 m0, s18
	ds_read_b128 v[172:175], v158 offset:32768
	ds_read_b128 v[176:179], v158 offset:33792
	ds_read_b128 v[180:183], v158 offset:34816
	ds_read_b128 v[184:187], v158 offset:35840
	ds_read_b128 v[188:191], v158 offset:36864
	ds_read_b128 v[192:195], v158 offset:37888
	ds_read_b128 v[196:199], v158 offset:38912
	ds_read_b128 v[200:203], v158 offset:39936
	global_load_lds_dwordx4 v240, s[64:65]
	s_mov_b32 m0, s19
	s_nop 0
	global_load_lds_dwordx4 v242, s[64:65]
	s_waitcnt lgkmcnt(0)
	s_barrier
	s_setprio 1
	s_waitcnt lgkmcnt(0)
	v_mfma_i32_16x16x64_i8 v[140:143], v[112:115], v[172:175], v[140:143]
	v_mfma_i32_16x16x64_i8 v[132:135], v[120:123], v[172:175], v[132:135]
	v_mfma_i32_16x16x64_i8 v[92:95], v[112:115], v[180:183], v[94:97]
	v_mfma_i32_16x16x64_i8 v[88:91], v[120:123], v[180:183], v[88:91]
	v_mfma_i32_16x16x64_i8 v[60:63], v[112:115], v[188:191], v[60:63]
	v_mfma_i32_16x16x64_i8 v[56:59], v[120:123], v[188:191], v[56:59]
	v_mfma_i32_16x16x64_i8 v[28:31], v[112:115], v[196:199], v[28:31]
	v_mfma_i32_16x16x64_i8 v[24:27], v[120:123], v[196:199], v[24:27]
	v_mfma_i32_16x16x64_i8 v[140:143], v[116:119], v[176:179], v[140:143]
	v_mfma_i32_16x16x64_i8 v[132:135], v[144:147], v[176:179], v[132:135]
	v_mfma_i32_16x16x64_i8 v[96:99], v[116:119], v[184:187], v[92:95]
	v_mfma_i32_16x16x64_i8 v[88:91], v[144:147], v[184:187], v[88:91]
	v_mfma_i32_16x16x64_i8 v[60:63], v[116:119], v[192:195], v[60:63]
	v_mfma_i32_16x16x64_i8 v[56:59], v[144:147], v[192:195], v[56:59]
	v_mfma_i32_16x16x64_i8 v[28:31], v[116:119], v[200:203], v[28:31]
	v_mfma_i32_16x16x64_i8 v[24:27], v[144:147], v[200:203], v[24:27]
	s_setprio 0
	s_setprio 1
	v_mfma_i32_16x16x64_i8 v[92:95], v[150:153], v[172:175], v[124:127]
	v_mfma_i32_16x16x64_i8 v[124:127], v[160:163], v[176:179], v[92:95]
	v_mfma_i32_16x16x64_i8 v[92:95], v[164:167], v[172:175], v[108:111]
	v_mfma_i32_16x16x64_i8 v[76:79], v[150:153], v[180:183], v[76:79]
	v_mfma_i32_16x16x64_i8 v[72:75], v[164:167], v[180:183], v[72:75]
	v_mfma_i32_16x16x64_i8 v[44:47], v[150:153], v[188:191], v[44:47]
	v_mfma_i32_16x16x64_i8 v[40:43], v[164:167], v[188:191], v[40:43]
	v_mfma_i32_16x16x64_i8 v[12:15], v[150:153], v[196:199], v[12:15]
	v_mfma_i32_16x16x64_i8 v[8:11], v[164:167], v[196:199], v[8:11]
	v_mfma_i32_16x16x64_i8 v[108:111], v[168:171], v[176:179], v[92:95]
	v_mfma_i32_16x16x64_i8 v[76:79], v[160:163], v[184:187], v[76:79]
	v_mfma_i32_16x16x64_i8 v[72:75], v[168:171], v[184:187], v[72:75]
	v_mfma_i32_16x16x64_i8 v[44:47], v[160:163], v[192:195], v[44:47]
	v_mfma_i32_16x16x64_i8 v[40:43], v[168:171], v[192:195], v[40:43]
	v_mfma_i32_16x16x64_i8 v[12:15], v[160:163], v[200:203], v[12:15]
	v_mfma_i32_16x16x64_i8 v[8:11], v[168:171], v[200:203], v[8:11]
	s_setprio 0
	s_waitcnt vmcnt(8)
	s_barrier
	s_add_i32 s64, s66, s97
	v_lshl_add_u64 v[200:201], v[208:209], 0, s[38:39]
	s_mov_b32 m0, s64
	ds_read_b128 v[92:95], v158 offset:49152
	ds_read_b128 v[172:175], v158 offset:50176
	ds_read_b128 v[176:179], v158 offset:51200
	ds_read_b128 v[180:183], v158 offset:52224
	ds_read_b128 v[184:187], v158 offset:53248
	ds_read_b128 v[188:191], v158 offset:54272
	ds_read_b128 v[192:195], v158 offset:55296
	ds_read_b128 v[196:199], v158 offset:56320
	global_load_lds_dwordx4 v[200:201], off
	v_lshl_add_u64 v[200:201], v[210:211], 0, s[38:39]
	s_add_i32 m0, s64, 0x2000
	s_add_i32 s64, s67, s97
	global_load_lds_dwordx4 v[200:201], off
	v_lshl_add_u64 v[200:201], v[212:213], 0, s[38:39]
	s_mov_b32 m0, s64
	s_nop 0
	global_load_lds_dwordx4 v[200:201], off
	v_lshl_add_u64 v[200:201], v[204:205], 0, s[38:39]
	s_add_i32 m0, s64, 0x2000
	s_nop 0
	global_load_lds_dwordx4 v[200:201], off
	v_lshl_add_u64 v[200:201], v[206:207], 0, s[38:39]
	s_mov_b32 m0, s21
	s_nop 0
	global_load_lds_dwordx4 v[200:201], off
	v_lshl_add_u64 v[200:201], v[214:215], 0, s[38:39]
	s_mov_b32 m0, s22
	s_nop 0
	global_load_lds_dwordx4 v[200:201], off
	s_waitcnt lgkmcnt(0)
	s_barrier
	s_setprio 1
	s_waitcnt lgkmcnt(0)
	v_mfma_i32_16x16x64_i8 v[136:139], v[112:115], v[92:95], v[136:139]
	v_mfma_i32_16x16x64_i8 v[128:131], v[120:123], v[92:95], v[128:131]
	v_mfma_i32_16x16x64_i8 v[84:87], v[112:115], v[176:179], v[84:87]
	v_mfma_i32_16x16x64_i8 v[80:83], v[120:123], v[176:179], v[80:83]
	v_mfma_i32_16x16x64_i8 v[52:55], v[112:115], v[184:187], v[52:55]
	v_mfma_i32_16x16x64_i8 v[48:51], v[120:123], v[184:187], v[48:51]
	v_mfma_i32_16x16x64_i8 v[20:23], v[112:115], v[192:195], v[20:23]
	v_mfma_i32_16x16x64_i8 v[16:19], v[120:123], v[192:195], v[16:19]
	v_mfma_i32_16x16x64_i8 v[136:139], v[116:119], v[172:175], v[136:139]
	v_mfma_i32_16x16x64_i8 v[128:131], v[144:147], v[172:175], v[128:131]
	v_mfma_i32_16x16x64_i8 v[84:87], v[116:119], v[180:183], v[84:87]
	v_mfma_i32_16x16x64_i8 v[80:83], v[144:147], v[180:183], v[80:83]
	v_mfma_i32_16x16x64_i8 v[52:55], v[116:119], v[188:191], v[52:55]
	v_mfma_i32_16x16x64_i8 v[48:51], v[144:147], v[188:191], v[48:51]
	v_mfma_i32_16x16x64_i8 v[20:23], v[116:119], v[196:199], v[20:23]
	v_mfma_i32_16x16x64_i8 v[16:19], v[144:147], v[196:199], v[16:19]
	s_setprio 0
	s_setprio 1
	v_mfma_i32_16x16x64_i8 v[100:103], v[150:153], v[92:95], v[100:103]
	v_mfma_i32_16x16x64_i8 v[92:95], v[164:167], v[92:95], v[104:107]
	v_mfma_i32_16x16x64_i8 v[68:71], v[150:153], v[176:179], v[68:71]
	v_mfma_i32_16x16x64_i8 v[64:67], v[164:167], v[176:179], v[64:67]
	v_mfma_i32_16x16x64_i8 v[36:39], v[150:153], v[184:187], v[36:39]
	v_mfma_i32_16x16x64_i8 v[32:35], v[164:167], v[184:187], v[32:35]
	v_mfma_i32_16x16x64_i8 v[4:7], v[150:153], v[192:195], v[4:7]
	v_mfma_i32_16x16x64_i8 v[0:3], v[164:167], v[192:195], v[0:3]
	v_mfma_i32_16x16x64_i8 v[116:119], v[160:163], v[172:175], v[100:103]
	v_mfma_i32_16x16x64_i8 v[104:107], v[168:171], v[172:175], v[92:95]
	v_mfma_i32_16x16x64_i8 v[68:71], v[160:163], v[180:183], v[68:71]
	v_mfma_i32_16x16x64_i8 v[64:67], v[168:171], v[180:183], v[64:67]
	v_mfma_i32_16x16x64_i8 v[36:39], v[160:163], v[188:191], v[36:39]
	v_mfma_i32_16x16x64_i8 v[32:35], v[168:171], v[188:191], v[32:35]
	v_mfma_i32_16x16x64_i8 v[4:7], v[160:163], v[196:199], v[4:7]
	v_mfma_i32_16x16x64_i8 v[0:3], v[168:171], v[196:199], v[0:3]
	s_setprio 0
	s_waitcnt vmcnt(8)
	s_barrier
	s_add_u32 s45, s45, 0x100
	s_addc_u32 s59, s59, 0
	s_add_u32 s61, s61, 0x100
	s_addc_u32 s70, s70, 0
	s_add_u32 s71, s71, 0x100
	s_addc_u32 s75, s75, 0
	s_add_u32 s62, s62, 0x100
	s_addc_u32 s63, s63, 0
	s_cmp_ge_i32 s76, s3
	s_mov_b32 s64, s76
	s_cbranch_scc0 .LBB0_284
	v_readlane_b32 s78, v255, 11
	v_readlane_b32 s79, v255, 13
	s_branch .LBB0_289

; __device__ __forceinline__ int lane_id() { int l; asm volatile("v_mbcnt_lo_u32_b32 %0, -1, 0\n\tv_mbcnt_hi_u32_b32 %0, -1, %0" : "=v"(l)); return l; }
; #define G_STAGE(bufoff, gbase, voff) do { _Pragma("unroll") for (int _i = 0; _i < 2; ++_i) \
;         __builtin_amdgcn_global_load_lds((const unsigned*)((const char*)(gbase) + (voff)[_i]), (LAS unsigned*)(lds + (bufoff) + ldsw + _i * 8192), 16, 0, 0); } while (0)
; #define G_LDA(dst, b, h) do { _Pragma("unroll") for (int m = 0; m < 4; ++m) G_LD8(dst[m], lds + G_SA(b, h) + aoff + m * 2048); } while (0)
; #define G_LDB(dst, b, h) do { _Pragma("unroll") for (int n = 0; n < 2; ++n) G_LD8(dst[n], lds + G_SB(b, h) + boff + n * 2048); } while (0)
; #define G_SCHED __builtin_amdgcn_sched_barrier(0)
;     ...
;         for (int t = 0; t < nt; t += 2) {
;             const bool last = (t == nt - 2);
;             { const int tz_ = wid * 64 + lane_id();
; #pragma unroll
;               for (int i = 0; i < 2; ++i) { int R, C; stage_rc(tz_ * 16 + i * 8192, R, C); const int Rb = Epi::PERM ? ((R & ~31) + perm32(R & 31)) : R;
;                   voffA[i] = (unsigned)(R * S.multA * S.pitchA + C) * 2u; voffB[i] = (unsigned)(Rb * S.multB * S.pitchB + C) * 2u; } }
;             if constexpr (GATHER) asm volatile("" : "+v"(gc0[0]), "+v"(gc0[1]), "+v"(gc1[0]), "+v"(gc1[1]));
;             if constexpr (PREF) { if (t == nt - 4) S.prefetch(nxt, lds); }
;             const char* a11 = cur.a1 + (size_t)(t + 1) * kstep;
;             const char* a02 = last ? nxt.a0 : cur.a0 + (size_t)(t + 2) * kstep; const char* a12 = last ? nxt.a1 : cur.a1 + (size_t)(t + 2) * kstep;
;             const char* b02 = last ? nxt.b0 : cur.b0 + (size_t)(t + 2) * kstep; const char* b12 = last ? nxt.b1 : cur.b1 + (size_t)(t + 2) * kstep;
;             G_LDB(B0, 0, 0); G_LDB(B1, 0, 1); G_SCHED; G_LDA(At, 0, 0); G_STAGE(G_SA(1, 1), a11, vA1);
;     ...
;         for (int a = 0; a < 2; ++a)
; #pragma unroll
;             for (int b = 0; b < 2; ++b)
; #pragma unroll
;                 for (int m = 0; m < 4; ++m)
; #pragma unroll
;                     for (int n = 0; n < 2; ++n) acc[a][b][m][n] = (acc_t){0, 0, 0, 0};
;         cur = nxt; ++ui;
.LBB0_521:
	s_add_u32 s62, s56, 0x100
	s_addc_u32 s63, s57, 0
	s_add_u32 s64, s54, 0x100
	s_addc_u32 s75, s55, 0
	s_add_u32 s77, s60, 0x100
	s_addc_u32 s78, s61, 0
	s_add_u32 s54, s58, 0x80
	v_mov_b32_e32 v0, 0
	s_addc_u32 s55, s59, 0
	s_mov_b32 s56, 0
	v_mov_b32_e32 v1, v0
	v_mov_b32_e32 v2, v0
	v_mov_b32_e32 v3, v0
	v_mov_b32_e32 v4, v0
	v_mov_b32_e32 v5, v0
	v_mov_b32_e32 v6, v0
	v_mov_b32_e32 v7, v0
	v_mov_b32_e32 v32, v0
	v_mov_b32_e32 v33, v0
	v_mov_b32_e32 v34, v0
	v_mov_b32_e32 v35, v0
	v_mov_b32_e32 v36, v0
	v_mov_b32_e32 v37, v0
	v_mov_b32_e32 v38, v0
	v_mov_b32_e32 v39, v0
	v_mov_b32_e32 v64, v0
	v_mov_b32_e32 v65, v0
	v_mov_b32_e32 v66, v0
	v_mov_b32_e32 v67, v0
	v_mov_b32_e32 v68, v0
	v_mov_b32_e32 v69, v0
	v_mov_b32_e32 v70, v0
	v_mov_b32_e32 v71, v0
	v_mov_b32_e32 v96, v0
	v_mov_b32_e32 v97, v0
	v_mov_b32_e32 v98, v0
	v_mov_b32_e32 v99, v0
	v_mov_b32_e32 v100, v0
	v_mov_b32_e32 v101, v0
	v_mov_b32_e32 v102, v0
	v_mov_b32_e32 v103, v0
	v_mov_b32_e32 v12, v0
	v_mov_b32_e32 v13, v0
	v_mov_b32_e32 v14, v0
	v_mov_b32_e32 v15, v0
	v_mov_b32_e32 v20, v0
	v_mov_b32_e32 v21, v0
	v_mov_b32_e32 v22, v0
	v_mov_b32_e32 v23, v0
	v_mov_b32_e32 v44, v0
	v_mov_b32_e32 v45, v0
	v_mov_b32_e32 v46, v0
	v_mov_b32_e32 v47, v0
	v_mov_b32_e32 v52, v0
	v_mov_b32_e32 v53, v0
	v_mov_b32_e32 v54, v0
	v_mov_b32_e32 v55, v0
	v_mov_b32_e32 v76, v0
	v_mov_b32_e32 v77, v0
	v_mov_b32_e32 v78, v0
	v_mov_b32_e32 v79, v0
	v_mov_b32_e32 v84, v0
	v_mov_b32_e32 v85, v0
	v_mov_b32_e32 v86, v0
	v_mov_b32_e32 v87, v0
	v_mov_b32_e32 v108, v0
	v_mov_b32_e32 v109, v0
	v_mov_b32_e32 v110, v0
	v_mov_b32_e32 v111, v0
	v_mov_b32_e32 v116, v0
	v_mov_b32_e32 v117, v0
	v_mov_b32_e32 v118, v0
	v_mov_b32_e32 v119, v0
	v_mov_b32_e32 v8, v0
	v_mov_b32_e32 v9, v0
	v_mov_b32_e32 v10, v0
	v_mov_b32_e32 v11, v0
	v_mov_b32_e32 v16, v0
	v_mov_b32_e32 v17, v0
	v_mov_b32_e32 v18, v0
	v_mov_b32_e32 v19, v0
	v_mov_b32_e32 v40, v0
	v_mov_b32_e32 v41, v0
	v_mov_b32_e32 v42, v0
	v_mov_b32_e32 v43, v0
	v_mov_b32_e32 v48, v0
	v_mov_b32_e32 v49, v0
	v_mov_b32_e32 v50, v0
	v_mov_b32_e32 v51, v0
	v_mov_b32_e32 v72, v0
	v_mov_b32_e32 v73, v0
	v_mov_b32_e32 v74, v0
	v_mov_b32_e32 v75, v0
	v_mov_b32_e32 v80, v0
	v_mov_b32_e32 v81, v0
	v_mov_b32_e32 v82, v0
	v_mov_b32_e32 v83, v0
	v_mov_b32_e32 v104, v0
	v_mov_b32_e32 v105, v0
	v_mov_b32_e32 v106, v0
	v_mov_b32_e32 v107, v0
	v_mov_b32_e32 v112, v0
	v_mov_b32_e32 v113, v0
	v_mov_b32_e32 v114, v0
	v_mov_b32_e32 v115, v0
	v_mov_b32_e32 v24, v0
	v_mov_b32_e32 v25, v0
	v_mov_b32_e32 v26, v0
	v_mov_b32_e32 v27, v0
	v_mov_b32_e32 v28, v0
	v_mov_b32_e32 v29, v0
	v_mov_b32_e32 v30, v0
	v_mov_b32_e32 v31, v0
	v_mov_b32_e32 v56, v0
	v_mov_b32_e32 v57, v0
	v_mov_b32_e32 v58, v0
	v_mov_b32_e32 v59, v0
	v_mov_b32_e32 v60, v0
	v_mov_b32_e32 v61, v0
	v_mov_b32_e32 v62, v0
	v_mov_b32_e32 v63, v0
	v_mov_b32_e32 v88, v0
	v_mov_b32_e32 v89, v0
	v_mov_b32_e32 v90, v0
	v_mov_b32_e32 v91, v0
	v_mov_b32_e32 v92, v0
	v_mov_b32_e32 v93, v0
	v_mov_b32_e32 v94, v0
	v_mov_b32_e32 v95, v0
	v_mov_b32_e32 v120, v0
	v_mov_b32_e32 v121, v0
	v_mov_b32_e32 v122, v0
	v_mov_b32_e32 v123, v0
	v_mov_b32_e32 v124, v0
	v_mov_b32_e32 v125, v0
	v_mov_b32_e32 v126, v0
	v_mov_b32_e32 v127, v0
	v_mbcnt_lo_u32_b32 v248, -1, 0
	v_mbcnt_hi_u32_b32 v248, -1, v248
	v_mov_b32_e32 v249, s88
	v_lshrrev_b32_e32 v249, 6, v249
	v_and_b32_e32 v250, 3, v248
	v_lshlrev_b32_e32 v250, 4, v250
	v_and_b32_e32 v251, 32, v248
	v_xor_b32_e32 v250, v250, v251
	v_and_b32_e32 v251, 1, v249
	v_lshl_add_u32 v250, v251, 6, v250
	v_lshrrev_b32_e32 v251, 1, v249
	v_lshrrev_b32_e32 v252, 2, v248
	v_lshl_add_u32 v251, v251, 4, v252
	v_mov_b32_e32 v253, 0x100
	v_mad_u32_u24 v240, v251, v253, v250
	v_add_u32_e32 v242, 0x4000, v240
	v_lshrrev_b32_e32 v251, 2, v249
	v_lshlrev_b32_e32 v251, 5, v251
	v_lshrrev_b32_e32 v252, 4, v248
	v_lshl_add_u32 v251, v252, 3, v251
	v_bfe_u32 v252, v249, 1, 1
	v_lshl_add_u32 v251, v252, 2, v251
	v_bfe_u32 v252, v248, 2, 2
	v_add_u32_e32 v251, v251, v252
	v_mov_b32_e32 v253, 0x100
	v_mad_u32_u24 v244, v251, v253, v250
	v_add_u32_e32 v246, 0x4000, v244
	v_mov_b32_e32 v241, 0
	v_mov_b32_e32 v243, 0
	v_mov_b32_e32 v245, 0
	v_mov_b32_e32 v247, 0
.LBB0_522:
	s_add_i32 s79, s56, 2
	ds_read_b128 v[142:145], v138
	ds_read_b128 v[146:149], v138 offset:1024
	ds_read_b128 v[150:153], v138 offset:2048
	ds_read_b128 v[154:157], v138 offset:3072
	ds_read_b128 v[158:161], v139
	ds_read_b128 v[162:165], v139 offset:1024
	ds_read_b128 v[166:169], v139 offset:2048
	ds_read_b128 v[170:173], v139 offset:3072
	s_add_u32 s80, s54, 0x80
	s_addc_u32 s57, s55, 0
	s_add_i32 s82, s72, s20
	s_add_i32 m0, s27, 0xc000
	s_add_i32 s81, s27, 0xe000
	s_add_i32 s83, s82, 0x2000
	s_cmp_eq_u32 s71, s56
	s_cselect_b32 s56, s48, s80
	s_cselect_b32 s59, s51, s78
	s_cselect_b32 s58, s50, s77
	s_cselect_b32 s61, s45, s63
	s_cselect_b32 s60, s44, s62
	s_cselect_b32 s57, s49, s57
	ds_read_b128 v[174:177], v140
	ds_read_b128 v[178:181], v140 offset:1024
	ds_read_b128 v[182:185], v140 offset:2048
	ds_read_b128 v[186:189], v140 offset:3072
	ds_read_b128 v[190:193], v140 offset:4096
	ds_read_b128 v[194:197], v140 offset:5120
	ds_read_b128 v[198:201], v140 offset:6144
	ds_read_b128 v[202:205], v140 offset:7168
	global_load_lds_dwordx4 v240, s[54:55]
	s_mov_b32 m0, s81
	s_nop 0
	global_load_lds_dwordx4 v242, s[54:55]
	s_waitcnt lgkmcnt(0)
	v_mov_b32_e32 v131, v129
	s_barrier
; #define G_STAGE(bufoff, gbase, voff) do { _Pragma("unroll") for (int _i = 0; _i < 2; ++_i) \
;         __builtin_amdgcn_global_load_lds((const unsigned*)((const char*)(gbase) + (voff)[_i]), (LAS unsigned*)(lds + (bufoff) + ldsw + _i * 8192), 16, 0, 0); } while (0)
; #define G_LDA(dst, b, h) do { _Pragma("unroll") for (int m = 0; m < 4; ++m) G_LD8(dst[m], lds + G_SA(b, h) + aoff + m * 2048); } while (0)
; #define G_WAIT_V(n) asm volatile("s_waitcnt vmcnt(" #n ")" ::: "memory")
; #define G_WAIT_L(n) asm volatile("s_waitcnt lgkmcnt(" #n ")" ::: "memory")
; #define G_BAR __builtin_amdgcn_s_barrier()
; #define G_SCHED __builtin_amdgcn_sched_barrier(0)
;     ...
;             G_WAIT_L(0); G_BAR; G_MMA(0, 0, At, B0); G_MMA(0, 1, At, B1); G_WAIT_V(8); G_BAR; G_SCHED;
;             G_LDA(At, 0, 1); G_STAGE(G_SB(0, 0), b02, voffB); G_STAGE(G_SB(0, 1), b12, voffB); G_STAGE(G_SA(0, 0), a02, vA0);
;             G_WAIT_L(0); G_BAR; G_MMA(1, 0, At, B0); G_MMA(1, 1, At, B1); G_WAIT_V(8); G_BAR; G_SCHED;
	s_setprio 1
	s_waitcnt lgkmcnt(0)
	v_mfma_f32_16x16x32_bf16 v[124:127], v[142:145], v[174:177], v[124:127]
	v_mfma_f32_16x16x32_bf16 v[120:123], v[150:153], v[174:177], v[120:123]
	v_mfma_f32_16x16x32_bf16 v[92:95], v[142:145], v[182:185], v[92:95]
	v_mfma_f32_16x16x32_bf16 v[88:91], v[150:153], v[182:185], v[88:91]
	v_mfma_f32_16x16x32_bf16 v[60:63], v[142:145], v[190:193], v[60:63]
	v_mfma_f32_16x16x32_bf16 v[56:59], v[150:153], v[190:193], v[56:59]
	v_mfma_f32_16x16x32_bf16 v[28:31], v[142:145], v[198:201], v[28:31]
	v_mfma_f32_16x16x32_bf16 v[24:27], v[150:153], v[198:201], v[24:27]
	v_mfma_f32_16x16x32_bf16 v[124:127], v[146:149], v[178:181], v[124:127]
	v_mfma_f32_16x16x32_bf16 v[120:123], v[154:157], v[178:181], v[120:123]
	v_mfma_f32_16x16x32_bf16 v[92:95], v[146:149], v[186:189], v[92:95]
	v_mfma_f32_16x16x32_bf16 v[88:91], v[154:157], v[186:189], v[88:91]
	v_mfma_f32_16x16x32_bf16 v[60:63], v[146:149], v[194:197], v[60:63]
	v_mfma_f32_16x16x32_bf16 v[56:59], v[154:157], v[194:197], v[56:59]
	v_mfma_f32_16x16x32_bf16 v[28:31], v[146:149], v[202:205], v[28:31]
	v_mfma_f32_16x16x32_bf16 v[24:27], v[154:157], v[202:205], v[24:27]
	s_setprio 0
	s_setprio 1
	v_mfma_f32_16x16x32_bf16 v[112:115], v[158:161], v[174:177], v[112:115]
	v_mfma_f32_16x16x32_bf16 v[104:107], v[166:169], v[174:177], v[104:107]
	v_mfma_f32_16x16x32_bf16 v[80:83], v[158:161], v[182:185], v[80:83]
	v_mfma_f32_16x16x32_bf16 v[72:75], v[166:169], v[182:185], v[72:75]
	v_mfma_f32_16x16x32_bf16 v[48:51], v[158:161], v[190:193], v[48:51]
	v_mfma_f32_16x16x32_bf16 v[40:43], v[166:169], v[190:193], v[40:43]
	v_mfma_f32_16x16x32_bf16 v[16:19], v[158:161], v[198:201], v[16:19]
	v_mfma_f32_16x16x32_bf16 v[8:11], v[166:169], v[198:201], v[8:11]
	v_mfma_f32_16x16x32_bf16 v[112:115], v[162:165], v[178:181], v[112:115]
	v_mfma_f32_16x16x32_bf16 v[104:107], v[170:173], v[178:181], v[104:107]
	v_mfma_f32_16x16x32_bf16 v[80:83], v[162:165], v[186:189], v[80:83]
	v_mfma_f32_16x16x32_bf16 v[72:75], v[170:173], v[186:189], v[72:75]
	v_mfma_f32_16x16x32_bf16 v[48:51], v[162:165], v[194:197], v[48:51]
	v_mfma_f32_16x16x32_bf16 v[40:43], v[170:173], v[194:197], v[40:43]
	v_mfma_f32_16x16x32_bf16 v[16:19], v[162:165], v[202:205], v[16:19]
	v_mfma_f32_16x16x32_bf16 v[8:11], v[170:173], v[202:205], v[8:11]
	s_setprio 0
	s_waitcnt vmcnt(8)
	s_barrier
	s_mov_b32 m0, s82
	ds_read_b128 v[174:177], v140 offset:16384
	ds_read_b128 v[178:181], v140 offset:17408
	ds_read_b128 v[182:185], v140 offset:18432
	ds_read_b128 v[186:189], v140 offset:19456
	ds_read_b128 v[190:193], v140 offset:20480
	ds_read_b128 v[194:197], v140 offset:21504
	ds_read_b128 v[198:201], v140 offset:22528
	ds_read_b128 v[202:205], v140 offset:23552
	v_mov_b32_e32 v133, v129
	global_load_lds_dwordx4 v244, s[60:61]
	v_mov_b32_e32 v207, v129
	s_mov_b32 m0, s83
	v_lshl_add_u64 v[208:209], s[60:61], 0, v[244:245]
	v_lshl_add_u64 v[210:211], s[60:61], 0, v[246:247]
	global_load_lds_dwordx4 v246, s[60:61]
	s_cselect_b32 s61, s47, s75
	s_cselect_b32 s60, s46, s64
	s_add_i32 s80, s73, s20
	s_mov_b32 m0, s80
	v_lshl_add_u64 v[212:213], s[60:61], 0, v[244:245]
	global_load_lds_dwordx4 v244, s[60:61]
	s_add_i32 m0, s80, 0x2000
	v_lshl_add_u64 v[214:215], s[60:61], 0, v[246:247]
	global_load_lds_dwordx4 v246, s[60:61]
	s_mov_b32 m0, s27
	v_lshl_add_u64 v[206:207], s[58:59], 0, v[240:241]
	global_load_lds_dwordx4 v240, s[58:59]
	s_mov_b32 m0, s33
	v_lshl_add_u64 v[216:217], s[58:59], 0, v[242:243]
	global_load_lds_dwordx4 v242, s[58:59]
	s_waitcnt lgkmcnt(0)
	s_barrier
	s_setprio 1
	s_waitcnt lgkmcnt(0)
	v_mfma_f32_16x16x32_bf16 v[116:119], v[142:145], v[174:177], v[116:119]
	v_mfma_f32_16x16x32_bf16 v[108:111], v[150:153], v[174:177], v[108:111]
	v_mfma_f32_16x16x32_bf16 v[84:87], v[142:145], v[182:185], v[84:87]
	v_mfma_f32_16x16x32_bf16 v[76:79], v[150:153], v[182:185], v[76:79]
	v_mfma_f32_16x16x32_bf16 v[52:55], v[142:145], v[190:193], v[52:55]
	v_mfma_f32_16x16x32_bf16 v[44:47], v[150:153], v[190:193], v[44:47]
	v_mfma_f32_16x16x32_bf16 v[20:23], v[142:145], v[198:201], v[20:23]
	v_mfma_f32_16x16x32_bf16 v[12:15], v[150:153], v[198:201], v[12:15]
	v_mfma_f32_16x16x32_bf16 v[116:119], v[146:149], v[178:181], v[116:119]
	v_mfma_f32_16x16x32_bf16 v[108:111], v[154:157], v[178:181], v[108:111]
	v_mfma_f32_16x16x32_bf16 v[84:87], v[146:149], v[186:189], v[84:87]
	v_mfma_f32_16x16x32_bf16 v[76:79], v[154:157], v[186:189], v[76:79]
	v_mfma_f32_16x16x32_bf16 v[52:55], v[146:149], v[194:197], v[52:55]
	v_mfma_f32_16x16x32_bf16 v[44:47], v[154:157], v[194:197], v[44:47]
	v_mfma_f32_16x16x32_bf16 v[20:23], v[146:149], v[202:205], v[20:23]
	v_mfma_f32_16x16x32_bf16 v[12:15], v[154:157], v[202:205], v[12:15]
	s_setprio 0
	s_setprio 1
	v_mfma_f32_16x16x32_bf16 v[100:103], v[158:161], v[174:177], v[100:103]
	v_mfma_f32_16x16x32_bf16 v[96:99], v[166:169], v[174:177], v[96:99]
	v_mfma_f32_16x16x32_bf16 v[68:71], v[158:161], v[182:185], v[68:71]
	v_mfma_f32_16x16x32_bf16 v[64:67], v[166:169], v[182:185], v[64:67]
	v_mfma_f32_16x16x32_bf16 v[36:39], v[158:161], v[190:193], v[36:39]
	v_mfma_f32_16x16x32_bf16 v[32:35], v[166:169], v[190:193], v[32:35]
	v_mfma_f32_16x16x32_bf16 v[4:7], v[158:161], v[198:201], v[4:7]
	v_mfma_f32_16x16x32_bf16 v[0:3], v[166:169], v[198:201], v[0:3]
	v_mfma_f32_16x16x32_bf16 v[100:103], v[162:165], v[178:181], v[100:103]
	v_mfma_f32_16x16x32_bf16 v[96:99], v[170:173], v[178:181], v[96:99]
	v_mfma_f32_16x16x32_bf16 v[68:71], v[162:165], v[186:189], v[68:71]
	v_mfma_f32_16x16x32_bf16 v[64:67], v[170:173], v[186:189], v[64:67]
	v_mfma_f32_16x16x32_bf16 v[36:39], v[162:165], v[194:197], v[36:39]
	v_mfma_f32_16x16x32_bf16 v[32:35], v[170:173], v[194:197], v[32:35]
	v_mfma_f32_16x16x32_bf16 v[4:7], v[162:165], v[202:205], v[4:7]
	v_mfma_f32_16x16x32_bf16 v[0:3], v[170:173], v[202:205], v[0:3]
	s_setprio 0
	s_waitcnt vmcnt(8)
	s_barrier
; #define G_STAGE(bufoff, gbase, voff) do { _Pragma("unroll") for (int _i = 0; _i < 2; ++_i) \
;         __builtin_amdgcn_global_load_lds((const unsigned*)((const char*)(gbase) + (voff)[_i]), (LAS unsigned*)(lds + (bufoff) + ldsw + _i * 8192), 16, 0, 0); } while (0)
; #define G_LDA(dst, b, h) do { _Pragma("unroll") for (int m = 0; m < 4; ++m) G_LD8(dst[m], lds + G_SA(b, h) + aoff + m * 2048); } while (0)
; #define G_LDB(dst, b, h) do { _Pragma("unroll") for (int n = 0; n < 2; ++n) G_LD8(dst[n], lds + G_SB(b, h) + boff + n * 2048); } while (0)
; #define G_WAIT_V(n) asm volatile("s_waitcnt vmcnt(" #n ")" ::: "memory")
; #define G_WAIT_L(n) asm volatile("s_waitcnt lgkmcnt(" #n ")" ::: "memory")
; #define G_BAR __builtin_amdgcn_s_barrier()
; #define G_SCHED __builtin_amdgcn_sched_barrier(0)
;     ...
;             G_LDB(B0, 1, 0); G_LDB(B1, 1, 1); G_SCHED; G_LDA(At, 1, 0); G_STAGE(G_SA(0, 1), a12, vA1);
;             G_WAIT_L(0); G_BAR; G_MMA(0, 0, At, B0); G_MMA(0, 1, At, B1); G_WAIT_V(8); G_BAR; G_SCHED;
	s_add_i32 s58, 0, 0x18000
	v_add_u32_e32 v131, s58, v137
	s_add_i32 s59, 0, 0x1c000
	ds_read_b128 v[142:145], v131
	ds_read_b128 v[146:149], v131 offset:1024
	ds_read_b128 v[150:153], v131 offset:2048
	ds_read_b128 v[154:157], v131 offset:3072
	v_add_u32_e32 v131, s59, v137
	ds_read_b128 v[158:161], v131
	ds_read_b128 v[162:165], v131 offset:1024
	ds_read_b128 v[166:169], v131 offset:2048
	ds_read_b128 v[170:173], v131 offset:3072
	s_mov_b32 m0, s66
	ds_read_b128 v[174:177], v140 offset:32768
	ds_read_b128 v[178:181], v140 offset:33792
	ds_read_b128 v[182:185], v140 offset:34816
	ds_read_b128 v[186:189], v140 offset:35840
	ds_read_b128 v[190:193], v140 offset:36864
	ds_read_b128 v[194:197], v140 offset:37888
	ds_read_b128 v[198:201], v140 offset:38912
	ds_read_b128 v[202:205], v140 offset:39936
	global_load_lds_dwordx4 v240, s[56:57]
	s_mov_b32 m0, s67
	s_nop 0
	global_load_lds_dwordx4 v242, s[56:57]
	s_waitcnt lgkmcnt(0)
	s_barrier
	s_setprio 1
	s_waitcnt lgkmcnt(0)
	v_mfma_f32_16x16x32_bf16 v[124:127], v[142:145], v[174:177], v[124:127]
	v_mfma_f32_16x16x32_bf16 v[120:123], v[150:153], v[174:177], v[120:123]
	v_mfma_f32_16x16x32_bf16 v[92:95], v[142:145], v[182:185], v[92:95]
	v_mfma_f32_16x16x32_bf16 v[88:91], v[150:153], v[182:185], v[88:91]
	v_mfma_f32_16x16x32_bf16 v[60:63], v[142:145], v[190:193], v[60:63]
	v_mfma_f32_16x16x32_bf16 v[56:59], v[150:153], v[190:193], v[56:59]
	v_mfma_f32_16x16x32_bf16 v[28:31], v[142:145], v[198:201], v[28:31]
	v_mfma_f32_16x16x32_bf16 v[24:27], v[150:153], v[198:201], v[24:27]
	v_mfma_f32_16x16x32_bf16 v[124:127], v[146:149], v[178:181], v[124:127]
	v_mfma_f32_16x16x32_bf16 v[120:123], v[154:157], v[178:181], v[120:123]
	v_mfma_f32_16x16x32_bf16 v[92:95], v[146:149], v[186:189], v[92:95]
	v_mfma_f32_16x16x32_bf16 v[88:91], v[154:157], v[186:189], v[88:91]
	v_mfma_f32_16x16x32_bf16 v[60:63], v[146:149], v[194:197], v[60:63]
	v_mfma_f32_16x16x32_bf16 v[56:59], v[154:157], v[194:197], v[56:59]
	v_mfma_f32_16x16x32_bf16 v[28:31], v[146:149], v[202:205], v[28:31]
	v_mfma_f32_16x16x32_bf16 v[24:27], v[154:157], v[202:205], v[24:27]
	s_setprio 0
	s_setprio 1
	v_mfma_f32_16x16x32_bf16 v[112:115], v[158:161], v[174:177], v[112:115]
	v_mfma_f32_16x16x32_bf16 v[104:107], v[166:169], v[174:177], v[104:107]
	v_mfma_f32_16x16x32_bf16 v[80:83], v[158:161], v[182:185], v[80:83]
	v_mfma_f32_16x16x32_bf16 v[72:75], v[166:169], v[182:185], v[72:75]
	v_mfma_f32_16x16x32_bf16 v[48:51], v[158:161], v[190:193], v[48:51]
	v_mfma_f32_16x16x32_bf16 v[40:43], v[166:169], v[190:193], v[40:43]
	v_mfma_f32_16x16x32_bf16 v[16:19], v[158:161], v[198:201], v[16:19]
	v_mfma_f32_16x16x32_bf16 v[8:11], v[166:169], v[198:201], v[8:11]
	v_mfma_f32_16x16x32_bf16 v[112:115], v[162:165], v[178:181], v[112:115]
	v_mfma_f32_16x16x32_bf16 v[104:107], v[170:173], v[178:181], v[104:107]
	v_mfma_f32_16x16x32_bf16 v[80:83], v[162:165], v[186:189], v[80:83]
	v_mfma_f32_16x16x32_bf16 v[72:75], v[170:173], v[186:189], v[72:75]
	v_mfma_f32_16x16x32_bf16 v[48:51], v[162:165], v[194:197], v[48:51]
	v_mfma_f32_16x16x32_bf16 v[40:43], v[170:173], v[194:197], v[40:43]
	v_mfma_f32_16x16x32_bf16 v[16:19], v[162:165], v[202:205], v[16:19]
	v_mfma_f32_16x16x32_bf16 v[8:11], v[170:173], v[202:205], v[8:11]
	s_setprio 0
	s_waitcnt vmcnt(8)
	s_barrier
; #define G_STAGE(bufoff, gbase, voff) do { _Pragma("unroll") for (int _i = 0; _i < 2; ++_i) \
;         __builtin_amdgcn_global_load_lds((const unsigned*)((const char*)(gbase) + (voff)[_i]), (LAS unsigned*)(lds + (bufoff) + ldsw + _i * 8192), 16, 0, 0); } while (0)
; #define G_LDA(dst, b, h) do { _Pragma("unroll") for (int m = 0; m < 4; ++m) G_LD8(dst[m], lds + G_SA(b, h) + aoff + m * 2048); } while (0)
; #define G_WAIT_V(n) asm volatile("s_waitcnt vmcnt(" #n ")" ::: "memory")
; #define G_WAIT_L(n) asm volatile("s_waitcnt lgkmcnt(" #n ")" ::: "memory")
; #define G_BAR __builtin_amdgcn_s_barrier()
; #define G_SCHED __builtin_amdgcn_sched_barrier(0)
;     ...
;             G_LDA(At, 1, 1); G_STAGE(G_SB(1, 0), b02 + kstep, voffB); G_STAGE(G_SB(1, 1), b12 + kstep, voffB); G_STAGE(G_SA(1, 0), a02 + kstep, vA0);
;             G_WAIT_L(0); G_BAR; G_MMA(1, 0, At, B0); G_MMA(1, 1, At, B1); G_WAIT_V(8); G_BAR; G_SCHED;
;         }
	s_add_i32 s56, s58, s20
	v_lshl_add_u64 v[202:203], v[208:209], 0, s[40:41]
	s_mov_b32 m0, s56
	ds_read_b128 v[130:133], v140 offset:49152
	ds_read_b128 v[174:177], v140 offset:50176
	ds_read_b128 v[178:181], v140 offset:51200
	ds_read_b128 v[182:185], v140 offset:52224
	ds_read_b128 v[186:189], v140 offset:53248
	ds_read_b128 v[190:193], v140 offset:54272
	ds_read_b128 v[194:197], v140 offset:55296
	ds_read_b128 v[198:201], v140 offset:56320
	global_load_lds_dwordx4 v[202:203], off
	v_lshl_add_u64 v[202:203], v[210:211], 0, s[40:41]
	s_add_i32 m0, s56, 0x2000
	s_add_i32 s56, s59, s20
	global_load_lds_dwordx4 v[202:203], off
	v_lshl_add_u64 v[202:203], v[212:213], 0, s[40:41]
	s_mov_b32 m0, s56
	s_nop 0
	global_load_lds_dwordx4 v[202:203], off
	v_lshl_add_u64 v[202:203], v[214:215], 0, s[40:41]
	s_add_i32 m0, s56, 0x2000
	s_nop 0
	global_load_lds_dwordx4 v[202:203], off
	v_lshl_add_u64 v[202:203], v[206:207], 0, s[40:41]
	s_mov_b32 m0, s69
	s_nop 0
	global_load_lds_dwordx4 v[202:203], off
	v_lshl_add_u64 v[202:203], v[216:217], 0, s[40:41]
	s_mov_b32 m0, s70
	s_nop 0
	global_load_lds_dwordx4 v[202:203], off
	s_waitcnt lgkmcnt(0)
	s_barrier
	s_setprio 1
	s_waitcnt lgkmcnt(0)
	v_mfma_f32_16x16x32_bf16 v[116:119], v[142:145], v[130:133], v[116:119]
	v_mfma_f32_16x16x32_bf16 v[108:111], v[150:153], v[130:133], v[108:111]
	v_mfma_f32_16x16x32_bf16 v[84:87], v[142:145], v[178:181], v[84:87]
	v_mfma_f32_16x16x32_bf16 v[76:79], v[150:153], v[178:181], v[76:79]
	v_mfma_f32_16x16x32_bf16 v[52:55], v[142:145], v[186:189], v[52:55]
	v_mfma_f32_16x16x32_bf16 v[44:47], v[150:153], v[186:189], v[44:47]
	v_mfma_f32_16x16x32_bf16 v[20:23], v[142:145], v[194:197], v[20:23]
	v_mfma_f32_16x16x32_bf16 v[12:15], v[150:153], v[194:197], v[12:15]
	v_mfma_f32_16x16x32_bf16 v[116:119], v[146:149], v[174:177], v[116:119]
	v_mfma_f32_16x16x32_bf16 v[108:111], v[154:157], v[174:177], v[108:111]
	v_mfma_f32_16x16x32_bf16 v[84:87], v[146:149], v[182:185], v[84:87]
	v_mfma_f32_16x16x32_bf16 v[76:79], v[154:157], v[182:185], v[76:79]
	v_mfma_f32_16x16x32_bf16 v[52:55], v[146:149], v[190:193], v[52:55]
	v_mfma_f32_16x16x32_bf16 v[44:47], v[154:157], v[190:193], v[44:47]
	v_mfma_f32_16x16x32_bf16 v[20:23], v[146:149], v[198:201], v[20:23]
	v_mfma_f32_16x16x32_bf16 v[12:15], v[154:157], v[198:201], v[12:15]
	s_setprio 0
	s_setprio 1
	v_mfma_f32_16x16x32_bf16 v[100:103], v[158:161], v[130:133], v[100:103]
	v_mfma_f32_16x16x32_bf16 v[96:99], v[166:169], v[130:133], v[96:99]
	v_mfma_f32_16x16x32_bf16 v[68:71], v[158:161], v[178:181], v[68:71]
	v_mfma_f32_16x16x32_bf16 v[64:67], v[166:169], v[178:181], v[64:67]
	v_mfma_f32_16x16x32_bf16 v[36:39], v[158:161], v[186:189], v[36:39]
	v_mfma_f32_16x16x32_bf16 v[32:35], v[166:169], v[186:189], v[32:35]
	v_mfma_f32_16x16x32_bf16 v[4:7], v[158:161], v[194:197], v[4:7]
	v_mfma_f32_16x16x32_bf16 v[0:3], v[166:169], v[194:197], v[0:3]
	v_mfma_f32_16x16x32_bf16 v[100:103], v[162:165], v[174:177], v[100:103]
	v_mfma_f32_16x16x32_bf16 v[96:99], v[170:173], v[174:177], v[96:99]
	v_mfma_f32_16x16x32_bf16 v[68:71], v[162:165], v[182:185], v[68:71]
	v_mfma_f32_16x16x32_bf16 v[64:67], v[170:173], v[182:185], v[64:67]
	v_mfma_f32_16x16x32_bf16 v[36:39], v[162:165], v[190:193], v[36:39]
	v_mfma_f32_16x16x32_bf16 v[32:35], v[170:173], v[190:193], v[32:35]
	v_mfma_f32_16x16x32_bf16 v[4:7], v[162:165], v[198:201], v[4:7]
	v_mfma_f32_16x16x32_bf16 v[0:3], v[170:173], v[198:201], v[0:3]
	s_setprio 0
	s_waitcnt vmcnt(8)
	s_barrier
	s_add_u32 s62, s62, 0x100
	s_addc_u32 s63, s63, 0
	s_add_u32 s64, s64, 0x100
	s_addc_u32 s75, s75, 0
	s_add_u32 s77, s77, 0x100
	s_addc_u32 s78, s78, 0
	s_add_u32 s54, s54, 0x100
	s_addc_u32 s55, s55, 0
	s_cmp_ge_i32 s79, s0
	s_mov_b32 s56, s79
	s_cbranch_scc0 .LBB0_522
	v_readlane_b32 s78, v255, 11
	v_readlane_b32 s79, v255, 13
	s_and_b64 vcc, exec, s[42:43]
	s_cbranch_vccz .LBB0_525

; __device__ __forceinline__ int lane_id() { int l; asm volatile("v_mbcnt_lo_u32_b32 %0, -1, 0\n\tv_mbcnt_hi_u32_b32 %0, -1, %0" : "=v"(l)); return l; }
; #define G_STAGE(bufoff, gbase, voff) do { _Pragma("unroll") for (int _i = 0; _i < 2; ++_i) \
;         __builtin_amdgcn_global_load_lds((const unsigned*)((const char*)(gbase) + (voff)[_i]), (LAS unsigned*)(lds + (bufoff) + ldsw + _i * 8192), 16, 0, 0); } while (0)
; #define G_LDA(dst, b, h) do { _Pragma("unroll") for (int m = 0; m < 4; ++m) G_LD8(dst[m], lds + G_SA(b, h) + aoff + m * 2048); } while (0)
; #define G_LDB(dst, b, h) do { _Pragma("unroll") for (int n = 0; n < 2; ++n) G_LD8(dst[n], lds + G_SB(b, h) + boff + n * 2048); } while (0)
; #define G_SCHED __builtin_amdgcn_sched_barrier(0)
;     ...
;         for (int t = 0; t < nt; t += 2) {
;             const bool last = (t == nt - 2);
;             { const int tz_ = wid * 64 + lane_id();
; #pragma unroll
;               for (int i = 0; i < 2; ++i) { int R, C; stage_rc(tz_ * 16 + i * 8192, R, C); const int Rb = Epi::PERM ? ((R & ~31) + perm32(R & 31)) : R;
;                   voffA[i] = (unsigned)(R * S.multA * S.pitchA + C) * 2u; voffB[i] = (unsigned)(Rb * S.multB * S.pitchB + C) * 2u; } }
;             if constexpr (GATHER) asm volatile("" : "+v"(gc0[0]), "+v"(gc0[1]), "+v"(gc1[0]), "+v"(gc1[1]));
;             if constexpr (PREF) { if (t == nt - 4) S.prefetch(nxt, lds); }
;             const char* a11 = cur.a1 + (size_t)(t + 1) * kstep;
;             const char* a02 = last ? nxt.a0 : cur.a0 + (size_t)(t + 2) * kstep; const char* a12 = last ? nxt.a1 : cur.a1 + (size_t)(t + 2) * kstep;
;             const char* b02 = last ? nxt.b0 : cur.b0 + (size_t)(t + 2) * kstep; const char* b12 = last ? nxt.b1 : cur.b1 + (size_t)(t + 2) * kstep;
;             G_LDB(B0, 0, 0); G_LDB(B1, 0, 1); G_SCHED; G_LDA(At, 0, 0); G_STAGE(G_SA(1, 1), a11, vA1);
;     ...
;         for (int a = 0; a < 2; ++a)
; #pragma unroll
;             for (int b = 0; b < 2; ++b)
; #pragma unroll
;                 for (int m = 0; m < 4; ++m)
; #pragma unroll
;                     for (int n = 0; n < 2; ++n) acc[a][b][m][n] = (acc_t){0, 0, 0, 0};
;         cur = nxt; ++ui;
.LBB0_548:
	s_add_u32 s41, s62, 0x100
	s_addc_u32 s53, s63, 0
	s_add_u32 s55, s60, 0x100
	s_addc_u32 s64, s61, 0
	s_add_u32 s65, s58, 0x100
	s_addc_u32 s79, s59, 0
	s_add_u32 s56, s56, 0x80
	v_mov_b32_e32 v0, 0
	s_addc_u32 s57, s57, 0
	s_mov_b32 s58, 0
	v_mov_b32_e32 v1, v0
	v_mov_b32_e32 v2, v0
	v_mov_b32_e32 v3, v0
	v_mov_b32_e32 v4, v0
	v_mov_b32_e32 v5, v0
	v_mov_b32_e32 v6, v0
	v_mov_b32_e32 v7, v0
	v_mov_b32_e32 v16, v0
	v_mov_b32_e32 v17, v0
	v_mov_b32_e32 v18, v0
	v_mov_b32_e32 v19, v0
	v_mov_b32_e32 v20, v0
	v_mov_b32_e32 v21, v0
	v_mov_b32_e32 v22, v0
	v_mov_b32_e32 v23, v0
	v_mov_b32_e32 v32, v0
	v_mov_b32_e32 v33, v0
	v_mov_b32_e32 v34, v0
	v_mov_b32_e32 v35, v0
	v_mov_b32_e32 v36, v0
	v_mov_b32_e32 v37, v0
	v_mov_b32_e32 v38, v0
	v_mov_b32_e32 v39, v0
	v_mov_b32_e32 v48, v0
	v_mov_b32_e32 v49, v0
	v_mov_b32_e32 v50, v0
	v_mov_b32_e32 v51, v0
	v_mov_b32_e32 v52, v0
	v_mov_b32_e32 v53, v0
	v_mov_b32_e32 v54, v0
	v_mov_b32_e32 v55, v0
	v_mov_b32_e32 v8, v0
	v_mov_b32_e32 v9, v0
	v_mov_b32_e32 v10, v0
	v_mov_b32_e32 v11, v0
	v_mov_b32_e32 v12, v0
	v_mov_b32_e32 v13, v0
	v_mov_b32_e32 v14, v0
	v_mov_b32_e32 v15, v0
	v_mov_b32_e32 v24, v0
	v_mov_b32_e32 v25, v0
	v_mov_b32_e32 v26, v0
	v_mov_b32_e32 v27, v0
	v_mov_b32_e32 v28, v0
	v_mov_b32_e32 v29, v0
	v_mov_b32_e32 v30, v0
	v_mov_b32_e32 v31, v0
	v_mov_b32_e32 v40, v0
	v_mov_b32_e32 v41, v0
	v_mov_b32_e32 v42, v0
	v_mov_b32_e32 v43, v0
	v_mov_b32_e32 v44, v0
	v_mov_b32_e32 v45, v0
	v_mov_b32_e32 v46, v0
	v_mov_b32_e32 v47, v0
	v_mov_b32_e32 v56, v0
	v_mov_b32_e32 v57, v0
	v_mov_b32_e32 v58, v0
	v_mov_b32_e32 v59, v0
	v_mov_b32_e32 v60, v0
	v_mov_b32_e32 v61, v0
	v_mov_b32_e32 v62, v0
	v_mov_b32_e32 v63, v0
	v_mov_b32_e32 v64, v0
	v_mov_b32_e32 v65, v0
	v_mov_b32_e32 v66, v0
	v_mov_b32_e32 v67, v0
	v_mov_b32_e32 v68, v0
	v_mov_b32_e32 v69, v0
	v_mov_b32_e32 v70, v0
	v_mov_b32_e32 v71, v0
	v_mov_b32_e32 v80, v0
	v_mov_b32_e32 v81, v0
	v_mov_b32_e32 v82, v0
	v_mov_b32_e32 v83, v0
	v_mov_b32_e32 v84, v0
	v_mov_b32_e32 v85, v0
	v_mov_b32_e32 v86, v0
	v_mov_b32_e32 v87, v0
	v_mov_b32_e32 v96, v0
	v_mov_b32_e32 v97, v0
	v_mov_b32_e32 v98, v0
	v_mov_b32_e32 v99, v0
	v_mov_b32_e32 v100, v0
	v_mov_b32_e32 v101, v0
	v_mov_b32_e32 v102, v0
	v_mov_b32_e32 v103, v0
	v_mov_b32_e32 v112, v0
	v_mov_b32_e32 v113, v0
	v_mov_b32_e32 v114, v0
	v_mov_b32_e32 v115, v0
	v_mov_b32_e32 v116, v0
	v_mov_b32_e32 v117, v0
	v_mov_b32_e32 v118, v0
	v_mov_b32_e32 v119, v0
	v_mov_b32_e32 v72, v0
	v_mov_b32_e32 v73, v0
	v_mov_b32_e32 v74, v0
	v_mov_b32_e32 v75, v0
	v_mov_b32_e32 v76, v0
	v_mov_b32_e32 v77, v0
	v_mov_b32_e32 v78, v0
	v_mov_b32_e32 v79, v0
	v_mov_b32_e32 v88, v0
	v_mov_b32_e32 v89, v0
	v_mov_b32_e32 v90, v0
	v_mov_b32_e32 v91, v0
	v_mov_b32_e32 v92, v0
	v_mov_b32_e32 v93, v0
	v_mov_b32_e32 v94, v0
	v_mov_b32_e32 v95, v0
	v_mov_b32_e32 v104, v0
	v_mov_b32_e32 v105, v0
	v_mov_b32_e32 v106, v0
	v_mov_b32_e32 v107, v0
	v_mov_b32_e32 v108, v0
	v_mov_b32_e32 v109, v0
	v_mov_b32_e32 v110, v0
	v_mov_b32_e32 v111, v0
	v_mov_b32_e32 v120, v0
	v_mov_b32_e32 v121, v0
	v_mov_b32_e32 v122, v0
	v_mov_b32_e32 v123, v0
	v_mov_b32_e32 v124, v0
	v_mov_b32_e32 v125, v0
	v_mov_b32_e32 v126, v0
	v_mov_b32_e32 v127, v0
	v_mbcnt_lo_u32_b32 v248, -1, 0
	v_mbcnt_hi_u32_b32 v248, -1, v248
	v_mov_b32_e32 v249, s88
	v_lshrrev_b32_e32 v249, 6, v249
	v_and_b32_e32 v250, 3, v248
	v_lshlrev_b32_e32 v250, 4, v250
	v_and_b32_e32 v251, 32, v248
	v_xor_b32_e32 v250, v250, v251
	v_and_b32_e32 v251, 1, v249
	v_lshl_add_u32 v250, v251, 6, v250
	v_lshrrev_b32_e32 v251, 1, v249
	v_lshrrev_b32_e32 v252, 2, v248
	v_lshl_add_u32 v251, v251, 4, v252
	v_mov_b32_e32 v253, 0x800
	v_mad_u32_u24 v240, v251, v253, v250
	v_add_u32_e32 v242, 0x20000, v240
	v_lshrrev_b32_e32 v251, 2, v249
	v_lshlrev_b32_e32 v251, 5, v251
	v_lshrrev_b32_e32 v252, 4, v248
	v_lshl_add_u32 v251, v252, 3, v251
	v_bfe_u32 v252, v249, 1, 1
	v_lshl_add_u32 v251, v252, 2, v251
	v_bfe_u32 v252, v248, 2, 2
	v_add_u32_e32 v251, v251, v252
	v_mov_b32_e32 v253, 0x800
	v_mad_u32_u24 v244, v251, v253, v250
	v_add_u32_e32 v246, 0x20000, v244
	v_mov_b32_e32 v241, 0
	v_mov_b32_e32 v243, 0
	v_mov_b32_e32 v245, 0
	v_mov_b32_e32 v247, 0
.LBB0_549:
	s_add_i32 s80, s58, 2
	ds_read_b128 v[130:133], v138
	ds_read_b128 v[142:145], v138 offset:1024
	ds_read_b128 v[146:149], v138 offset:2048
	ds_read_b128 v[150:153], v138 offset:3072
	ds_read_b128 v[154:157], v139
	ds_read_b128 v[158:161], v139 offset:1024
	ds_read_b128 v[162:165], v139 offset:2048
	ds_read_b128 v[166:169], v139 offset:3072
	s_add_u32 s81, s56, 0x80
	s_addc_u32 s59, s57, 0
	s_add_i32 s83, s75, s20
	s_add_i32 m0, s67, 0xc000
	s_add_i32 s82, s67, 0xe000
	s_add_i32 s84, s83, 0x2000
	s_cmp_eq_u32 s74, s58
	s_cselect_b32 s58, s44, s81
	s_cselect_b32 s61, s43, s79
	s_cselect_b32 s60, s42, s65
	s_cselect_b32 s63, s47, s53
	s_cselect_b32 s62, s46, s41
	s_cselect_b32 s59, s45, s59
	ds_read_b128 v[170:173], v140
	ds_read_b128 v[174:177], v140 offset:1024
	ds_read_b128 v[178:181], v140 offset:2048
	ds_read_b128 v[182:185], v140 offset:3072
	ds_read_b128 v[186:189], v140 offset:4096
	ds_read_b128 v[190:193], v140 offset:5120
	ds_read_b128 v[194:197], v140 offset:6144
	ds_read_b128 v[198:201], v140 offset:7168
	global_load_lds_dwordx4 v240, s[56:57]
	s_mov_b32 m0, s82
	v_mov_b32_e32 v205, v129
	global_load_lds_dwordx4 v242, s[56:57]
	s_waitcnt lgkmcnt(0)
	s_barrier
; #define G_STAGE(bufoff, gbase, voff) do { _Pragma("unroll") for (int _i = 0; _i < 2; ++_i) \
;         __builtin_amdgcn_global_load_lds((const unsigned*)((const char*)(gbase) + (voff)[_i]), (LAS unsigned*)(lds + (bufoff) + ldsw + _i * 8192), 16, 0, 0); } while (0)
; #define G_LDA(dst, b, h) do { _Pragma("unroll") for (int m = 0; m < 4; ++m) G_LD8(dst[m], lds + G_SA(b, h) + aoff + m * 2048); } while (0)
; #define G_WAIT_V(n) asm volatile("s_waitcnt vmcnt(" #n ")" ::: "memory")
; #define G_WAIT_L(n) asm volatile("s_waitcnt lgkmcnt(" #n ")" ::: "memory")
; #define G_BAR __builtin_amdgcn_s_barrier()
; #define G_SCHED __builtin_amdgcn_sched_barrier(0)
;     ...
;             G_WAIT_L(0); G_BAR; G_MMA(0, 0, At, B0); G_MMA(0, 1, At, B1); G_WAIT_V(8); G_BAR; G_SCHED;
;             G_LDA(At, 0, 1); G_STAGE(G_SB(0, 0), b02, voffB); G_STAGE(G_SB(0, 1), b12, voffB); G_STAGE(G_SA(0, 0), a02, vA0);
;             G_WAIT_L(0); G_BAR; G_MMA(1, 0, At, B0); G_MMA(1, 1, At, B1); G_WAIT_V(8); G_BAR; G_SCHED;
	s_setprio 1
	s_waitcnt lgkmcnt(0)
	v_mfma_f32_16x16x32_bf16 v[124:127], v[130:133], v[170:173], v[124:127]
	v_mfma_f32_16x16x32_bf16 v[120:123], v[146:149], v[170:173], v[120:123]
	v_mfma_f32_16x16x32_bf16 v[108:111], v[130:133], v[178:181], v[108:111]
	v_mfma_f32_16x16x32_bf16 v[104:107], v[146:149], v[178:181], v[104:107]
	v_mfma_f32_16x16x32_bf16 v[92:95], v[130:133], v[186:189], v[92:95]
	v_mfma_f32_16x16x32_bf16 v[88:91], v[146:149], v[186:189], v[88:91]
	v_mfma_f32_16x16x32_bf16 v[76:79], v[130:133], v[194:197], v[76:79]
	v_mfma_f32_16x16x32_bf16 v[72:75], v[146:149], v[194:197], v[72:75]
	v_mfma_f32_16x16x32_bf16 v[124:127], v[142:145], v[174:177], v[124:127]
	v_mfma_f32_16x16x32_bf16 v[120:123], v[150:153], v[174:177], v[120:123]
	v_mfma_f32_16x16x32_bf16 v[108:111], v[142:145], v[182:185], v[108:111]
	v_mfma_f32_16x16x32_bf16 v[104:107], v[150:153], v[182:185], v[104:107]
	v_mfma_f32_16x16x32_bf16 v[92:95], v[142:145], v[190:193], v[92:95]
	v_mfma_f32_16x16x32_bf16 v[88:91], v[150:153], v[190:193], v[88:91]
	v_mfma_f32_16x16x32_bf16 v[76:79], v[142:145], v[198:201], v[76:79]
	v_mfma_f32_16x16x32_bf16 v[72:75], v[150:153], v[198:201], v[72:75]
	s_setprio 0
	s_setprio 1
	v_mfma_f32_16x16x32_bf16 v[116:119], v[154:157], v[170:173], v[116:119]
	v_mfma_f32_16x16x32_bf16 v[112:115], v[162:165], v[170:173], v[112:115]
	v_mfma_f32_16x16x32_bf16 v[100:103], v[154:157], v[178:181], v[100:103]
	v_mfma_f32_16x16x32_bf16 v[96:99], v[162:165], v[178:181], v[96:99]
	v_mfma_f32_16x16x32_bf16 v[84:87], v[154:157], v[186:189], v[84:87]
	v_mfma_f32_16x16x32_bf16 v[80:83], v[162:165], v[186:189], v[80:83]
	v_mfma_f32_16x16x32_bf16 v[68:71], v[154:157], v[194:197], v[68:71]
	v_mfma_f32_16x16x32_bf16 v[64:67], v[162:165], v[194:197], v[64:67]
	v_mfma_f32_16x16x32_bf16 v[116:119], v[158:161], v[174:177], v[116:119]
	v_mfma_f32_16x16x32_bf16 v[112:115], v[166:169], v[174:177], v[112:115]
	v_mfma_f32_16x16x32_bf16 v[100:103], v[158:161], v[182:185], v[100:103]
	v_mfma_f32_16x16x32_bf16 v[96:99], v[166:169], v[182:185], v[96:99]
	v_mfma_f32_16x16x32_bf16 v[84:87], v[158:161], v[190:193], v[84:87]
	v_mfma_f32_16x16x32_bf16 v[80:83], v[166:169], v[190:193], v[80:83]
	v_mfma_f32_16x16x32_bf16 v[68:71], v[158:161], v[198:201], v[68:71]
	v_mfma_f32_16x16x32_bf16 v[64:67], v[166:169], v[198:201], v[64:67]
	s_setprio 0
	s_waitcnt vmcnt(8)
	s_barrier
	s_mov_b32 m0, s83
	ds_read_b128 v[170:173], v140 offset:16384
	ds_read_b128 v[174:177], v140 offset:17408
	ds_read_b128 v[178:181], v140 offset:18432
	ds_read_b128 v[182:185], v140 offset:19456
	ds_read_b128 v[186:189], v140 offset:20480
	ds_read_b128 v[190:193], v140 offset:21504
	ds_read_b128 v[194:197], v140 offset:22528
	ds_read_b128 v[198:201], v140 offset:23552
	global_load_lds_dwordx4 v244, s[62:63]
	s_mov_b32 m0, s84
	s_cselect_b32 s83, s49, s64
	s_cselect_b32 s82, s48, s55
	s_add_i32 s81, s76, s20
	global_load_lds_dwordx4 v246, s[62:63]
	s_mov_b32 m0, s81
	v_mov_b32_e32 v203, v129
	global_load_lds_dwordx4 v244, s[82:83]
	s_add_i32 m0, s81, 0x2000
	v_mov_b32_e32 v207, v129
	global_load_lds_dwordx4 v246, s[82:83]
	s_mov_b32 m0, s67
	v_lshl_add_u64 v[208:209], s[62:63], 0, v[244:245]
	global_load_lds_dwordx4 v240, s[60:61]
	s_mov_b32 m0, s68
	v_lshl_add_u64 v[210:211], s[62:63], 0, v[246:247]
	global_load_lds_dwordx4 v242, s[60:61]
	s_waitcnt lgkmcnt(0)
	v_lshl_add_u64 v[202:203], s[82:83], 0, v[244:245]
	v_lshl_add_u64 v[206:207], s[82:83], 0, v[246:247]
	v_lshl_add_u64 v[212:213], s[60:61], 0, v[240:241]
	v_lshl_add_u64 v[214:215], s[60:61], 0, v[242:243]
	s_barrier
	s_setprio 1
	s_waitcnt lgkmcnt(0)
	v_mfma_f32_16x16x32_bf16 v[60:63], v[130:133], v[170:173], v[60:63]
	v_mfma_f32_16x16x32_bf16 v[56:59], v[146:149], v[170:173], v[56:59]
	v_mfma_f32_16x16x32_bf16 v[44:47], v[130:133], v[178:181], v[44:47]
	v_mfma_f32_16x16x32_bf16 v[40:43], v[146:149], v[178:181], v[40:43]
	v_mfma_f32_16x16x32_bf16 v[28:31], v[130:133], v[186:189], v[28:31]
	v_mfma_f32_16x16x32_bf16 v[24:27], v[146:149], v[186:189], v[24:27]
	v_mfma_f32_16x16x32_bf16 v[12:15], v[130:133], v[194:197], v[12:15]
	v_mfma_f32_16x16x32_bf16 v[8:11], v[146:149], v[194:197], v[8:11]
	v_mfma_f32_16x16x32_bf16 v[60:63], v[142:145], v[174:177], v[60:63]
	v_mfma_f32_16x16x32_bf16 v[56:59], v[150:153], v[174:177], v[56:59]
	v_mfma_f32_16x16x32_bf16 v[44:47], v[142:145], v[182:185], v[44:47]
	v_mfma_f32_16x16x32_bf16 v[40:43], v[150:153], v[182:185], v[40:43]
	v_mfma_f32_16x16x32_bf16 v[28:31], v[142:145], v[190:193], v[28:31]
	v_mfma_f32_16x16x32_bf16 v[24:27], v[150:153], v[190:193], v[24:27]
	v_mfma_f32_16x16x32_bf16 v[12:15], v[142:145], v[198:201], v[12:15]
	v_mfma_f32_16x16x32_bf16 v[8:11], v[150:153], v[198:201], v[8:11]
	s_setprio 0
	s_setprio 1
	v_mfma_f32_16x16x32_bf16 v[52:55], v[154:157], v[170:173], v[52:55]
	v_mfma_f32_16x16x32_bf16 v[48:51], v[162:165], v[170:173], v[48:51]
	v_mfma_f32_16x16x32_bf16 v[36:39], v[154:157], v[178:181], v[36:39]
	v_mfma_f32_16x16x32_bf16 v[32:35], v[162:165], v[178:181], v[32:35]
	v_mfma_f32_16x16x32_bf16 v[20:23], v[154:157], v[186:189], v[20:23]
	v_mfma_f32_16x16x32_bf16 v[16:19], v[162:165], v[186:189], v[16:19]
	v_mfma_f32_16x16x32_bf16 v[4:7], v[154:157], v[194:197], v[4:7]
	v_mfma_f32_16x16x32_bf16 v[0:3], v[162:165], v[194:197], v[0:3]
	v_mfma_f32_16x16x32_bf16 v[52:55], v[158:161], v[174:177], v[52:55]
	v_mfma_f32_16x16x32_bf16 v[48:51], v[166:169], v[174:177], v[48:51]
	v_mfma_f32_16x16x32_bf16 v[36:39], v[158:161], v[182:185], v[36:39]
	v_mfma_f32_16x16x32_bf16 v[32:35], v[166:169], v[182:185], v[32:35]
	v_mfma_f32_16x16x32_bf16 v[20:23], v[158:161], v[190:193], v[20:23]
	v_mfma_f32_16x16x32_bf16 v[16:19], v[166:169], v[190:193], v[16:19]
	v_mfma_f32_16x16x32_bf16 v[4:7], v[158:161], v[198:201], v[4:7]
	v_mfma_f32_16x16x32_bf16 v[0:3], v[166:169], v[198:201], v[0:3]
	s_setprio 0
	s_waitcnt vmcnt(8)
	s_barrier
; #define G_STAGE(bufoff, gbase, voff) do { _Pragma("unroll") for (int _i = 0; _i < 2; ++_i) \
;         __builtin_amdgcn_global_load_lds((const unsigned*)((const char*)(gbase) + (voff)[_i]), (LAS unsigned*)(lds + (bufoff) + ldsw + _i * 8192), 16, 0, 0); } while (0)
; #define G_LDA(dst, b, h) do { _Pragma("unroll") for (int m = 0; m < 4; ++m) G_LD8(dst[m], lds + G_SA(b, h) + aoff + m * 2048); } while (0)
; #define G_LDB(dst, b, h) do { _Pragma("unroll") for (int n = 0; n < 2; ++n) G_LD8(dst[n], lds + G_SB(b, h) + boff + n * 2048); } while (0)
; #define G_WAIT_V(n) asm volatile("s_waitcnt vmcnt(" #n ")" ::: "memory")
; #define G_WAIT_L(n) asm volatile("s_waitcnt lgkmcnt(" #n ")" ::: "memory")
; #define G_BAR __builtin_amdgcn_s_barrier()
; #define G_SCHED __builtin_amdgcn_sched_barrier(0)
;     ...
;             G_LDB(B0, 1, 0); G_LDB(B1, 1, 1); G_SCHED; G_LDA(At, 1, 0); G_STAGE(G_SA(0, 1), a12, vA1);
;             G_WAIT_L(0); G_BAR; G_MMA(0, 0, At, B0); G_MMA(0, 1, At, B1); G_WAIT_V(8); G_BAR; G_SCHED;
	s_add_i32 s60, 0, 0x18000
	v_add_u32_e32 v141, s60, v137
	s_add_i32 s61, 0, 0x1c000
	ds_read_b128 v[130:133], v141
	ds_read_b128 v[142:145], v141 offset:1024
	ds_read_b128 v[146:149], v141 offset:2048
	ds_read_b128 v[150:153], v141 offset:3072
	v_add_u32_e32 v141, s61, v137
	ds_read_b128 v[154:157], v141
	ds_read_b128 v[158:161], v141 offset:1024
	ds_read_b128 v[162:165], v141 offset:2048
	ds_read_b128 v[166:169], v141 offset:3072
	s_mov_b32 m0, s69
	ds_read_b128 v[170:173], v140 offset:32768
	ds_read_b128 v[174:177], v140 offset:33792
	ds_read_b128 v[178:181], v140 offset:34816
	ds_read_b128 v[182:185], v140 offset:35840
	ds_read_b128 v[186:189], v140 offset:36864
	ds_read_b128 v[190:193], v140 offset:37888
	ds_read_b128 v[194:197], v140 offset:38912
	ds_read_b128 v[198:201], v140 offset:39936
	global_load_lds_dwordx4 v240, s[58:59]
	s_mov_b32 m0, s70
	s_nop 0
	global_load_lds_dwordx4 v242, s[58:59]
	s_waitcnt lgkmcnt(0)
	s_barrier
	s_setprio 1
	s_waitcnt lgkmcnt(0)
	v_mfma_f32_16x16x32_bf16 v[124:127], v[130:133], v[170:173], v[124:127]
	v_mfma_f32_16x16x32_bf16 v[120:123], v[146:149], v[170:173], v[120:123]
	v_mfma_f32_16x16x32_bf16 v[108:111], v[130:133], v[178:181], v[108:111]
	v_mfma_f32_16x16x32_bf16 v[104:107], v[146:149], v[178:181], v[104:107]
	v_mfma_f32_16x16x32_bf16 v[92:95], v[130:133], v[186:189], v[92:95]
	v_mfma_f32_16x16x32_bf16 v[88:91], v[146:149], v[186:189], v[88:91]
	v_mfma_f32_16x16x32_bf16 v[76:79], v[130:133], v[194:197], v[76:79]
	v_mfma_f32_16x16x32_bf16 v[72:75], v[146:149], v[194:197], v[72:75]
	v_mfma_f32_16x16x32_bf16 v[124:127], v[142:145], v[174:177], v[124:127]
	v_mfma_f32_16x16x32_bf16 v[120:123], v[150:153], v[174:177], v[120:123]
	v_mfma_f32_16x16x32_bf16 v[108:111], v[142:145], v[182:185], v[108:111]
	v_mfma_f32_16x16x32_bf16 v[104:107], v[150:153], v[182:185], v[104:107]
	v_mfma_f32_16x16x32_bf16 v[92:95], v[142:145], v[190:193], v[92:95]
	v_mfma_f32_16x16x32_bf16 v[88:91], v[150:153], v[190:193], v[88:91]
	v_mfma_f32_16x16x32_bf16 v[76:79], v[142:145], v[198:201], v[76:79]
	v_mfma_f32_16x16x32_bf16 v[72:75], v[150:153], v[198:201], v[72:75]
	s_setprio 0
	s_setprio 1
	v_mfma_f32_16x16x32_bf16 v[116:119], v[154:157], v[170:173], v[116:119]
	v_mfma_f32_16x16x32_bf16 v[112:115], v[162:165], v[170:173], v[112:115]
	v_mfma_f32_16x16x32_bf16 v[100:103], v[154:157], v[178:181], v[100:103]
	v_mfma_f32_16x16x32_bf16 v[96:99], v[162:165], v[178:181], v[96:99]
	v_mfma_f32_16x16x32_bf16 v[84:87], v[154:157], v[186:189], v[84:87]
	v_mfma_f32_16x16x32_bf16 v[80:83], v[162:165], v[186:189], v[80:83]
	v_mfma_f32_16x16x32_bf16 v[68:71], v[154:157], v[194:197], v[68:71]
	v_mfma_f32_16x16x32_bf16 v[64:67], v[162:165], v[194:197], v[64:67]
	v_mfma_f32_16x16x32_bf16 v[116:119], v[158:161], v[174:177], v[116:119]
	v_mfma_f32_16x16x32_bf16 v[112:115], v[166:169], v[174:177], v[112:115]
	v_mfma_f32_16x16x32_bf16 v[100:103], v[158:161], v[182:185], v[100:103]
	v_mfma_f32_16x16x32_bf16 v[96:99], v[166:169], v[182:185], v[96:99]
	v_mfma_f32_16x16x32_bf16 v[84:87], v[158:161], v[190:193], v[84:87]
	v_mfma_f32_16x16x32_bf16 v[80:83], v[166:169], v[190:193], v[80:83]
	v_mfma_f32_16x16x32_bf16 v[68:71], v[158:161], v[198:201], v[68:71]
	v_mfma_f32_16x16x32_bf16 v[64:67], v[166:169], v[198:201], v[64:67]
	s_setprio 0
	s_waitcnt vmcnt(8)
	s_barrier
; #define G_STAGE(bufoff, gbase, voff) do { _Pragma("unroll") for (int _i = 0; _i < 2; ++_i) \
;         __builtin_amdgcn_global_load_lds((const unsigned*)((const char*)(gbase) + (voff)[_i]), (LAS unsigned*)(lds + (bufoff) + ldsw + _i * 8192), 16, 0, 0); } while (0)
; #define G_LDA(dst, b, h) do { _Pragma("unroll") for (int m = 0; m < 4; ++m) G_LD8(dst[m], lds + G_SA(b, h) + aoff + m * 2048); } while (0)
; #define G_WAIT_V(n) asm volatile("s_waitcnt vmcnt(" #n ")" ::: "memory")
; #define G_WAIT_L(n) asm volatile("s_waitcnt lgkmcnt(" #n ")" ::: "memory")
; #define G_BAR __builtin_amdgcn_s_barrier()
; #define G_SCHED __builtin_amdgcn_sched_barrier(0)
;     ...
;             G_LDA(At, 1, 1); G_STAGE(G_SB(1, 0), b02 + kstep, voffB); G_STAGE(G_SB(1, 1), b12 + kstep, voffB); G_STAGE(G_SA(1, 0), a02 + kstep, vA0);
;             G_WAIT_L(0); G_BAR; G_MMA(1, 0, At, B0); G_MMA(1, 1, At, B1); G_WAIT_V(8); G_BAR; G_SCHED;
;         }
	s_add_i32 s58, s60, s20
	v_lshl_add_u64 v[204:205], v[208:209], 0, s[8:9]
	s_mov_b32 m0, s58
	ds_read_b128 v[170:173], v140 offset:49152
	ds_read_b128 v[174:177], v140 offset:50176
	ds_read_b128 v[178:181], v140 offset:51200
	ds_read_b128 v[182:185], v140 offset:52224
	ds_read_b128 v[186:189], v140 offset:53248
	ds_read_b128 v[190:193], v140 offset:54272
	ds_read_b128 v[194:197], v140 offset:55296
	ds_read_b128 v[198:201], v140 offset:56320
	global_load_lds_dwordx4 v[204:205], off
	v_lshl_add_u64 v[204:205], v[210:211], 0, s[8:9]
	s_add_i32 m0, s58, 0x2000
	s_add_i32 s58, s61, s20
	global_load_lds_dwordx4 v[204:205], off
	v_lshl_add_u64 v[202:203], v[202:203], 0, s[8:9]
	s_mov_b32 m0, s58
	s_nop 0
	global_load_lds_dwordx4 v[202:203], off
	v_lshl_add_u64 v[202:203], v[206:207], 0, s[8:9]
	s_add_i32 m0, s58, 0x2000
	s_nop 0
	global_load_lds_dwordx4 v[202:203], off
	v_lshl_add_u64 v[202:203], v[212:213], 0, s[8:9]
	s_mov_b32 m0, s72
	s_nop 0
	global_load_lds_dwordx4 v[202:203], off
	v_lshl_add_u64 v[202:203], v[214:215], 0, s[8:9]
	s_mov_b32 m0, s73
	s_nop 0
	global_load_lds_dwordx4 v[202:203], off
	s_waitcnt lgkmcnt(0)
	s_barrier
	s_setprio 1
	s_waitcnt lgkmcnt(0)
	v_mfma_f32_16x16x32_bf16 v[60:63], v[130:133], v[170:173], v[60:63]
	v_mfma_f32_16x16x32_bf16 v[56:59], v[146:149], v[170:173], v[56:59]
	v_mfma_f32_16x16x32_bf16 v[44:47], v[130:133], v[178:181], v[44:47]
	v_mfma_f32_16x16x32_bf16 v[40:43], v[146:149], v[178:181], v[40:43]
	v_mfma_f32_16x16x32_bf16 v[28:31], v[130:133], v[186:189], v[28:31]
	v_mfma_f32_16x16x32_bf16 v[24:27], v[146:149], v[186:189], v[24:27]
	v_mfma_f32_16x16x32_bf16 v[12:15], v[130:133], v[194:197], v[12:15]
	v_mfma_f32_16x16x32_bf16 v[8:11], v[146:149], v[194:197], v[8:11]
	v_mfma_f32_16x16x32_bf16 v[60:63], v[142:145], v[174:177], v[60:63]
	v_mfma_f32_16x16x32_bf16 v[56:59], v[150:153], v[174:177], v[56:59]
	v_mfma_f32_16x16x32_bf16 v[44:47], v[142:145], v[182:185], v[44:47]
	v_mfma_f32_16x16x32_bf16 v[40:43], v[150:153], v[182:185], v[40:43]
	v_mfma_f32_16x16x32_bf16 v[28:31], v[142:145], v[190:193], v[28:31]
	v_mfma_f32_16x16x32_bf16 v[24:27], v[150:153], v[190:193], v[24:27]
	v_mfma_f32_16x16x32_bf16 v[12:15], v[142:145], v[198:201], v[12:15]
	v_mfma_f32_16x16x32_bf16 v[8:11], v[150:153], v[198:201], v[8:11]
	s_setprio 0
	s_setprio 1
	v_mfma_f32_16x16x32_bf16 v[52:55], v[154:157], v[170:173], v[52:55]
	v_mfma_f32_16x16x32_bf16 v[48:51], v[162:165], v[170:173], v[48:51]
	v_mfma_f32_16x16x32_bf16 v[36:39], v[154:157], v[178:181], v[36:39]
	v_mfma_f32_16x16x32_bf16 v[32:35], v[162:165], v[178:181], v[32:35]
	v_mfma_f32_16x16x32_bf16 v[20:23], v[154:157], v[186:189], v[20:23]
	v_mfma_f32_16x16x32_bf16 v[16:19], v[162:165], v[186:189], v[16:19]
	v_mfma_f32_16x16x32_bf16 v[4:7], v[154:157], v[194:197], v[4:7]
	v_mfma_f32_16x16x32_bf16 v[0:3], v[162:165], v[194:197], v[0:3]
	v_mfma_f32_16x16x32_bf16 v[52:55], v[158:161], v[174:177], v[52:55]
	v_mfma_f32_16x16x32_bf16 v[48:51], v[166:169], v[174:177], v[48:51]
	v_mfma_f32_16x16x32_bf16 v[36:39], v[158:161], v[182:185], v[36:39]
	v_mfma_f32_16x16x32_bf16 v[32:35], v[166:169], v[182:185], v[32:35]
	v_mfma_f32_16x16x32_bf16 v[20:23], v[158:161], v[190:193], v[20:23]
	v_mfma_f32_16x16x32_bf16 v[16:19], v[166:169], v[190:193], v[16:19]
	v_mfma_f32_16x16x32_bf16 v[4:7], v[158:161], v[198:201], v[4:7]
	v_mfma_f32_16x16x32_bf16 v[0:3], v[166:169], v[198:201], v[0:3]
	s_setprio 0
	s_waitcnt vmcnt(8)
	s_barrier
	s_add_u32 s41, s41, 0x100
	s_addc_u32 s53, s53, 0
	s_add_u32 s55, s55, 0x100
	s_addc_u32 s64, s64, 0
	s_add_u32 s65, s65, 0x100
	s_addc_u32 s79, s79, 0
	s_add_u32 s56, s56, 0x100
	s_addc_u32 s57, s57, 0
	s_cmp_ge_i32 s80, s0
	s_mov_b32 s58, s80
	s_cbranch_scc0 .LBB0_549
	v_readlane_b32 s79, v255, 13
	s_and_b64 vcc, exec, s[38:39]
	s_cbranch_vccz .LBB0_552

; __device__ __forceinline__ int lane_id() { int l; asm volatile("v_mbcnt_lo_u32_b32 %0, -1, 0\n\tv_mbcnt_hi_u32_b32 %0, -1, %0" : "=v"(l)); return l; }
; #define G_STAGE(bufoff, gbase, voff) do { _Pragma("unroll") for (int _i = 0; _i < 2; ++_i) \
;         __builtin_amdgcn_global_load_lds((const unsigned*)((const char*)(gbase) + (voff)[_i]), (LAS unsigned*)(lds + (bufoff) + ldsw + _i * 8192), 16, 0, 0); } while (0)
; #define G_LDA(dst, b, h) do { _Pragma("unroll") for (int m = 0; m < 4; ++m) G_LD8(dst[m], lds + G_SA(b, h) + aoff + m * 2048); } while (0)
; #define G_LDB(dst, b, h) do { _Pragma("unroll") for (int n = 0; n < 2; ++n) G_LD8(dst[n], lds + G_SB(b, h) + boff + n * 2048); } while (0)
; #define G_SCHED __builtin_amdgcn_sched_barrier(0)
;     ...
;         for (int t = 0; t < nt; t += 2) {
;             const bool last = (t == nt - 2);
;             { const int tz_ = wid * 64 + lane_id();
; #pragma unroll
;               for (int i = 0; i < 2; ++i) { int R, C; stage_rc(tz_ * 16 + i * 8192, R, C); const int Rb = Epi::PERM ? ((R & ~31) + perm32(R & 31)) : R;
;                   voffA[i] = (unsigned)(R * S.multA * S.pitchA + C) * 2u; voffB[i] = (unsigned)(Rb * S.multB * S.pitchB + C) * 2u; } }
;             if constexpr (GATHER) asm volatile("" : "+v"(gc0[0]), "+v"(gc0[1]), "+v"(gc1[0]), "+v"(gc1[1]));
;             if constexpr (PREF) { if (t == nt - 4) S.prefetch(nxt, lds); }
;             const char* a11 = cur.a1 + (size_t)(t + 1) * kstep;
;             const char* a02 = last ? nxt.a0 : cur.a0 + (size_t)(t + 2) * kstep; const char* a12 = last ? nxt.a1 : cur.a1 + (size_t)(t + 2) * kstep;
;             const char* b02 = last ? nxt.b0 : cur.b0 + (size_t)(t + 2) * kstep; const char* b12 = last ? nxt.b1 : cur.b1 + (size_t)(t + 2) * kstep;
;             G_LDB(B0, 0, 0); G_LDB(B1, 0, 1); G_SCHED; G_LDA(At, 0, 0); G_STAGE(G_SA(1, 1), a11, vA1);
;     ...
;         for (int a = 0; a < 2; ++a)
; #pragma unroll
;             for (int b = 0; b < 2; ++b)
; #pragma unroll
;                 for (int m = 0; m < 4; ++m)
; #pragma unroll
;                     for (int n = 0; n < 2; ++n) acc[a][b][m][n] = (acc_t){0, 0, 0, 0};
;         cur = nxt; ++ui;
.LBB0_575:
	s_add_u32 s35, s56, 0x100
	s_addc_u32 s45, s57, 0
	s_add_u32 s49, s54, 0x100
	s_addc_u32 s58, s55, 0
	s_add_u32 s59, s52, 0x100
	s_addc_u32 s70, s53, 0
	s_add_u32 s50, s50, 0x80
	v_mov_b32_e32 v0, 0
	s_addc_u32 s51, s51, 0
	s_mov_b32 s52, 0
	v_mov_b32_e32 v1, v0
	v_mov_b32_e32 v2, v0
	v_mov_b32_e32 v3, v0
	v_mov_b32_e32 v4, v0
	v_mov_b32_e32 v5, v0
	v_mov_b32_e32 v6, v0
	v_mov_b32_e32 v7, v0
	v_mov_b32_e32 v16, v0
	v_mov_b32_e32 v17, v0
	v_mov_b32_e32 v18, v0
	v_mov_b32_e32 v19, v0
	v_mov_b32_e32 v20, v0
	v_mov_b32_e32 v21, v0
	v_mov_b32_e32 v22, v0
	v_mov_b32_e32 v23, v0
	v_mov_b32_e32 v32, v0
	v_mov_b32_e32 v33, v0
	v_mov_b32_e32 v34, v0
	v_mov_b32_e32 v35, v0
	v_mov_b32_e32 v36, v0
	v_mov_b32_e32 v37, v0
	v_mov_b32_e32 v38, v0
	v_mov_b32_e32 v39, v0
	v_mov_b32_e32 v48, v0
	v_mov_b32_e32 v49, v0
	v_mov_b32_e32 v50, v0
	v_mov_b32_e32 v51, v0
	v_mov_b32_e32 v52, v0
	v_mov_b32_e32 v53, v0
	v_mov_b32_e32 v54, v0
	v_mov_b32_e32 v55, v0
	v_mov_b32_e32 v8, v0
	v_mov_b32_e32 v9, v0
	v_mov_b32_e32 v10, v0
	v_mov_b32_e32 v11, v0
	v_mov_b32_e32 v12, v0
	v_mov_b32_e32 v13, v0
	v_mov_b32_e32 v14, v0
	v_mov_b32_e32 v15, v0
	v_mov_b32_e32 v24, v0
	v_mov_b32_e32 v25, v0
	v_mov_b32_e32 v26, v0
	v_mov_b32_e32 v27, v0
	v_mov_b32_e32 v28, v0
	v_mov_b32_e32 v29, v0
	v_mov_b32_e32 v30, v0
	v_mov_b32_e32 v31, v0
	v_mov_b32_e32 v40, v0
	v_mov_b32_e32 v41, v0
	v_mov_b32_e32 v42, v0
	v_mov_b32_e32 v43, v0
	v_mov_b32_e32 v44, v0
	v_mov_b32_e32 v45, v0
	v_mov_b32_e32 v46, v0
	v_mov_b32_e32 v47, v0
	v_mov_b32_e32 v56, v0
	v_mov_b32_e32 v57, v0
	v_mov_b32_e32 v58, v0
	v_mov_b32_e32 v59, v0
	v_mov_b32_e32 v60, v0
	v_mov_b32_e32 v61, v0
	v_mov_b32_e32 v62, v0
	v_mov_b32_e32 v63, v0
	v_mov_b32_e32 v64, v0
	v_mov_b32_e32 v65, v0
	v_mov_b32_e32 v66, v0
	v_mov_b32_e32 v67, v0
	v_mov_b32_e32 v68, v0
	v_mov_b32_e32 v69, v0
	v_mov_b32_e32 v70, v0
	v_mov_b32_e32 v71, v0
	v_mov_b32_e32 v80, v0
	v_mov_b32_e32 v81, v0
	v_mov_b32_e32 v82, v0
	v_mov_b32_e32 v83, v0
	v_mov_b32_e32 v84, v0
	v_mov_b32_e32 v85, v0
	v_mov_b32_e32 v86, v0
	v_mov_b32_e32 v87, v0
	v_mov_b32_e32 v96, v0
	v_mov_b32_e32 v97, v0
	v_mov_b32_e32 v98, v0
	v_mov_b32_e32 v99, v0
	v_mov_b32_e32 v100, v0
	v_mov_b32_e32 v101, v0
	v_mov_b32_e32 v102, v0
	v_mov_b32_e32 v103, v0
	v_mov_b32_e32 v112, v0
	v_mov_b32_e32 v113, v0
	v_mov_b32_e32 v114, v0
	v_mov_b32_e32 v115, v0
	v_mov_b32_e32 v116, v0
	v_mov_b32_e32 v117, v0
	v_mov_b32_e32 v118, v0
	v_mov_b32_e32 v119, v0
	v_mov_b32_e32 v72, v0
	v_mov_b32_e32 v73, v0
	v_mov_b32_e32 v74, v0
	v_mov_b32_e32 v75, v0
	v_mov_b32_e32 v76, v0
	v_mov_b32_e32 v77, v0
	v_mov_b32_e32 v78, v0
	v_mov_b32_e32 v79, v0
	v_mov_b32_e32 v88, v0
	v_mov_b32_e32 v89, v0
	v_mov_b32_e32 v90, v0
	v_mov_b32_e32 v91, v0
	v_mov_b32_e32 v92, v0
	v_mov_b32_e32 v93, v0
	v_mov_b32_e32 v94, v0
	v_mov_b32_e32 v95, v0
	v_mov_b32_e32 v104, v0
	v_mov_b32_e32 v105, v0
	v_mov_b32_e32 v106, v0
	v_mov_b32_e32 v107, v0
	v_mov_b32_e32 v108, v0
	v_mov_b32_e32 v109, v0
	v_mov_b32_e32 v110, v0
	v_mov_b32_e32 v111, v0
	v_mov_b32_e32 v120, v0
	v_mov_b32_e32 v121, v0
	v_mov_b32_e32 v122, v0
	v_mov_b32_e32 v123, v0
	v_mov_b32_e32 v124, v0
	v_mov_b32_e32 v125, v0
	v_mov_b32_e32 v126, v0
	v_mov_b32_e32 v127, v0
	v_mbcnt_lo_u32_b32 v248, -1, 0
	v_mbcnt_hi_u32_b32 v248, -1, v248
	v_mov_b32_e32 v249, s88
	v_lshrrev_b32_e32 v249, 6, v249
	v_and_b32_e32 v250, 3, v248
	v_lshlrev_b32_e32 v250, 4, v250
	v_and_b32_e32 v251, 32, v248
	v_xor_b32_e32 v250, v250, v251
	v_and_b32_e32 v251, 1, v249
	v_lshl_add_u32 v250, v251, 6, v250
	v_lshrrev_b32_e32 v251, 1, v249
	v_lshrrev_b32_e32 v252, 2, v248
	v_lshl_add_u32 v251, v251, 4, v252
	v_mov_b32_e32 v253, 0x600
	v_mad_u32_u24 v240, v251, v253, v250
	v_add_u32_e32 v242, 0x18000, v240
	v_lshrrev_b32_e32 v251, 2, v249
	v_lshlrev_b32_e32 v251, 5, v251
	v_lshrrev_b32_e32 v252, 4, v248
	v_lshl_add_u32 v251, v252, 3, v251
	v_bfe_u32 v252, v249, 1, 1
	v_lshl_add_u32 v251, v252, 2, v251
	v_bfe_u32 v252, v248, 2, 2
	v_add_u32_e32 v251, v251, v252
	v_mov_b32_e32 v253, 0x8000
	v_mad_u32_u24 v244, v251, v253, v250
	v_add_u32_e32 v246, 0x200000, v244
	v_mov_b32_e32 v241, 0
	v_mov_b32_e32 v243, 0
	v_mov_b32_e32 v245, 0
	v_mov_b32_e32 v247, 0
.LBB0_576:
	s_add_i32 s71, s52, 2
	ds_read_b128 v[138:141], v134
	ds_read_b128 v[142:145], v134 offset:1024
	ds_read_b128 v[146:149], v134 offset:2048
	ds_read_b128 v[150:153], v134 offset:3072
	ds_read_b128 v[154:157], v135
	ds_read_b128 v[158:161], v135 offset:1024
	ds_read_b128 v[162:165], v135 offset:2048
	ds_read_b128 v[166:169], v135 offset:3072
	s_add_u32 s72, s50, 0x80
	s_addc_u32 s53, s51, 0
	s_add_i32 s75, s22, s20
	s_add_i32 m0, s62, 0xc000
	s_add_i32 s74, s62, 0xe000
	s_add_i32 s76, s75, 0x2000
	s_cmp_eq_u32 s23, s52
	s_cselect_b32 s52, s38, s72
	s_cselect_b32 s55, s37, s70
	s_cselect_b32 s54, s36, s59
	s_cselect_b32 s57, s41, s45
	s_cselect_b32 s56, s40, s35
	s_cselect_b32 s53, s39, s53
	ds_read_b128 v[170:173], v136
	ds_read_b128 v[174:177], v136 offset:1024
	ds_read_b128 v[178:181], v136 offset:2048
	ds_read_b128 v[182:185], v136 offset:3072
	ds_read_b128 v[186:189], v136 offset:4096
	ds_read_b128 v[190:193], v136 offset:5120
	ds_read_b128 v[194:197], v136 offset:6144
	ds_read_b128 v[198:201], v136 offset:7168
	global_load_lds_dwordx4 v240, s[50:51]
	s_mov_b32 m0, s74
	v_mov_b32_e32 v205, v129
	global_load_lds_dwordx4 v242, s[50:51]
	s_waitcnt lgkmcnt(0)
	s_barrier
; #define G_STAGE(bufoff, gbase, voff) do { _Pragma("unroll") for (int _i = 0; _i < 2; ++_i) \
;         __builtin_amdgcn_global_load_lds((const unsigned*)((const char*)(gbase) + (voff)[_i]), (LAS unsigned*)(lds + (bufoff) + ldsw + _i * 8192), 16, 0, 0); } while (0)
; #define G_LDA(dst, b, h) do { _Pragma("unroll") for (int m = 0; m < 4; ++m) G_LD8(dst[m], lds + G_SA(b, h) + aoff + m * 2048); } while (0)
; #define G_WAIT_V(n) asm volatile("s_waitcnt vmcnt(" #n ")" ::: "memory")
; #define G_WAIT_L(n) asm volatile("s_waitcnt lgkmcnt(" #n ")" ::: "memory")
; #define G_BAR __builtin_amdgcn_s_barrier()
; #define G_SCHED __builtin_amdgcn_sched_barrier(0)
;     ...
;             G_WAIT_L(0); G_BAR; G_MMA(0, 0, At, B0); G_MMA(0, 1, At, B1); G_WAIT_V(8); G_BAR; G_SCHED;
;             G_LDA(At, 0, 1); G_STAGE(G_SB(0, 0), b02, voffB); G_STAGE(G_SB(0, 1), b12, voffB); G_STAGE(G_SA(0, 0), a02, vA0);
;             G_WAIT_L(0); G_BAR; G_MMA(1, 0, At, B0); G_MMA(1, 1, At, B1); G_WAIT_V(8); G_BAR; G_SCHED;
	s_setprio 1
	s_waitcnt lgkmcnt(0)
	v_mfma_f32_16x16x32_bf16 v[124:127], v[138:141], v[170:173], v[124:127]
	v_mfma_f32_16x16x32_bf16 v[120:123], v[146:149], v[170:173], v[120:123]
	v_mfma_f32_16x16x32_bf16 v[108:111], v[138:141], v[178:181], v[108:111]
	v_mfma_f32_16x16x32_bf16 v[104:107], v[146:149], v[178:181], v[104:107]
	v_mfma_f32_16x16x32_bf16 v[92:95], v[138:141], v[186:189], v[92:95]
	v_mfma_f32_16x16x32_bf16 v[88:91], v[146:149], v[186:189], v[88:91]
	v_mfma_f32_16x16x32_bf16 v[76:79], v[138:141], v[194:197], v[76:79]
	v_mfma_f32_16x16x32_bf16 v[72:75], v[146:149], v[194:197], v[72:75]
	v_mfma_f32_16x16x32_bf16 v[124:127], v[142:145], v[174:177], v[124:127]
	v_mfma_f32_16x16x32_bf16 v[120:123], v[150:153], v[174:177], v[120:123]
	v_mfma_f32_16x16x32_bf16 v[108:111], v[142:145], v[182:185], v[108:111]
	v_mfma_f32_16x16x32_bf16 v[104:107], v[150:153], v[182:185], v[104:107]
	v_mfma_f32_16x16x32_bf16 v[92:95], v[142:145], v[190:193], v[92:95]
	v_mfma_f32_16x16x32_bf16 v[88:91], v[150:153], v[190:193], v[88:91]
	v_mfma_f32_16x16x32_bf16 v[76:79], v[142:145], v[198:201], v[76:79]
	v_mfma_f32_16x16x32_bf16 v[72:75], v[150:153], v[198:201], v[72:75]
	s_setprio 0
	s_setprio 1
	v_mfma_f32_16x16x32_bf16 v[116:119], v[154:157], v[170:173], v[116:119]
	v_mfma_f32_16x16x32_bf16 v[112:115], v[162:165], v[170:173], v[112:115]
	v_mfma_f32_16x16x32_bf16 v[100:103], v[154:157], v[178:181], v[100:103]
	v_mfma_f32_16x16x32_bf16 v[96:99], v[162:165], v[178:181], v[96:99]
	v_mfma_f32_16x16x32_bf16 v[84:87], v[154:157], v[186:189], v[84:87]
	v_mfma_f32_16x16x32_bf16 v[80:83], v[162:165], v[186:189], v[80:83]
	v_mfma_f32_16x16x32_bf16 v[68:71], v[154:157], v[194:197], v[68:71]
	v_mfma_f32_16x16x32_bf16 v[64:67], v[162:165], v[194:197], v[64:67]
	v_mfma_f32_16x16x32_bf16 v[116:119], v[158:161], v[174:177], v[116:119]
	v_mfma_f32_16x16x32_bf16 v[112:115], v[166:169], v[174:177], v[112:115]
	v_mfma_f32_16x16x32_bf16 v[100:103], v[158:161], v[182:185], v[100:103]
	v_mfma_f32_16x16x32_bf16 v[96:99], v[166:169], v[182:185], v[96:99]
	v_mfma_f32_16x16x32_bf16 v[84:87], v[158:161], v[190:193], v[84:87]
	v_mfma_f32_16x16x32_bf16 v[80:83], v[166:169], v[190:193], v[80:83]
	v_mfma_f32_16x16x32_bf16 v[68:71], v[158:161], v[198:201], v[68:71]
	v_mfma_f32_16x16x32_bf16 v[64:67], v[166:169], v[198:201], v[64:67]
	s_setprio 0
	s_waitcnt vmcnt(8)
	s_barrier
	s_mov_b32 m0, s75
	ds_read_b128 v[170:173], v136 offset:16384
	ds_read_b128 v[174:177], v136 offset:17408
	ds_read_b128 v[178:181], v136 offset:18432
	ds_read_b128 v[182:185], v136 offset:19456
	ds_read_b128 v[186:189], v136 offset:20480
	ds_read_b128 v[190:193], v136 offset:21504
	ds_read_b128 v[194:197], v136 offset:22528
	ds_read_b128 v[198:201], v136 offset:23552
	global_load_lds_dwordx4 v244, s[56:57]
	s_mov_b32 m0, s76
	s_cselect_b32 s73, s43, s58
	s_cselect_b32 s72, s42, s49
	s_add_i32 s74, s24, s20
	global_load_lds_dwordx4 v246, s[56:57]
	s_mov_b32 m0, s74
	v_mov_b32_e32 v203, v129
	global_load_lds_dwordx4 v244, s[72:73]
	s_add_i32 m0, s74, 0x2000
	v_mov_b32_e32 v207, v129
	global_load_lds_dwordx4 v246, s[72:73]
	s_mov_b32 m0, s62
	v_lshl_add_u64 v[208:209], s[56:57], 0, v[244:245]
	global_load_lds_dwordx4 v240, s[54:55]
	s_mov_b32 m0, s63
	v_lshl_add_u64 v[210:211], s[56:57], 0, v[246:247]
	global_load_lds_dwordx4 v242, s[54:55]
	s_waitcnt lgkmcnt(0)
	v_lshl_add_u64 v[202:203], s[72:73], 0, v[244:245]
	v_lshl_add_u64 v[206:207], s[72:73], 0, v[246:247]
	v_lshl_add_u64 v[212:213], s[54:55], 0, v[240:241]
	v_lshl_add_u64 v[214:215], s[54:55], 0, v[242:243]
	s_barrier
	s_setprio 1
	s_waitcnt lgkmcnt(0)
	v_mfma_f32_16x16x32_bf16 v[60:63], v[138:141], v[170:173], v[60:63]
	v_mfma_f32_16x16x32_bf16 v[56:59], v[146:149], v[170:173], v[56:59]
	v_mfma_f32_16x16x32_bf16 v[44:47], v[138:141], v[178:181], v[44:47]
	v_mfma_f32_16x16x32_bf16 v[40:43], v[146:149], v[178:181], v[40:43]
	v_mfma_f32_16x16x32_bf16 v[28:31], v[138:141], v[186:189], v[28:31]
	v_mfma_f32_16x16x32_bf16 v[24:27], v[146:149], v[186:189], v[24:27]
	v_mfma_f32_16x16x32_bf16 v[12:15], v[138:141], v[194:197], v[12:15]
	v_mfma_f32_16x16x32_bf16 v[8:11], v[146:149], v[194:197], v[8:11]
	v_mfma_f32_16x16x32_bf16 v[60:63], v[142:145], v[174:177], v[60:63]
	v_mfma_f32_16x16x32_bf16 v[56:59], v[150:153], v[174:177], v[56:59]
	v_mfma_f32_16x16x32_bf16 v[44:47], v[142:145], v[182:185], v[44:47]
	v_mfma_f32_16x16x32_bf16 v[40:43], v[150:153], v[182:185], v[40:43]
	v_mfma_f32_16x16x32_bf16 v[28:31], v[142:145], v[190:193], v[28:31]
	v_mfma_f32_16x16x32_bf16 v[24:27], v[150:153], v[190:193], v[24:27]
	v_mfma_f32_16x16x32_bf16 v[12:15], v[142:145], v[198:201], v[12:15]
	v_mfma_f32_16x16x32_bf16 v[8:11], v[150:153], v[198:201], v[8:11]
	s_setprio 0
	s_setprio 1
	v_mfma_f32_16x16x32_bf16 v[52:55], v[154:157], v[170:173], v[52:55]
	v_mfma_f32_16x16x32_bf16 v[48:51], v[162:165], v[170:173], v[48:51]
	v_mfma_f32_16x16x32_bf16 v[36:39], v[154:157], v[178:181], v[36:39]
	v_mfma_f32_16x16x32_bf16 v[32:35], v[162:165], v[178:181], v[32:35]
	v_mfma_f32_16x16x32_bf16 v[20:23], v[154:157], v[186:189], v[20:23]
	v_mfma_f32_16x16x32_bf16 v[16:19], v[162:165], v[186:189], v[16:19]
	v_mfma_f32_16x16x32_bf16 v[4:7], v[154:157], v[194:197], v[4:7]
	v_mfma_f32_16x16x32_bf16 v[0:3], v[162:165], v[194:197], v[0:3]
	v_mfma_f32_16x16x32_bf16 v[52:55], v[158:161], v[174:177], v[52:55]
	v_mfma_f32_16x16x32_bf16 v[48:51], v[166:169], v[174:177], v[48:51]
	v_mfma_f32_16x16x32_bf16 v[36:39], v[158:161], v[182:185], v[36:39]
	v_mfma_f32_16x16x32_bf16 v[32:35], v[166:169], v[182:185], v[32:35]
	v_mfma_f32_16x16x32_bf16 v[20:23], v[158:161], v[190:193], v[20:23]
	v_mfma_f32_16x16x32_bf16 v[16:19], v[166:169], v[190:193], v[16:19]
	v_mfma_f32_16x16x32_bf16 v[4:7], v[158:161], v[198:201], v[4:7]
	v_mfma_f32_16x16x32_bf16 v[0:3], v[166:169], v[198:201], v[0:3]
	s_setprio 0
	s_waitcnt vmcnt(8)
	s_barrier
; #define G_STAGE(bufoff, gbase, voff) do { _Pragma("unroll") for (int _i = 0; _i < 2; ++_i) \
;         __builtin_amdgcn_global_load_lds((const unsigned*)((const char*)(gbase) + (voff)[_i]), (LAS unsigned*)(lds + (bufoff) + ldsw + _i * 8192), 16, 0, 0); } while (0)
; #define G_LDA(dst, b, h) do { _Pragma("unroll") for (int m = 0; m < 4; ++m) G_LD8(dst[m], lds + G_SA(b, h) + aoff + m * 2048); } while (0)
; #define G_LDB(dst, b, h) do { _Pragma("unroll") for (int n = 0; n < 2; ++n) G_LD8(dst[n], lds + G_SB(b, h) + boff + n * 2048); } while (0)
; #define G_WAIT_V(n) asm volatile("s_waitcnt vmcnt(" #n ")" ::: "memory")
; #define G_WAIT_L(n) asm volatile("s_waitcnt lgkmcnt(" #n ")" ::: "memory")
; #define G_BAR __builtin_amdgcn_s_barrier()
; #define G_SCHED __builtin_amdgcn_sched_barrier(0)
;     ...
;             G_LDB(B0, 1, 0); G_LDB(B1, 1, 1); G_SCHED; G_LDA(At, 1, 0); G_STAGE(G_SA(0, 1), a12, vA1);
;             G_WAIT_L(0); G_BAR; G_MMA(0, 0, At, B0); G_MMA(0, 1, At, B1); G_WAIT_V(8); G_BAR; G_SCHED;
	s_add_i32 s54, 0, 0x18000
	v_add_u32_e32 v137, s54, v133
	s_add_i32 s55, 0, 0x1c000
	ds_read_b128 v[138:141], v137
	ds_read_b128 v[142:145], v137 offset:1024
	ds_read_b128 v[146:149], v137 offset:2048
	ds_read_b128 v[150:153], v137 offset:3072
	v_add_u32_e32 v137, s55, v133
	ds_read_b128 v[154:157], v137
	ds_read_b128 v[158:161], v137 offset:1024
	ds_read_b128 v[162:165], v137 offset:2048
	ds_read_b128 v[166:169], v137 offset:3072
	s_mov_b32 m0, s64
	ds_read_b128 v[170:173], v136 offset:32768
	ds_read_b128 v[174:177], v136 offset:33792
	ds_read_b128 v[178:181], v136 offset:34816
	ds_read_b128 v[182:185], v136 offset:35840
	ds_read_b128 v[186:189], v136 offset:36864
	ds_read_b128 v[190:193], v136 offset:37888
	ds_read_b128 v[194:197], v136 offset:38912
	ds_read_b128 v[198:201], v136 offset:39936
	global_load_lds_dwordx4 v240, s[52:53]
	s_mov_b32 m0, s65
	s_nop 0
	global_load_lds_dwordx4 v242, s[52:53]
	s_waitcnt lgkmcnt(0)
	s_barrier
	s_setprio 1
	s_waitcnt lgkmcnt(0)
	v_mfma_f32_16x16x32_bf16 v[124:127], v[138:141], v[170:173], v[124:127]
	v_mfma_f32_16x16x32_bf16 v[120:123], v[146:149], v[170:173], v[120:123]
	v_mfma_f32_16x16x32_bf16 v[108:111], v[138:141], v[178:181], v[108:111]
	v_mfma_f32_16x16x32_bf16 v[104:107], v[146:149], v[178:181], v[104:107]
	v_mfma_f32_16x16x32_bf16 v[92:95], v[138:141], v[186:189], v[92:95]
	v_mfma_f32_16x16x32_bf16 v[88:91], v[146:149], v[186:189], v[88:91]
	v_mfma_f32_16x16x32_bf16 v[76:79], v[138:141], v[194:197], v[76:79]
	v_mfma_f32_16x16x32_bf16 v[72:75], v[146:149], v[194:197], v[72:75]
	v_mfma_f32_16x16x32_bf16 v[124:127], v[142:145], v[174:177], v[124:127]
	v_mfma_f32_16x16x32_bf16 v[120:123], v[150:153], v[174:177], v[120:123]
	v_mfma_f32_16x16x32_bf16 v[108:111], v[142:145], v[182:185], v[108:111]
	v_mfma_f32_16x16x32_bf16 v[104:107], v[150:153], v[182:185], v[104:107]
	v_mfma_f32_16x16x32_bf16 v[92:95], v[142:145], v[190:193], v[92:95]
	v_mfma_f32_16x16x32_bf16 v[88:91], v[150:153], v[190:193], v[88:91]
	v_mfma_f32_16x16x32_bf16 v[76:79], v[142:145], v[198:201], v[76:79]
	v_mfma_f32_16x16x32_bf16 v[72:75], v[150:153], v[198:201], v[72:75]
	s_setprio 0
	s_setprio 1
	v_mfma_f32_16x16x32_bf16 v[116:119], v[154:157], v[170:173], v[116:119]
	v_mfma_f32_16x16x32_bf16 v[112:115], v[162:165], v[170:173], v[112:115]
	v_mfma_f32_16x16x32_bf16 v[100:103], v[154:157], v[178:181], v[100:103]
	v_mfma_f32_16x16x32_bf16 v[96:99], v[162:165], v[178:181], v[96:99]
	v_mfma_f32_16x16x32_bf16 v[84:87], v[154:157], v[186:189], v[84:87]
	v_mfma_f32_16x16x32_bf16 v[80:83], v[162:165], v[186:189], v[80:83]
	v_mfma_f32_16x16x32_bf16 v[68:71], v[154:157], v[194:197], v[68:71]
	v_mfma_f32_16x16x32_bf16 v[64:67], v[162:165], v[194:197], v[64:67]
	v_mfma_f32_16x16x32_bf16 v[116:119], v[158:161], v[174:177], v[116:119]
	v_mfma_f32_16x16x32_bf16 v[112:115], v[166:169], v[174:177], v[112:115]
	v_mfma_f32_16x16x32_bf16 v[100:103], v[158:161], v[182:185], v[100:103]
	v_mfma_f32_16x16x32_bf16 v[96:99], v[166:169], v[182:185], v[96:99]
	v_mfma_f32_16x16x32_bf16 v[84:87], v[158:161], v[190:193], v[84:87]
	v_mfma_f32_16x16x32_bf16 v[80:83], v[166:169], v[190:193], v[80:83]
	v_mfma_f32_16x16x32_bf16 v[68:71], v[158:161], v[198:201], v[68:71]
	v_mfma_f32_16x16x32_bf16 v[64:67], v[166:169], v[198:201], v[64:67]
	s_setprio 0
	s_waitcnt vmcnt(8)
	s_barrier
; #define G_STAGE(bufoff, gbase, voff) do { _Pragma("unroll") for (int _i = 0; _i < 2; ++_i) \
;         __builtin_amdgcn_global_load_lds((const unsigned*)((const char*)(gbase) + (voff)[_i]), (LAS unsigned*)(lds + (bufoff) + ldsw + _i * 8192), 16, 0, 0); } while (0)
; #define G_LDA(dst, b, h) do { _Pragma("unroll") for (int m = 0; m < 4; ++m) G_LD8(dst[m], lds + G_SA(b, h) + aoff + m * 2048); } while (0)
; #define G_WAIT_V(n) asm volatile("s_waitcnt vmcnt(" #n ")" ::: "memory")
; #define G_WAIT_L(n) asm volatile("s_waitcnt lgkmcnt(" #n ")" ::: "memory")
; #define G_BAR __builtin_amdgcn_s_barrier()
; #define G_SCHED __builtin_amdgcn_sched_barrier(0)
;     ...
;             G_LDA(At, 1, 1); G_STAGE(G_SB(1, 0), b02 + kstep, voffB); G_STAGE(G_SB(1, 1), b12 + kstep, voffB); G_STAGE(G_SA(1, 0), a02 + kstep, vA0);
;             G_WAIT_L(0); G_BAR; G_MMA(1, 0, At, B0); G_MMA(1, 1, At, B1); G_WAIT_V(8); G_BAR; G_SCHED;
;         }
	s_add_i32 s52, s54, s20
	v_lshl_add_u64 v[204:205], v[208:209], 0, s[6:7]
	s_mov_b32 m0, s52
	ds_read_b128 v[170:173], v136 offset:49152
	ds_read_b128 v[174:177], v136 offset:50176
	ds_read_b128 v[178:181], v136 offset:51200
	ds_read_b128 v[182:185], v136 offset:52224
	ds_read_b128 v[186:189], v136 offset:53248
	ds_read_b128 v[190:193], v136 offset:54272
	ds_read_b128 v[194:197], v136 offset:55296
	ds_read_b128 v[198:201], v136 offset:56320
	global_load_lds_dwordx4 v[204:205], off
	v_lshl_add_u64 v[204:205], v[210:211], 0, s[6:7]
	s_add_i32 m0, s52, 0x2000
	s_add_i32 s52, s55, s20
	global_load_lds_dwordx4 v[204:205], off
	v_lshl_add_u64 v[202:203], v[202:203], 0, s[6:7]
	s_mov_b32 m0, s52
	s_nop 0
	global_load_lds_dwordx4 v[202:203], off
	v_lshl_add_u64 v[202:203], v[206:207], 0, s[6:7]
	s_add_i32 m0, s52, 0x2000
	s_nop 0
	global_load_lds_dwordx4 v[202:203], off
	v_lshl_add_u64 v[202:203], v[212:213], 0, s[6:7]
	s_mov_b32 m0, s25
	s_nop 0
	global_load_lds_dwordx4 v[202:203], off
	v_lshl_add_u64 v[202:203], v[214:215], 0, s[6:7]
	s_mov_b32 m0, s67
	s_nop 0
	global_load_lds_dwordx4 v[202:203], off
	s_waitcnt lgkmcnt(0)
	s_barrier
	s_setprio 1
	s_waitcnt lgkmcnt(0)
	v_mfma_f32_16x16x32_bf16 v[60:63], v[138:141], v[170:173], v[60:63]
	v_mfma_f32_16x16x32_bf16 v[56:59], v[146:149], v[170:173], v[56:59]
	v_mfma_f32_16x16x32_bf16 v[44:47], v[138:141], v[178:181], v[44:47]
	v_mfma_f32_16x16x32_bf16 v[40:43], v[146:149], v[178:181], v[40:43]
	v_mfma_f32_16x16x32_bf16 v[28:31], v[138:141], v[186:189], v[28:31]
	v_mfma_f32_16x16x32_bf16 v[24:27], v[146:149], v[186:189], v[24:27]
	v_mfma_f32_16x16x32_bf16 v[12:15], v[138:141], v[194:197], v[12:15]
	v_mfma_f32_16x16x32_bf16 v[8:11], v[146:149], v[194:197], v[8:11]
	v_mfma_f32_16x16x32_bf16 v[60:63], v[142:145], v[174:177], v[60:63]
	v_mfma_f32_16x16x32_bf16 v[56:59], v[150:153], v[174:177], v[56:59]
	v_mfma_f32_16x16x32_bf16 v[44:47], v[142:145], v[182:185], v[44:47]
	v_mfma_f32_16x16x32_bf16 v[40:43], v[150:153], v[182:185], v[40:43]
	v_mfma_f32_16x16x32_bf16 v[28:31], v[142:145], v[190:193], v[28:31]
	v_mfma_f32_16x16x32_bf16 v[24:27], v[150:153], v[190:193], v[24:27]
	v_mfma_f32_16x16x32_bf16 v[12:15], v[142:145], v[198:201], v[12:15]
	v_mfma_f32_16x16x32_bf16 v[8:11], v[150:153], v[198:201], v[8:11]
	s_setprio 0
	s_setprio 1
	v_mfma_f32_16x16x32_bf16 v[52:55], v[154:157], v[170:173], v[52:55]
	v_mfma_f32_16x16x32_bf16 v[48:51], v[162:165], v[170:173], v[48:51]
	v_mfma_f32_16x16x32_bf16 v[36:39], v[154:157], v[178:181], v[36:39]
	v_mfma_f32_16x16x32_bf16 v[32:35], v[162:165], v[178:181], v[32:35]
	v_mfma_f32_16x16x32_bf16 v[20:23], v[154:157], v[186:189], v[20:23]
	v_mfma_f32_16x16x32_bf16 v[16:19], v[162:165], v[186:189], v[16:19]
	v_mfma_f32_16x16x32_bf16 v[4:7], v[154:157], v[194:197], v[4:7]
	v_mfma_f32_16x16x32_bf16 v[0:3], v[162:165], v[194:197], v[0:3]
	v_mfma_f32_16x16x32_bf16 v[52:55], v[158:161], v[174:177], v[52:55]
	v_mfma_f32_16x16x32_bf16 v[48:51], v[166:169], v[174:177], v[48:51]
	v_mfma_f32_16x16x32_bf16 v[36:39], v[158:161], v[182:185], v[36:39]
	v_mfma_f32_16x16x32_bf16 v[32:35], v[166:169], v[182:185], v[32:35]
	v_mfma_f32_16x16x32_bf16 v[20:23], v[158:161], v[190:193], v[20:23]
	v_mfma_f32_16x16x32_bf16 v[16:19], v[166:169], v[190:193], v[16:19]
	v_mfma_f32_16x16x32_bf16 v[4:7], v[158:161], v[198:201], v[4:7]
	v_mfma_f32_16x16x32_bf16 v[0:3], v[166:169], v[198:201], v[0:3]
	s_setprio 0
	s_waitcnt vmcnt(8)
	s_barrier
	s_add_u32 s35, s35, 0x100
	s_addc_u32 s45, s45, 0
	s_add_u32 s49, s49, 0x100
	s_addc_u32 s58, s58, 0
	s_add_u32 s59, s59, 0x100
	s_addc_u32 s70, s70, 0
	s_add_u32 s50, s50, 0x100
	s_addc_u32 s51, s51, 0
	s_cmp_ge_i32 s71, s2
	s_mov_b32 s52, s71
	s_cbranch_scc0 .LBB0_576
	s_and_b64 vcc, exec, s[14:15]
	s_cbranch_vccz .LBB0_579

; __device__ __forceinline__ int lane_id() { int l; asm volatile("v_mbcnt_lo_u32_b32 %0, -1, 0\n\tv_mbcnt_hi_u32_b32 %0, -1, %0" : "=v"(l)); return l; }
; #define G_STAGE(bufoff, gbase, voff) do { _Pragma("unroll") for (int _i = 0; _i < 2; ++_i) \
;         __builtin_amdgcn_global_load_lds((const unsigned*)((const char*)(gbase) + (voff)[_i]), (LAS unsigned*)(lds + (bufoff) + ldsw + _i * 8192), 16, 0, 0); } while (0)
; #define G_LDA(dst, b, h) do { _Pragma("unroll") for (int m = 0; m < 4; ++m) G_LD8(dst[m], lds + G_SA(b, h) + aoff + m * 2048); } while (0)
; #define G_LDB(dst, b, h) do { _Pragma("unroll") for (int n = 0; n < 2; ++n) G_LD8(dst[n], lds + G_SB(b, h) + boff + n * 2048); } while (0)
; #define G_SCHED __builtin_amdgcn_sched_barrier(0)
;     ...
;         for (int t = 0; t < nt; t += 2) {
;             const bool last = (t == nt - 2);
;             { const int tz_ = wid * 64 + lane_id();
; #pragma unroll
;               for (int i = 0; i < 2; ++i) { int R, C; stage_rc(tz_ * 16 + i * 8192, R, C); const int Rb = Epi::PERM ? ((R & ~31) + perm32(R & 31)) : R;
;                   voffA[i] = (unsigned)(R * S.multA * S.pitchA + C) * 2u; voffB[i] = (unsigned)(Rb * S.multB * S.pitchB + C) * 2u; } }
;             if constexpr (GATHER) asm volatile("" : "+v"(gc0[0]), "+v"(gc0[1]), "+v"(gc1[0]), "+v"(gc1[1]));
;             if constexpr (PREF) { if (t == nt - 4) S.prefetch(nxt, lds); }
;             const char* a11 = cur.a1 + (size_t)(t + 1) * kstep;
;             const char* a02 = last ? nxt.a0 : cur.a0 + (size_t)(t + 2) * kstep; const char* a12 = last ? nxt.a1 : cur.a1 + (size_t)(t + 2) * kstep;
;             const char* b02 = last ? nxt.b0 : cur.b0 + (size_t)(t + 2) * kstep; const char* b12 = last ? nxt.b1 : cur.b1 + (size_t)(t + 2) * kstep;
;             G_LDB(B0, 0, 0); G_LDB(B1, 0, 1); G_SCHED; G_LDA(At, 0, 0); G_STAGE(G_SA(1, 1), a11, vA1);
;     ...
; #pragma unroll
;         for (int a = 0; a < 2; ++a)
; #pragma unroll
;             for (int b = 0; b < 2; ++b)
; #pragma unroll
;                 for (int m = 0; m < 4; ++m)
; #pragma unroll
;                     for (int n = 0; n < 2; ++n) acc[a][b][m][n] = (acc_t){0, 0, 0, 0};
;         cur = nxt; ++ui;
.LBB0_811:
	s_add_u32 s60, s54, 0x100
	s_addc_u32 s61, s55, 0
	s_add_u32 s62, s52, 0x100
	s_addc_u32 s71, s53, 0
	s_add_u32 s72, s58, 0x100
	s_addc_u32 s73, s59, 0
	s_add_u32 s52, s56, 0x80
	v_mov_b32_e32 v0, 0
	s_addc_u32 s53, s57, 0
	s_mov_b32 s54, 0
	v_mov_b32_e32 v1, v0
	v_mov_b32_e32 v2, v0
	v_mov_b32_e32 v3, v0
	v_mov_b32_e32 v4, v0
	v_mov_b32_e32 v5, v0
	v_mov_b32_e32 v6, v0
	v_mov_b32_e32 v7, v0
	v_mov_b32_e32 v16, v0
	v_mov_b32_e32 v17, v0
	v_mov_b32_e32 v18, v0
	v_mov_b32_e32 v19, v0
	v_mov_b32_e32 v20, v0
	v_mov_b32_e32 v21, v0
	v_mov_b32_e32 v22, v0
	v_mov_b32_e32 v23, v0
	v_mov_b32_e32 v32, v0
	v_mov_b32_e32 v33, v0
	v_mov_b32_e32 v34, v0
	v_mov_b32_e32 v35, v0
	v_mov_b32_e32 v36, v0
	v_mov_b32_e32 v37, v0
	v_mov_b32_e32 v38, v0
	v_mov_b32_e32 v39, v0
	v_mov_b32_e32 v48, v0
	v_mov_b32_e32 v49, v0
	v_mov_b32_e32 v50, v0
	v_mov_b32_e32 v51, v0
	v_mov_b32_e32 v52, v0
	v_mov_b32_e32 v53, v0
	v_mov_b32_e32 v54, v0
	v_mov_b32_e32 v55, v0
	v_mov_b32_e32 v8, v0
	v_mov_b32_e32 v9, v0
	v_mov_b32_e32 v10, v0
	v_mov_b32_e32 v11, v0
	v_mov_b32_e32 v12, v0
	v_mov_b32_e32 v13, v0
	v_mov_b32_e32 v14, v0
	v_mov_b32_e32 v15, v0
	v_mov_b32_e32 v24, v0
	v_mov_b32_e32 v25, v0
	v_mov_b32_e32 v26, v0
	v_mov_b32_e32 v27, v0
	v_mov_b32_e32 v28, v0
	v_mov_b32_e32 v29, v0
	v_mov_b32_e32 v30, v0
	v_mov_b32_e32 v31, v0
	v_mov_b32_e32 v40, v0
	v_mov_b32_e32 v41, v0
	v_mov_b32_e32 v42, v0
	v_mov_b32_e32 v43, v0
	v_mov_b32_e32 v44, v0
	v_mov_b32_e32 v45, v0
	v_mov_b32_e32 v46, v0
	v_mov_b32_e32 v47, v0
	v_mov_b32_e32 v56, v0
	v_mov_b32_e32 v57, v0
	v_mov_b32_e32 v58, v0
	v_mov_b32_e32 v59, v0
	v_mov_b32_e32 v60, v0
	v_mov_b32_e32 v61, v0
	v_mov_b32_e32 v62, v0
	v_mov_b32_e32 v63, v0
	v_mov_b32_e32 v64, v0
	v_mov_b32_e32 v65, v0
	v_mov_b32_e32 v66, v0
	v_mov_b32_e32 v67, v0
	v_mov_b32_e32 v68, v0
	v_mov_b32_e32 v69, v0
	v_mov_b32_e32 v70, v0
	v_mov_b32_e32 v71, v0
	v_mov_b32_e32 v80, v0
	v_mov_b32_e32 v81, v0
	v_mov_b32_e32 v82, v0
	v_mov_b32_e32 v83, v0
	v_mov_b32_e32 v84, v0
	v_mov_b32_e32 v85, v0
	v_mov_b32_e32 v86, v0
	v_mov_b32_e32 v87, v0
	v_mov_b32_e32 v96, v0
	v_mov_b32_e32 v97, v0
	v_mov_b32_e32 v98, v0
	v_mov_b32_e32 v99, v0
	v_mov_b32_e32 v100, v0
	v_mov_b32_e32 v101, v0
	v_mov_b32_e32 v102, v0
	v_mov_b32_e32 v103, v0
	v_mov_b32_e32 v112, v0
	v_mov_b32_e32 v113, v0
	v_mov_b32_e32 v114, v0
	v_mov_b32_e32 v115, v0
	v_mov_b32_e32 v116, v0
	v_mov_b32_e32 v117, v0
	v_mov_b32_e32 v118, v0
	v_mov_b32_e32 v119, v0
	v_mov_b32_e32 v72, v0
	v_mov_b32_e32 v73, v0
	v_mov_b32_e32 v74, v0
	v_mov_b32_e32 v75, v0
	v_mov_b32_e32 v76, v0
	v_mov_b32_e32 v77, v0
	v_mov_b32_e32 v78, v0
	v_mov_b32_e32 v79, v0
	v_mov_b32_e32 v88, v0
	v_mov_b32_e32 v89, v0
	v_mov_b32_e32 v90, v0
	v_mov_b32_e32 v91, v0
	v_mov_b32_e32 v92, v0
	v_mov_b32_e32 v93, v0
	v_mov_b32_e32 v94, v0
	v_mov_b32_e32 v95, v0
	v_mov_b32_e32 v104, v0
	v_mov_b32_e32 v105, v0
	v_mov_b32_e32 v106, v0
	v_mov_b32_e32 v107, v0
	v_mov_b32_e32 v108, v0
	v_mov_b32_e32 v109, v0
	v_mov_b32_e32 v110, v0
	v_mov_b32_e32 v111, v0
	v_mov_b32_e32 v120, v0
	v_mov_b32_e32 v121, v0
	v_mov_b32_e32 v122, v0
	v_mov_b32_e32 v123, v0
	v_mov_b32_e32 v124, v0
	v_mov_b32_e32 v125, v0
	v_mov_b32_e32 v126, v0
	v_mov_b32_e32 v127, v0
	v_mbcnt_lo_u32_b32 v248, -1, 0
	v_mbcnt_hi_u32_b32 v248, -1, v248
	v_mov_b32_e32 v249, s88
	v_lshrrev_b32_e32 v249, 6, v249
	v_and_b32_e32 v250, 3, v248
	v_lshlrev_b32_e32 v250, 4, v250
	v_and_b32_e32 v251, 32, v248
	v_xor_b32_e32 v250, v250, v251
	v_and_b32_e32 v251, 1, v249
	v_lshl_add_u32 v250, v251, 6, v250
	v_lshrrev_b32_e32 v251, 1, v249
	v_lshrrev_b32_e32 v252, 2, v248
	v_lshl_add_u32 v251, v251, 4, v252
	v_mov_b32_e32 v253, 0x200
	v_mad_u32_u24 v240, v251, v253, v250
	v_add_u32_e32 v242, 0x8000, v240
	v_lshrrev_b32_e32 v251, 2, v249
	v_lshlrev_b32_e32 v251, 5, v251
	v_lshrrev_b32_e32 v252, 4, v248
	v_lshl_add_u32 v251, v252, 3, v251
	v_bfe_u32 v252, v249, 1, 1
	v_lshl_add_u32 v251, v252, 2, v251
	v_bfe_u32 v252, v248, 2, 2
	v_add_u32_e32 v251, v251, v252
	v_mov_b32_e32 v253, 0x200
	v_mad_u32_u24 v244, v251, v253, v250
	v_add_u32_e32 v246, 0x8000, v244
	v_mov_b32_e32 v241, 0
	v_mov_b32_e32 v243, 0
	v_mov_b32_e32 v245, 0
	v_mov_b32_e32 v247, 0
.LBB0_812:
	s_add_i32 s74, s54, 2
	ds_read_b128 v[138:141], v134
	ds_read_b128 v[142:145], v134 offset:1024
	ds_read_b128 v[146:149], v134 offset:2048
	ds_read_b128 v[150:153], v134 offset:3072
	ds_read_b128 v[154:157], v135
	ds_read_b128 v[158:161], v135 offset:1024
	ds_read_b128 v[162:165], v135 offset:2048
	ds_read_b128 v[166:169], v135 offset:3072
	s_add_u32 s75, s52, 0x80
	s_addc_u32 s55, s53, 0
	s_add_i32 s78, s68, s20
	s_add_i32 m0, s22, 0xc000
	s_add_i32 s77, s22, 0xe000
	s_add_i32 s79, s78, 0x2000
	s_cmp_eq_u32 s67, s54
	s_cselect_b32 s54, s46, s75
	s_cselect_b32 s57, s49, s73
	s_cselect_b32 s56, s48, s72
	s_cselect_b32 s59, s43, s61
	s_cselect_b32 s58, s42, s60
	s_cselect_b32 s55, s47, s55
	ds_read_b128 v[170:173], v136
	ds_read_b128 v[174:177], v136 offset:1024
	ds_read_b128 v[178:181], v136 offset:2048
	ds_read_b128 v[182:185], v136 offset:3072
	ds_read_b128 v[186:189], v136 offset:4096
	ds_read_b128 v[190:193], v136 offset:5120
	ds_read_b128 v[194:197], v136 offset:6144
	ds_read_b128 v[198:201], v136 offset:7168
	global_load_lds_dwordx4 v240, s[52:53]
	s_mov_b32 m0, s77
	v_mov_b32_e32 v205, v129
	global_load_lds_dwordx4 v242, s[52:53]
	s_waitcnt lgkmcnt(0)
	s_barrier
; #define G_STAGE(bufoff, gbase, voff) do { _Pragma("unroll") for (int _i = 0; _i < 2; ++_i) \
;         __builtin_amdgcn_global_load_lds((const unsigned*)((const char*)(gbase) + (voff)[_i]), (LAS unsigned*)(lds + (bufoff) + ldsw + _i * 8192), 16, 0, 0); } while (0)
; #define G_LDA(dst, b, h) do { _Pragma("unroll") for (int m = 0; m < 4; ++m) G_LD8(dst[m], lds + G_SA(b, h) + aoff + m * 2048); } while (0)
; #define G_LDB(dst, b, h) do { _Pragma("unroll") for (int n = 0; n < 2; ++n) G_LD8(dst[n], lds + G_SB(b, h) + boff + n * 2048); } while (0)
; #define G_WAIT_V(n) asm volatile("s_waitcnt vmcnt(" #n ")" ::: "memory")
; #define G_WAIT_L(n) asm volatile("s_waitcnt lgkmcnt(" #n ")" ::: "memory")
; #define G_BAR __builtin_amdgcn_s_barrier()
; #define G_SCHED __builtin_amdgcn_sched_barrier(0)
;     __device__ __forceinline__ unsigned row_off(const Unit& u, int r, LAS unsigned char* lds) const { return (unsigned)((const LAS int*)(lds + LDS_STAGE + u.q * 4096))[r] * (unsigned)rowbytes; }
;     ...
;             G_LDB(B0, 0, 0); G_LDB(B1, 0, 1); G_SCHED; G_LDA(At, 0, 0); G_STAGE(G_SA(1, 1), a11, vA1);
;             if constexpr (GATHER) { if (last) { int tz = tid; asm volatile("" : "+v"(tz));
; #pragma unroll
;                 for (int i = 0; i < 2; ++i) { int R, C; stage_rc(tz * 16 + i * 8192, R, C); gc0[i] = S.row_off(nxt, R, lds) + (unsigned)C * 2u; gc1[i] = S.row_off(nxt, 128 + R, lds) + (unsigned)C * 2u; } } }
;             G_WAIT_L(0); G_BAR; G_MMA(0, 0, At, B0); G_MMA(0, 1, At, B1); G_WAIT_V(8); G_BAR; G_SCHED;
;             G_LDA(At, 0, 1); G_STAGE(G_SB(0, 0), b02, voffB); G_STAGE(G_SB(0, 1), b12, voffB); G_STAGE(G_SA(0, 0), a02, vA0);
;             G_WAIT_L(0); G_BAR; G_MMA(1, 0, At, B0); G_MMA(1, 1, At, B1); G_WAIT_V(8); G_BAR; G_SCHED;
	s_setprio 1
	s_waitcnt lgkmcnt(0)
	v_mfma_f32_16x16x32_bf16 v[124:127], v[138:141], v[170:173], v[124:127]
	v_mfma_f32_16x16x32_bf16 v[120:123], v[146:149], v[170:173], v[120:123]
	v_mfma_f32_16x16x32_bf16 v[108:111], v[138:141], v[178:181], v[108:111]
	v_mfma_f32_16x16x32_bf16 v[104:107], v[146:149], v[178:181], v[104:107]
	v_mfma_f32_16x16x32_bf16 v[92:95], v[138:141], v[186:189], v[92:95]
	v_mfma_f32_16x16x32_bf16 v[88:91], v[146:149], v[186:189], v[88:91]
	v_mfma_f32_16x16x32_bf16 v[76:79], v[138:141], v[194:197], v[76:79]
	v_mfma_f32_16x16x32_bf16 v[72:75], v[146:149], v[194:197], v[72:75]
	v_mfma_f32_16x16x32_bf16 v[124:127], v[142:145], v[174:177], v[124:127]
	v_mfma_f32_16x16x32_bf16 v[120:123], v[150:153], v[174:177], v[120:123]
	v_mfma_f32_16x16x32_bf16 v[108:111], v[142:145], v[182:185], v[108:111]
	v_mfma_f32_16x16x32_bf16 v[104:107], v[150:153], v[182:185], v[104:107]
	v_mfma_f32_16x16x32_bf16 v[92:95], v[142:145], v[190:193], v[92:95]
	v_mfma_f32_16x16x32_bf16 v[88:91], v[150:153], v[190:193], v[88:91]
	v_mfma_f32_16x16x32_bf16 v[76:79], v[142:145], v[198:201], v[76:79]
	v_mfma_f32_16x16x32_bf16 v[72:75], v[150:153], v[198:201], v[72:75]
	s_setprio 0
	s_setprio 1
	v_mfma_f32_16x16x32_bf16 v[116:119], v[154:157], v[170:173], v[116:119]
	v_mfma_f32_16x16x32_bf16 v[112:115], v[162:165], v[170:173], v[112:115]
	v_mfma_f32_16x16x32_bf16 v[100:103], v[154:157], v[178:181], v[100:103]
	v_mfma_f32_16x16x32_bf16 v[96:99], v[162:165], v[178:181], v[96:99]
	v_mfma_f32_16x16x32_bf16 v[84:87], v[154:157], v[186:189], v[84:87]
	v_mfma_f32_16x16x32_bf16 v[80:83], v[162:165], v[186:189], v[80:83]
	v_mfma_f32_16x16x32_bf16 v[68:71], v[154:157], v[194:197], v[68:71]
	v_mfma_f32_16x16x32_bf16 v[64:67], v[162:165], v[194:197], v[64:67]
	v_mfma_f32_16x16x32_bf16 v[116:119], v[158:161], v[174:177], v[116:119]
	v_mfma_f32_16x16x32_bf16 v[112:115], v[166:169], v[174:177], v[112:115]
	v_mfma_f32_16x16x32_bf16 v[100:103], v[158:161], v[182:185], v[100:103]
	v_mfma_f32_16x16x32_bf16 v[96:99], v[166:169], v[182:185], v[96:99]
	v_mfma_f32_16x16x32_bf16 v[84:87], v[158:161], v[190:193], v[84:87]
	v_mfma_f32_16x16x32_bf16 v[80:83], v[166:169], v[190:193], v[80:83]
	v_mfma_f32_16x16x32_bf16 v[68:71], v[158:161], v[198:201], v[68:71]
	v_mfma_f32_16x16x32_bf16 v[64:67], v[166:169], v[198:201], v[64:67]
	s_setprio 0
	s_waitcnt vmcnt(8)
	s_barrier
	s_mov_b32 m0, s78
	ds_read_b128 v[170:173], v136 offset:16384
	ds_read_b128 v[174:177], v136 offset:17408
	ds_read_b128 v[178:181], v136 offset:18432
	ds_read_b128 v[182:185], v136 offset:19456
	ds_read_b128 v[186:189], v136 offset:20480
	ds_read_b128 v[190:193], v136 offset:21504
	ds_read_b128 v[194:197], v136 offset:22528
	ds_read_b128 v[198:201], v136 offset:23552
	global_load_lds_dwordx4 v244, s[58:59]
	s_mov_b32 m0, s79
	s_cselect_b32 s79, s45, s71
	s_cselect_b32 s78, s44, s62
	s_add_i32 s75, s69, s20
	global_load_lds_dwordx4 v246, s[58:59]
	s_mov_b32 m0, s75
	v_mov_b32_e32 v203, v129
	global_load_lds_dwordx4 v244, s[78:79]
	s_add_i32 m0, s75, 0x2000
	v_mov_b32_e32 v207, v129
	global_load_lds_dwordx4 v246, s[78:79]
	s_mov_b32 m0, s22
	v_lshl_add_u64 v[208:209], s[58:59], 0, v[244:245]
	global_load_lds_dwordx4 v240, s[56:57]
	s_mov_b32 m0, s23
	v_lshl_add_u64 v[210:211], s[58:59], 0, v[246:247]
	global_load_lds_dwordx4 v242, s[56:57]
	s_waitcnt lgkmcnt(0)
	v_lshl_add_u64 v[202:203], s[78:79], 0, v[244:245]
	v_lshl_add_u64 v[206:207], s[78:79], 0, v[246:247]
	v_lshl_add_u64 v[212:213], s[56:57], 0, v[240:241]
	v_lshl_add_u64 v[214:215], s[56:57], 0, v[242:243]
	s_barrier
	s_setprio 1
	s_waitcnt lgkmcnt(0)
	v_mfma_f32_16x16x32_bf16 v[60:63], v[138:141], v[170:173], v[60:63]
	v_mfma_f32_16x16x32_bf16 v[56:59], v[146:149], v[170:173], v[56:59]
	v_mfma_f32_16x16x32_bf16 v[44:47], v[138:141], v[178:181], v[44:47]
	v_mfma_f32_16x16x32_bf16 v[40:43], v[146:149], v[178:181], v[40:43]
	v_mfma_f32_16x16x32_bf16 v[28:31], v[138:141], v[186:189], v[28:31]
	v_mfma_f32_16x16x32_bf16 v[24:27], v[146:149], v[186:189], v[24:27]
	v_mfma_f32_16x16x32_bf16 v[12:15], v[138:141], v[194:197], v[12:15]
	v_mfma_f32_16x16x32_bf16 v[8:11], v[146:149], v[194:197], v[8:11]
	v_mfma_f32_16x16x32_bf16 v[60:63], v[142:145], v[174:177], v[60:63]
	v_mfma_f32_16x16x32_bf16 v[56:59], v[150:153], v[174:177], v[56:59]
	v_mfma_f32_16x16x32_bf16 v[44:47], v[142:145], v[182:185], v[44:47]
	v_mfma_f32_16x16x32_bf16 v[40:43], v[150:153], v[182:185], v[40:43]
	v_mfma_f32_16x16x32_bf16 v[28:31], v[142:145], v[190:193], v[28:31]
	v_mfma_f32_16x16x32_bf16 v[24:27], v[150:153], v[190:193], v[24:27]
	v_mfma_f32_16x16x32_bf16 v[12:15], v[142:145], v[198:201], v[12:15]
	v_mfma_f32_16x16x32_bf16 v[8:11], v[150:153], v[198:201], v[8:11]
	s_setprio 0
	s_setprio 1
	v_mfma_f32_16x16x32_bf16 v[52:55], v[154:157], v[170:173], v[52:55]
	v_mfma_f32_16x16x32_bf16 v[48:51], v[162:165], v[170:173], v[48:51]
	v_mfma_f32_16x16x32_bf16 v[36:39], v[154:157], v[178:181], v[36:39]
	v_mfma_f32_16x16x32_bf16 v[32:35], v[162:165], v[178:181], v[32:35]
	v_mfma_f32_16x16x32_bf16 v[20:23], v[154:157], v[186:189], v[20:23]
	v_mfma_f32_16x16x32_bf16 v[16:19], v[162:165], v[186:189], v[16:19]
	v_mfma_f32_16x16x32_bf16 v[4:7], v[154:157], v[194:197], v[4:7]
	v_mfma_f32_16x16x32_bf16 v[0:3], v[162:165], v[194:197], v[0:3]
	v_mfma_f32_16x16x32_bf16 v[52:55], v[158:161], v[174:177], v[52:55]
	v_mfma_f32_16x16x32_bf16 v[48:51], v[166:169], v[174:177], v[48:51]
	v_mfma_f32_16x16x32_bf16 v[36:39], v[158:161], v[182:185], v[36:39]
	v_mfma_f32_16x16x32_bf16 v[32:35], v[166:169], v[182:185], v[32:35]
	v_mfma_f32_16x16x32_bf16 v[20:23], v[158:161], v[190:193], v[20:23]
	v_mfma_f32_16x16x32_bf16 v[16:19], v[166:169], v[190:193], v[16:19]
	v_mfma_f32_16x16x32_bf16 v[4:7], v[158:161], v[198:201], v[4:7]
	v_mfma_f32_16x16x32_bf16 v[0:3], v[166:169], v[198:201], v[0:3]
	s_setprio 0
	s_waitcnt vmcnt(8)
	s_barrier
; #define G_STAGE(bufoff, gbase, voff) do { _Pragma("unroll") for (int _i = 0; _i < 2; ++_i) \
;         __builtin_amdgcn_global_load_lds((const unsigned*)((const char*)(gbase) + (voff)[_i]), (LAS unsigned*)(lds + (bufoff) + ldsw + _i * 8192), 16, 0, 0); } while (0)
; #define G_LDA(dst, b, h) do { _Pragma("unroll") for (int m = 0; m < 4; ++m) G_LD8(dst[m], lds + G_SA(b, h) + aoff + m * 2048); } while (0)
; #define G_LDB(dst, b, h) do { _Pragma("unroll") for (int n = 0; n < 2; ++n) G_LD8(dst[n], lds + G_SB(b, h) + boff + n * 2048); } while (0)
; #define G_WAIT_V(n) asm volatile("s_waitcnt vmcnt(" #n ")" ::: "memory")
; #define G_WAIT_L(n) asm volatile("s_waitcnt lgkmcnt(" #n ")" ::: "memory")
; #define G_BAR __builtin_amdgcn_s_barrier()
; #define G_SCHED __builtin_amdgcn_sched_barrier(0)
;     ...
;             G_LDB(B0, 1, 0); G_LDB(B1, 1, 1); G_SCHED; G_LDA(At, 1, 0); G_STAGE(G_SA(0, 1), a12, vA1);
;             G_WAIT_L(0); G_BAR; G_MMA(0, 0, At, B0); G_MMA(0, 1, At, B1); G_WAIT_V(8); G_BAR; G_SCHED;
	s_add_i32 s56, 0, 0x18000
	v_add_u32_e32 v137, s56, v133
	s_add_i32 s57, 0, 0x1c000
	ds_read_b128 v[138:141], v137
	ds_read_b128 v[142:145], v137 offset:1024
	ds_read_b128 v[146:149], v137 offset:2048
	ds_read_b128 v[150:153], v137 offset:3072
	v_add_u32_e32 v137, s57, v133
	ds_read_b128 v[154:157], v137
	ds_read_b128 v[158:161], v137 offset:1024
	ds_read_b128 v[162:165], v137 offset:2048
	ds_read_b128 v[166:169], v137 offset:3072
	s_mov_b32 m0, s24
	ds_read_b128 v[170:173], v136 offset:32768
	ds_read_b128 v[174:177], v136 offset:33792
	ds_read_b128 v[178:181], v136 offset:34816
	ds_read_b128 v[182:185], v136 offset:35840
	ds_read_b128 v[186:189], v136 offset:36864
	ds_read_b128 v[190:193], v136 offset:37888
	ds_read_b128 v[194:197], v136 offset:38912
	ds_read_b128 v[198:201], v136 offset:39936
	global_load_lds_dwordx4 v240, s[54:55]
	s_mov_b32 m0, s25
	s_nop 0
	global_load_lds_dwordx4 v242, s[54:55]
	s_waitcnt lgkmcnt(0)
	s_barrier
	s_setprio 1
	s_waitcnt lgkmcnt(0)
	v_mfma_f32_16x16x32_bf16 v[124:127], v[138:141], v[170:173], v[124:127]
	v_mfma_f32_16x16x32_bf16 v[120:123], v[146:149], v[170:173], v[120:123]
	v_mfma_f32_16x16x32_bf16 v[108:111], v[138:141], v[178:181], v[108:111]
	v_mfma_f32_16x16x32_bf16 v[104:107], v[146:149], v[178:181], v[104:107]
	v_mfma_f32_16x16x32_bf16 v[92:95], v[138:141], v[186:189], v[92:95]
	v_mfma_f32_16x16x32_bf16 v[88:91], v[146:149], v[186:189], v[88:91]
	v_mfma_f32_16x16x32_bf16 v[76:79], v[138:141], v[194:197], v[76:79]
	v_mfma_f32_16x16x32_bf16 v[72:75], v[146:149], v[194:197], v[72:75]
	v_mfma_f32_16x16x32_bf16 v[124:127], v[142:145], v[174:177], v[124:127]
	v_mfma_f32_16x16x32_bf16 v[120:123], v[150:153], v[174:177], v[120:123]
	v_mfma_f32_16x16x32_bf16 v[108:111], v[142:145], v[182:185], v[108:111]
	v_mfma_f32_16x16x32_bf16 v[104:107], v[150:153], v[182:185], v[104:107]
	v_mfma_f32_16x16x32_bf16 v[92:95], v[142:145], v[190:193], v[92:95]
	v_mfma_f32_16x16x32_bf16 v[88:91], v[150:153], v[190:193], v[88:91]
	v_mfma_f32_16x16x32_bf16 v[76:79], v[142:145], v[198:201], v[76:79]
	v_mfma_f32_16x16x32_bf16 v[72:75], v[150:153], v[198:201], v[72:75]
	s_setprio 0
	s_setprio 1
	v_mfma_f32_16x16x32_bf16 v[116:119], v[154:157], v[170:173], v[116:119]
	v_mfma_f32_16x16x32_bf16 v[112:115], v[162:165], v[170:173], v[112:115]
	v_mfma_f32_16x16x32_bf16 v[100:103], v[154:157], v[178:181], v[100:103]
	v_mfma_f32_16x16x32_bf16 v[96:99], v[162:165], v[178:181], v[96:99]
	v_mfma_f32_16x16x32_bf16 v[84:87], v[154:157], v[186:189], v[84:87]
	v_mfma_f32_16x16x32_bf16 v[80:83], v[162:165], v[186:189], v[80:83]
	v_mfma_f32_16x16x32_bf16 v[68:71], v[154:157], v[194:197], v[68:71]
	v_mfma_f32_16x16x32_bf16 v[64:67], v[162:165], v[194:197], v[64:67]
	v_mfma_f32_16x16x32_bf16 v[116:119], v[158:161], v[174:177], v[116:119]
	v_mfma_f32_16x16x32_bf16 v[112:115], v[166:169], v[174:177], v[112:115]
	v_mfma_f32_16x16x32_bf16 v[100:103], v[158:161], v[182:185], v[100:103]
	v_mfma_f32_16x16x32_bf16 v[96:99], v[166:169], v[182:185], v[96:99]
	v_mfma_f32_16x16x32_bf16 v[84:87], v[158:161], v[190:193], v[84:87]
	v_mfma_f32_16x16x32_bf16 v[80:83], v[166:169], v[190:193], v[80:83]
	v_mfma_f32_16x16x32_bf16 v[68:71], v[158:161], v[198:201], v[68:71]
	v_mfma_f32_16x16x32_bf16 v[64:67], v[166:169], v[198:201], v[64:67]
	s_setprio 0
	s_waitcnt vmcnt(8)
	s_barrier
; #define G_STAGE(bufoff, gbase, voff) do { _Pragma("unroll") for (int _i = 0; _i < 2; ++_i) \
;         __builtin_amdgcn_global_load_lds((const unsigned*)((const char*)(gbase) + (voff)[_i]), (LAS unsigned*)(lds + (bufoff) + ldsw + _i * 8192), 16, 0, 0); } while (0)
; #define G_LDA(dst, b, h) do { _Pragma("unroll") for (int m = 0; m < 4; ++m) G_LD8(dst[m], lds + G_SA(b, h) + aoff + m * 2048); } while (0)
; #define G_WAIT_V(n) asm volatile("s_waitcnt vmcnt(" #n ")" ::: "memory")
; #define G_WAIT_L(n) asm volatile("s_waitcnt lgkmcnt(" #n ")" ::: "memory")
; #define G_BAR __builtin_amdgcn_s_barrier()
; #define G_SCHED __builtin_amdgcn_sched_barrier(0)
;     ...
;             G_LDA(At, 1, 1); G_STAGE(G_SB(1, 0), b02 + kstep, voffB); G_STAGE(G_SB(1, 1), b12 + kstep, voffB); G_STAGE(G_SA(1, 0), a02 + kstep, vA0);
;             G_WAIT_L(0); G_BAR; G_MMA(1, 0, At, B0); G_MMA(1, 1, At, B1); G_WAIT_V(8); G_BAR; G_SCHED;
;         }
	s_add_i32 s54, s56, s20
	v_lshl_add_u64 v[204:205], v[208:209], 0, s[36:37]
	s_mov_b32 m0, s54
	ds_read_b128 v[170:173], v136 offset:49152
	ds_read_b128 v[174:177], v136 offset:50176
	ds_read_b128 v[178:181], v136 offset:51200
	ds_read_b128 v[182:185], v136 offset:52224
	ds_read_b128 v[186:189], v136 offset:53248
	ds_read_b128 v[190:193], v136 offset:54272
	ds_read_b128 v[194:197], v136 offset:55296
	ds_read_b128 v[198:201], v136 offset:56320
	global_load_lds_dwordx4 v[204:205], off
	v_lshl_add_u64 v[204:205], v[210:211], 0, s[36:37]
	s_add_i32 m0, s54, 0x2000
	s_add_i32 s54, s57, s20
	global_load_lds_dwordx4 v[204:205], off
	v_lshl_add_u64 v[202:203], v[202:203], 0, s[36:37]
	s_mov_b32 m0, s54
	s_nop 0
	global_load_lds_dwordx4 v[202:203], off
	v_lshl_add_u64 v[202:203], v[206:207], 0, s[36:37]
	s_add_i32 m0, s54, 0x2000
	s_nop 0
	global_load_lds_dwordx4 v[202:203], off
	v_lshl_add_u64 v[202:203], v[212:213], 0, s[36:37]
	s_mov_b32 m0, s65
	s_nop 0
	global_load_lds_dwordx4 v[202:203], off
	v_lshl_add_u64 v[202:203], v[214:215], 0, s[36:37]
	s_mov_b32 m0, s66
	s_nop 0
	global_load_lds_dwordx4 v[202:203], off
	s_waitcnt lgkmcnt(0)
	s_barrier
	s_setprio 1
	s_waitcnt lgkmcnt(0)
	v_mfma_f32_16x16x32_bf16 v[60:63], v[138:141], v[170:173], v[60:63]
	v_mfma_f32_16x16x32_bf16 v[56:59], v[146:149], v[170:173], v[56:59]
	v_mfma_f32_16x16x32_bf16 v[44:47], v[138:141], v[178:181], v[44:47]
	v_mfma_f32_16x16x32_bf16 v[40:43], v[146:149], v[178:181], v[40:43]
	v_mfma_f32_16x16x32_bf16 v[28:31], v[138:141], v[186:189], v[28:31]
	v_mfma_f32_16x16x32_bf16 v[24:27], v[146:149], v[186:189], v[24:27]
	v_mfma_f32_16x16x32_bf16 v[12:15], v[138:141], v[194:197], v[12:15]
	v_mfma_f32_16x16x32_bf16 v[8:11], v[146:149], v[194:197], v[8:11]
	v_mfma_f32_16x16x32_bf16 v[60:63], v[142:145], v[174:177], v[60:63]
	v_mfma_f32_16x16x32_bf16 v[56:59], v[150:153], v[174:177], v[56:59]
	v_mfma_f32_16x16x32_bf16 v[44:47], v[142:145], v[182:185], v[44:47]
	v_mfma_f32_16x16x32_bf16 v[40:43], v[150:153], v[182:185], v[40:43]
	v_mfma_f32_16x16x32_bf16 v[28:31], v[142:145], v[190:193], v[28:31]
	v_mfma_f32_16x16x32_bf16 v[24:27], v[150:153], v[190:193], v[24:27]
	v_mfma_f32_16x16x32_bf16 v[12:15], v[142:145], v[198:201], v[12:15]
	v_mfma_f32_16x16x32_bf16 v[8:11], v[150:153], v[198:201], v[8:11]
	s_setprio 0
	s_setprio 1
	v_mfma_f32_16x16x32_bf16 v[52:55], v[154:157], v[170:173], v[52:55]
	v_mfma_f32_16x16x32_bf16 v[48:51], v[162:165], v[170:173], v[48:51]
	v_mfma_f32_16x16x32_bf16 v[36:39], v[154:157], v[178:181], v[36:39]
	v_mfma_f32_16x16x32_bf16 v[32:35], v[162:165], v[178:181], v[32:35]
	v_mfma_f32_16x16x32_bf16 v[20:23], v[154:157], v[186:189], v[20:23]
	v_mfma_f32_16x16x32_bf16 v[16:19], v[162:165], v[186:189], v[16:19]
	v_mfma_f32_16x16x32_bf16 v[4:7], v[154:157], v[194:197], v[4:7]
	v_mfma_f32_16x16x32_bf16 v[0:3], v[162:165], v[194:197], v[0:3]
	v_mfma_f32_16x16x32_bf16 v[52:55], v[158:161], v[174:177], v[52:55]
	v_mfma_f32_16x16x32_bf16 v[48:51], v[166:169], v[174:177], v[48:51]
	v_mfma_f32_16x16x32_bf16 v[36:39], v[158:161], v[182:185], v[36:39]
	v_mfma_f32_16x16x32_bf16 v[32:35], v[166:169], v[182:185], v[32:35]
	v_mfma_f32_16x16x32_bf16 v[20:23], v[158:161], v[190:193], v[20:23]
	v_mfma_f32_16x16x32_bf16 v[16:19], v[166:169], v[190:193], v[16:19]
	v_mfma_f32_16x16x32_bf16 v[4:7], v[158:161], v[198:201], v[4:7]
	v_mfma_f32_16x16x32_bf16 v[0:3], v[166:169], v[198:201], v[0:3]
	s_setprio 0
	s_waitcnt vmcnt(8)
	s_barrier
	s_add_u32 s60, s60, 0x100
	s_addc_u32 s61, s61, 0
	s_add_u32 s62, s62, 0x100
	s_addc_u32 s71, s71, 0
	s_add_u32 s72, s72, 0x100
	s_addc_u32 s73, s73, 0
	s_add_u32 s52, s52, 0x100
	s_addc_u32 s53, s53, 0
	s_cmp_ge_i32 s74, s0
	s_mov_b32 s54, s74
	s_cbranch_scc0 .LBB0_812
	v_readlane_b32 s78, v255, 11
	v_readlane_b32 s79, v255, 13
	s_and_b64 vcc, exec, s[40:41]
	s_cbranch_vccz .LBB0_815

; __device__ __forceinline__ int lane_id() { int l; asm volatile("v_mbcnt_lo_u32_b32 %0, -1, 0\n\tv_mbcnt_hi_u32_b32 %0, -1, %0" : "=v"(l)); return l; }
; #define G_STAGE(bufoff, gbase, voff) do { _Pragma("unroll") for (int _i = 0; _i < 2; ++_i) \
;         __builtin_amdgcn_global_load_lds((const unsigned*)((const char*)(gbase) + (voff)[_i]), (LAS unsigned*)(lds + (bufoff) + ldsw + _i * 8192), 16, 0, 0); } while (0)
; #define G_LDA(dst, b, h) do { _Pragma("unroll") for (int m = 0; m < 4; ++m) G_LD8(dst[m], lds + G_SA(b, h) + aoff + m * 2048); } while (0)
; #define G_LDB(dst, b, h) do { _Pragma("unroll") for (int n = 0; n < 2; ++n) G_LD8(dst[n], lds + G_SB(b, h) + boff + n * 2048); } while (0)
; #define G_SCHED __builtin_amdgcn_sched_barrier(0)
;     ...
;         for (int t = 0; t < nt; t += 2) {
;             const bool last = (t == nt - 2);
;             { const int tz_ = wid * 64 + lane_id();
; #pragma unroll
;               for (int i = 0; i < 2; ++i) { int R, C; stage_rc(tz_ * 16 + i * 8192, R, C); const int Rb = Epi::PERM ? ((R & ~31) + perm32(R & 31)) : R;
;                   voffA[i] = (unsigned)(R * S.multA * S.pitchA + C) * 2u; voffB[i] = (unsigned)(Rb * S.multB * S.pitchB + C) * 2u; } }
;             if constexpr (GATHER) asm volatile("" : "+v"(gc0[0]), "+v"(gc0[1]), "+v"(gc1[0]), "+v"(gc1[1]));
;             if constexpr (PREF) { if (t == nt - 4) S.prefetch(nxt, lds); }
;             const char* a11 = cur.a1 + (size_t)(t + 1) * kstep;
;             const char* a02 = last ? nxt.a0 : cur.a0 + (size_t)(t + 2) * kstep; const char* a12 = last ? nxt.a1 : cur.a1 + (size_t)(t + 2) * kstep;
;             const char* b02 = last ? nxt.b0 : cur.b0 + (size_t)(t + 2) * kstep; const char* b12 = last ? nxt.b1 : cur.b1 + (size_t)(t + 2) * kstep;
;             G_LDB(B0, 0, 0); G_LDB(B1, 0, 1); G_SCHED; G_LDA(At, 0, 0); G_STAGE(G_SA(1, 1), a11, vA1);
;     ...
; #pragma unroll
;         for (int a = 0; a < 2; ++a)
; #pragma unroll
;             for (int b = 0; b < 2; ++b)
; #pragma unroll
;                 for (int m = 0; m < 4; ++m)
; #pragma unroll
;                     for (int n = 0; n < 2; ++n) acc[a][b][m][n] = (acc_t){0, 0, 0, 0};
;         cur = nxt; ++ui;
.LBB0_1022:
	s_add_u32 s60, s58, 0x100
	s_addc_u32 s61, s59, 0
	s_add_u32 s62, s56, 0x100
	s_addc_u32 s74, s57, 0
	s_add_u32 s75, s54, 0x100
	s_addc_u32 s77, s55, 0
	s_add_u32 s52, s52, 0x80
	v_mov_b32_e32 v0, 0
	s_addc_u32 s53, s53, 0
	s_mov_b32 s54, 0
	v_mov_b32_e32 v1, v0
	v_mov_b32_e32 v2, v0
	v_mov_b32_e32 v3, v0
	v_mov_b32_e32 v4, v0
	v_mov_b32_e32 v5, v0
	v_mov_b32_e32 v6, v0
	v_mov_b32_e32 v7, v0
	v_mov_b32_e32 v8, v0
	v_mov_b32_e32 v9, v0
	v_mov_b32_e32 v10, v0
	v_mov_b32_e32 v11, v0
	v_mov_b32_e32 v12, v0
	v_mov_b32_e32 v13, v0
	v_mov_b32_e32 v14, v0
	v_mov_b32_e32 v15, v0
	v_mov_b32_e32 v16, v0
	v_mov_b32_e32 v17, v0
	v_mov_b32_e32 v18, v0
	v_mov_b32_e32 v19, v0
	v_mov_b32_e32 v20, v0
	v_mov_b32_e32 v21, v0
	v_mov_b32_e32 v22, v0
	v_mov_b32_e32 v23, v0
	v_mov_b32_e32 v24, v0
	v_mov_b32_e32 v25, v0
	v_mov_b32_e32 v26, v0
	v_mov_b32_e32 v27, v0
	v_mov_b32_e32 v28, v0
	v_mov_b32_e32 v29, v0
	v_mov_b32_e32 v30, v0
	v_mov_b32_e32 v31, v0
	v_mov_b32_e32 v32, v0
	v_mov_b32_e32 v33, v0
	v_mov_b32_e32 v34, v0
	v_mov_b32_e32 v35, v0
	v_mov_b32_e32 v36, v0
	v_mov_b32_e32 v37, v0
	v_mov_b32_e32 v38, v0
	v_mov_b32_e32 v39, v0
	v_mov_b32_e32 v40, v0
	v_mov_b32_e32 v41, v0
	v_mov_b32_e32 v42, v0
	v_mov_b32_e32 v43, v0
	v_mov_b32_e32 v44, v0
	v_mov_b32_e32 v45, v0
	v_mov_b32_e32 v46, v0
	v_mov_b32_e32 v47, v0
	v_mov_b32_e32 v48, v0
	v_mov_b32_e32 v49, v0
	v_mov_b32_e32 v50, v0
	v_mov_b32_e32 v51, v0
	v_mov_b32_e32 v52, v0
	v_mov_b32_e32 v53, v0
	v_mov_b32_e32 v54, v0
	v_mov_b32_e32 v55, v0
	v_mov_b32_e32 v56, v0
	v_mov_b32_e32 v57, v0
	v_mov_b32_e32 v58, v0
	v_mov_b32_e32 v59, v0
	v_mov_b32_e32 v60, v0
	v_mov_b32_e32 v61, v0
	v_mov_b32_e32 v62, v0
	v_mov_b32_e32 v63, v0
	v_mbcnt_lo_u32_b32 v248, -1, 0
	v_mbcnt_hi_u32_b32 v248, -1, v248
	v_mov_b32_e32 v249, s88
	v_lshrrev_b32_e32 v249, 6, v249
	v_and_b32_e32 v250, 3, v248
	v_lshlrev_b32_e32 v250, 4, v250
	v_and_b32_e32 v251, 32, v248
	v_xor_b32_e32 v250, v250, v251
	v_and_b32_e32 v251, 1, v249
	v_lshl_add_u32 v250, v251, 6, v250
	v_lshrrev_b32_e32 v251, 1, v249
	v_lshrrev_b32_e32 v252, 2, v248
	v_lshl_add_u32 v251, v251, 4, v252
	v_mov_b32_e32 v253, 0x200
	v_mad_u32_u24 v240, v251, v253, v250
	v_add_u32_e32 v242, 0x8000, v240
	v_lshrrev_b32_e32 v251, 2, v249
	v_lshlrev_b32_e32 v251, 5, v251
	v_lshrrev_b32_e32 v252, 4, v248
	v_lshl_add_u32 v251, v252, 3, v251
	v_bfe_u32 v252, v249, 1, 1
	v_lshl_add_u32 v251, v252, 2, v251
	v_bfe_u32 v252, v248, 2, 2
	v_add_u32_e32 v251, v251, v252
	v_mov_b32_e32 v253, 0x200
	v_mad_u32_u24 v244, v251, v253, v250
	v_add_u32_e32 v246, 0x8000, v244
	v_mov_b32_e32 v241, 0
	v_mov_b32_e32 v243, 0
	v_mov_b32_e32 v245, 0
	v_mov_b32_e32 v247, 0
.LBB0_1023:
	s_add_i32 s78, s54, 2
	ds_read_b128 v[72:75], v70
	ds_read_b128 v[76:79], v70 offset:1024
	ds_read_b128 v[80:83], v70 offset:2048
	ds_read_b128 v[84:87], v70 offset:3072
	s_add_u32 s79, s52, 0x80
	s_addc_u32 s55, s53, 0
	s_add_i32 s81, s73, s20
	s_add_i32 m0, s23, 0xc000
	s_add_i32 s80, s23, 0xe000
	s_add_i32 s82, s81, 0x2000
	s_cmp_eq_u32 s72, s54
	s_cselect_b32 s54, s44, s79
	s_cselect_b32 s57, s43, s77
	s_cselect_b32 s56, s42, s75
	s_cselect_b32 s59, s49, s61
	s_cselect_b32 s58, s48, s60
	s_cselect_b32 s55, s45, s55
	ds_read_b128 v[88:91], v71
	ds_read_b128 v[92:95], v71 offset:1024
	ds_read_b128 v[96:99], v71 offset:2048
	ds_read_b128 v[100:103], v71 offset:3072
	ds_read_b128 v[104:107], v71 offset:4096
	ds_read_b128 v[108:111], v71 offset:5120
	ds_read_b128 v[112:115], v71 offset:6144
	ds_read_b128 v[116:119], v71 offset:7168
	global_load_lds_dwordx4 v240, s[52:53]
	s_mov_b32 m0, s80
	v_mov_b32_e32 v123, v65
	global_load_lds_dwordx4 v242, s[52:53]
	s_waitcnt lgkmcnt(0)
	s_barrier
	s_setprio 1
	s_waitcnt lgkmcnt(0)
	v_mfma_f32_16x16x32_bf16 v[60:63], v[72:75], v[88:91], v[60:63]
	v_mfma_f32_16x16x32_bf16 v[56:59], v[80:83], v[88:91], v[56:59]
	v_mfma_f32_16x16x32_bf16 v[52:55], v[72:75], v[96:99], v[52:55]
	v_mfma_f32_16x16x32_bf16 v[48:51], v[80:83], v[96:99], v[48:51]
	v_mfma_f32_16x16x32_bf16 v[44:47], v[72:75], v[104:107], v[44:47]
	v_mfma_f32_16x16x32_bf16 v[40:43], v[80:83], v[104:107], v[40:43]
	v_mfma_f32_16x16x32_bf16 v[36:39], v[72:75], v[112:115], v[36:39]
	v_mfma_f32_16x16x32_bf16 v[32:35], v[80:83], v[112:115], v[32:35]
	v_mfma_f32_16x16x32_bf16 v[60:63], v[76:79], v[92:95], v[60:63]
	v_mfma_f32_16x16x32_bf16 v[56:59], v[84:87], v[92:95], v[56:59]
	v_mfma_f32_16x16x32_bf16 v[52:55], v[76:79], v[100:103], v[52:55]
	v_mfma_f32_16x16x32_bf16 v[48:51], v[84:87], v[100:103], v[48:51]
	v_mfma_f32_16x16x32_bf16 v[44:47], v[76:79], v[108:111], v[44:47]
	v_mfma_f32_16x16x32_bf16 v[40:43], v[84:87], v[108:111], v[40:43]
	v_mfma_f32_16x16x32_bf16 v[36:39], v[76:79], v[116:119], v[36:39]
	v_mfma_f32_16x16x32_bf16 v[32:35], v[84:87], v[116:119], v[32:35]
	s_setprio 0
	s_setprio 1
	s_setprio 0
	s_waitcnt vmcnt(8)
	s_barrier
	s_mov_b32 m0, s81
	ds_read_b128 v[88:91], v71 offset:16384
	ds_read_b128 v[92:95], v71 offset:17408
	ds_read_b128 v[96:99], v71 offset:18432
	ds_read_b128 v[100:103], v71 offset:19456
	ds_read_b128 v[104:107], v71 offset:20480
	ds_read_b128 v[108:111], v71 offset:21504
	ds_read_b128 v[112:115], v71 offset:22528
	ds_read_b128 v[116:119], v71 offset:23552
	global_load_lds_dwordx4 v244, s[58:59]
	s_mov_b32 m0, s82
	s_cselect_b32 s81, s47, s74
	global_load_lds_dwordx4 v246, s[58:59]
	s_cselect_b32 s80, s46, s62
	s_mov_b32 m0, s24
	v_mov_b32_e32 v121, v65
	global_load_lds_dwordx4 v244, s[80:81]
	s_mov_b32 m0, s25
	v_mov_b32_e32 v125, v65
	global_load_lds_dwordx4 v246, s[80:81]
	s_mov_b32 m0, s23
	v_lshl_add_u64 v[126:127], s[58:59], 0, v[244:245]
	global_load_lds_dwordx4 v240, s[56:57]
	s_mov_b32 m0, s27
	v_lshl_add_u64 v[128:129], s[58:59], 0, v[246:247]
	global_load_lds_dwordx4 v242, s[56:57]
	s_waitcnt lgkmcnt(0)
	v_lshl_add_u64 v[120:121], s[80:81], 0, v[244:245]
	v_lshl_add_u64 v[124:125], s[80:81], 0, v[246:247]
	v_lshl_add_u64 v[130:131], s[56:57], 0, v[240:241]
	v_lshl_add_u64 v[132:133], s[56:57], 0, v[242:243]
	s_barrier
; #define G_STAGE(bufoff, gbase, voff) do { _Pragma("unroll") for (int _i = 0; _i < 2; ++_i) \
;         __builtin_amdgcn_global_load_lds((const unsigned*)((const char*)(gbase) + (voff)[_i]), (LAS unsigned*)(lds + (bufoff) + ldsw + _i * 8192), 16, 0, 0); } while (0)
; #define G_LDA(dst, b, h) do { _Pragma("unroll") for (int m = 0; m < 4; ++m) G_LD8(dst[m], lds + G_SA(b, h) + aoff + m * 2048); } while (0)
; #define G_LDB(dst, b, h) do { _Pragma("unroll") for (int n = 0; n < 2; ++n) G_LD8(dst[n], lds + G_SB(b, h) + boff + n * 2048); } while (0)
; #define G_WAIT_V(n) asm volatile("s_waitcnt vmcnt(" #n ")" ::: "memory")
; #define G_WAIT_L(n) asm volatile("s_waitcnt lgkmcnt(" #n ")" ::: "memory")
; #define G_BAR __builtin_amdgcn_s_barrier()
; #define G_SCHED __builtin_amdgcn_sched_barrier(0)
;     ...
;             G_WAIT_L(0); G_BAR; G_MMA(1, 0, At, B0); G_MMA(1, 1, At, B1); G_WAIT_V(8); G_BAR; G_SCHED;
;             G_LDB(B0, 1, 0); G_LDB(B1, 1, 1); G_SCHED; G_LDA(At, 1, 0); G_STAGE(G_SA(0, 1), a12, vA1);
;             G_WAIT_L(0); G_BAR; G_MMA(0, 0, At, B0); G_MMA(0, 1, At, B1); G_WAIT_V(8); G_BAR; G_SCHED;
;             G_LDA(At, 1, 1); G_STAGE(G_SB(1, 0), b02 + kstep, voffB); G_STAGE(G_SB(1, 1), b12 + kstep, voffB); G_STAGE(G_SA(1, 0), a02 + kstep, vA0);
;             G_WAIT_L(0); G_BAR; G_MMA(1, 0, At, B0); G_MMA(1, 1, At, B1); G_WAIT_V(8); G_BAR; G_SCHED;
	s_setprio 1
	s_waitcnt lgkmcnt(0)
	v_mfma_f32_16x16x32_bf16 v[28:31], v[72:75], v[88:91], v[28:31]
	v_mfma_f32_16x16x32_bf16 v[24:27], v[80:83], v[88:91], v[24:27]
	v_mfma_f32_16x16x32_bf16 v[20:23], v[72:75], v[96:99], v[20:23]
	v_mfma_f32_16x16x32_bf16 v[16:19], v[80:83], v[96:99], v[16:19]
	v_mfma_f32_16x16x32_bf16 v[12:15], v[72:75], v[104:107], v[12:15]
	v_mfma_f32_16x16x32_bf16 v[8:11], v[80:83], v[104:107], v[8:11]
	v_mfma_f32_16x16x32_bf16 v[4:7], v[72:75], v[112:115], v[4:7]
	v_mfma_f32_16x16x32_bf16 v[0:3], v[80:83], v[112:115], v[0:3]
	v_mfma_f32_16x16x32_bf16 v[28:31], v[76:79], v[92:95], v[28:31]
	v_mfma_f32_16x16x32_bf16 v[24:27], v[84:87], v[92:95], v[24:27]
	v_mfma_f32_16x16x32_bf16 v[20:23], v[76:79], v[100:103], v[20:23]
	v_mfma_f32_16x16x32_bf16 v[16:19], v[84:87], v[100:103], v[16:19]
	v_mfma_f32_16x16x32_bf16 v[12:15], v[76:79], v[108:111], v[12:15]
	v_mfma_f32_16x16x32_bf16 v[8:11], v[84:87], v[108:111], v[8:11]
	v_mfma_f32_16x16x32_bf16 v[4:7], v[76:79], v[116:119], v[4:7]
	v_mfma_f32_16x16x32_bf16 v[0:3], v[84:87], v[116:119], v[0:3]
	s_setprio 0
	s_setprio 1
	s_setprio 0
	s_waitcnt vmcnt(8)
	s_barrier
	s_add_i32 s56, 0, 0x18000
	v_add_u32_e32 v84, s56, v69
	ds_read_b128 v[72:75], v84
	ds_read_b128 v[76:79], v84 offset:1024
	ds_read_b128 v[80:83], v84 offset:2048
	ds_read_b128 v[84:87], v84 offset:3072
	s_mov_b32 m0, s33
	ds_read_b128 v[88:91], v71 offset:32768
	ds_read_b128 v[92:95], v71 offset:33792
	ds_read_b128 v[96:99], v71 offset:34816
	ds_read_b128 v[100:103], v71 offset:35840
	ds_read_b128 v[104:107], v71 offset:36864
	ds_read_b128 v[108:111], v71 offset:37888
	ds_read_b128 v[112:115], v71 offset:38912
	ds_read_b128 v[116:119], v71 offset:39936
	global_load_lds_dwordx4 v240, s[54:55]
	s_mov_b32 m0, s41
	s_nop 0
	global_load_lds_dwordx4 v242, s[54:55]
	s_waitcnt lgkmcnt(0)
	s_barrier
	s_setprio 1
	s_waitcnt lgkmcnt(0)
	v_mfma_f32_16x16x32_bf16 v[60:63], v[72:75], v[88:91], v[60:63]
	v_mfma_f32_16x16x32_bf16 v[56:59], v[80:83], v[88:91], v[56:59]
	v_mfma_f32_16x16x32_bf16 v[52:55], v[72:75], v[96:99], v[52:55]
	v_mfma_f32_16x16x32_bf16 v[48:51], v[80:83], v[96:99], v[48:51]
	v_mfma_f32_16x16x32_bf16 v[44:47], v[72:75], v[104:107], v[44:47]
	v_mfma_f32_16x16x32_bf16 v[40:43], v[80:83], v[104:107], v[40:43]
	v_mfma_f32_16x16x32_bf16 v[36:39], v[72:75], v[112:115], v[36:39]
	v_mfma_f32_16x16x32_bf16 v[32:35], v[80:83], v[112:115], v[32:35]
	v_mfma_f32_16x16x32_bf16 v[60:63], v[76:79], v[92:95], v[60:63]
	v_mfma_f32_16x16x32_bf16 v[56:59], v[84:87], v[92:95], v[56:59]
	v_mfma_f32_16x16x32_bf16 v[52:55], v[76:79], v[100:103], v[52:55]
	v_mfma_f32_16x16x32_bf16 v[48:51], v[84:87], v[100:103], v[48:51]
	v_mfma_f32_16x16x32_bf16 v[44:47], v[76:79], v[108:111], v[44:47]
	v_mfma_f32_16x16x32_bf16 v[40:43], v[84:87], v[108:111], v[40:43]
	v_mfma_f32_16x16x32_bf16 v[36:39], v[76:79], v[116:119], v[36:39]
	v_mfma_f32_16x16x32_bf16 v[32:35], v[84:87], v[116:119], v[32:35]
	s_setprio 0
	s_setprio 1
	s_setprio 0
	s_waitcnt vmcnt(8)
	s_barrier
	s_add_i32 s54, s56, s20
	v_lshl_add_u64 v[122:123], v[126:127], 0, s[36:37]
	s_mov_b32 m0, s54
	ds_read_b128 v[88:91], v71 offset:49152
	ds_read_b128 v[92:95], v71 offset:50176
	ds_read_b128 v[96:99], v71 offset:51200
	ds_read_b128 v[100:103], v71 offset:52224
	ds_read_b128 v[104:107], v71 offset:53248
	ds_read_b128 v[108:111], v71 offset:54272
	ds_read_b128 v[112:115], v71 offset:55296
	ds_read_b128 v[116:119], v71 offset:56320
	global_load_lds_dwordx4 v[122:123], off
	v_lshl_add_u64 v[122:123], v[128:129], 0, s[36:37]
	s_add_i32 m0, s54, 0x2000
	v_lshl_add_u64 v[120:121], v[120:121], 0, s[36:37]
	global_load_lds_dwordx4 v[122:123], off
	s_mov_b32 m0, s69
	s_nop 0
	global_load_lds_dwordx4 v[120:121], off
	v_lshl_add_u64 v[120:121], v[124:125], 0, s[36:37]
	s_mov_b32 m0, s71
	s_nop 0
	global_load_lds_dwordx4 v[120:121], off
	v_lshl_add_u64 v[120:121], v[130:131], 0, s[36:37]
	s_mov_b32 m0, s66
	s_nop 0
	global_load_lds_dwordx4 v[120:121], off
	v_lshl_add_u64 v[120:121], v[132:133], 0, s[36:37]
	s_mov_b32 m0, s67
	s_nop 0
	global_load_lds_dwordx4 v[120:121], off
	s_waitcnt lgkmcnt(0)
	s_barrier
; #define GAS __attribute__((address_space(1)))
; #define LAS __attribute__((address_space(3)))
; __device__ __forceinline__ v4u pack8(const f32x4 a, const f32x4 b) { v4u w; w.x = cvt_pk_bf16(a[0], a[1]); w.y = cvt_pk_bf16(a[2], a[3]); w.z = cvt_pk_bf16(b[0], b[1]); w.w = cvt_pk_bf16(b[2], b[3]); return w; }
; #define G_STAGE(bufoff, gbase, voff) do { _Pragma("unroll") for (int _i = 0; _i < 2; ++_i) \
;         __builtin_amdgcn_global_load_lds((const unsigned*)((const char*)(gbase) + (voff)[_i]), (LAS unsigned*)(lds + (bufoff) + ldsw + _i * 8192), 16, 0, 0); } while (0)
; #define G_LDA(dst, b, h) do { _Pragma("unroll") for (int m = 0; m < 4; ++m) G_LD8(dst[m], lds + G_SA(b, h) + aoff + m * 2048); } while (0)
; #define G_WAIT_V(n) asm volatile("s_waitcnt vmcnt(" #n ")" ::: "memory")
; #define G_WAIT_L(n) asm volatile("s_waitcnt lgkmcnt(" #n ")" ::: "memory")
; #define G_BAR __builtin_amdgcn_s_barrier()
; #define G_SCHED __builtin_amdgcn_sched_barrier(0)
; #define EPI_LOOP_AM for (int ai = 0; ai < 2; ++ai) _Pragma("unroll") for (int m = 0; m < 4; ++m)
;     ...
;             G_WAIT_L(0); G_BAR; G_MMA(0, 0, At, B0); G_MMA(0, 1, At, B1); G_WAIT_V(8); G_BAR; G_SCHED;
;             G_LDA(At, 1, 1); G_STAGE(G_SB(1, 0), b02 + kstep, voffB); G_STAGE(G_SB(1, 1), b12 + kstep, voffB); G_STAGE(G_SA(1, 0), a02 + kstep, vA0);
;             G_WAIT_L(0); G_BAR; G_MMA(1, 0, At, B0); G_MMA(1, 1, At, B1); G_WAIT_V(8); G_BAR; G_SCHED;
;         }
;     __device__ __forceinline__ void operator()(Acc& acc, const Unit& u, LAS unsigned char*, int wr, int wc, int fr, int fq) const {
;         const int l0 = wc * 32 + 8 * fq; const float norm = 6.9053396600248786e-4f;
; #pragma unroll
;         EPI_LOOP_AM { const int R = u.p0 * 256 + 128 * ai + 64 * wr + 16 * m + fr, k = R >> 3, g = R & 7;
;             *(GAS v4u*)(y + (size_t)k * D + g * 128 + l0) = pack8(acc[ai][0][m][0] * norm, acc[ai][0][m][1] * norm); }
	s_setprio 1
	s_waitcnt lgkmcnt(0)
	v_mfma_f32_16x16x32_bf16 v[28:31], v[72:75], v[88:91], v[28:31]
	v_mfma_f32_16x16x32_bf16 v[24:27], v[80:83], v[88:91], v[24:27]
	v_mfma_f32_16x16x32_bf16 v[20:23], v[72:75], v[96:99], v[20:23]
	v_mfma_f32_16x16x32_bf16 v[16:19], v[80:83], v[96:99], v[16:19]
	v_mfma_f32_16x16x32_bf16 v[12:15], v[72:75], v[104:107], v[12:15]
	v_mfma_f32_16x16x32_bf16 v[8:11], v[80:83], v[104:107], v[8:11]
	v_mfma_f32_16x16x32_bf16 v[4:7], v[72:75], v[112:115], v[4:7]
	v_mfma_f32_16x16x32_bf16 v[0:3], v[80:83], v[112:115], v[0:3]
	v_mfma_f32_16x16x32_bf16 v[28:31], v[76:79], v[92:95], v[28:31]
	v_mfma_f32_16x16x32_bf16 v[24:27], v[84:87], v[92:95], v[24:27]
	v_mfma_f32_16x16x32_bf16 v[20:23], v[76:79], v[100:103], v[20:23]
	v_mfma_f32_16x16x32_bf16 v[16:19], v[84:87], v[100:103], v[16:19]
	v_mfma_f32_16x16x32_bf16 v[12:15], v[76:79], v[108:111], v[12:15]
	v_mfma_f32_16x16x32_bf16 v[8:11], v[84:87], v[108:111], v[8:11]
	v_mfma_f32_16x16x32_bf16 v[4:7], v[76:79], v[116:119], v[4:7]
	v_mfma_f32_16x16x32_bf16 v[0:3], v[84:87], v[116:119], v[0:3]
	s_setprio 0
	s_setprio 1
	s_setprio 0
	s_waitcnt vmcnt(8)
	s_barrier
	s_add_u32 s60, s60, 0x100
	s_addc_u32 s61, s61, 0
	s_add_u32 s62, s62, 0x100
	s_addc_u32 s74, s74, 0
	s_add_u32 s75, s75, 0x100
	s_addc_u32 s77, s77, 0
	s_add_u32 s52, s52, 0x100
	s_addc_u32 s53, s53, 0
	s_cmp_ge_i32 s78, s0
	s_mov_b32 s54, s78
	s_cbranch_scc0 .LBB0_1023
	v_pk_mul_f32 v[62:63], v[62:63], s[40:41] op_sel_hi:[1,0]
	v_pk_mul_f32 v[60:61], v[60:61], s[40:41] op_sel_hi:[1,0]
	v_pk_mul_f32 v[58:59], v[58:59], s[40:41] op_sel_hi:[1,0]
	v_pk_mul_f32 v[56:57], v[56:57], s[40:41] op_sel_hi:[1,0]
	v_pk_mul_f32 v[54:55], v[54:55], s[40:41] op_sel_hi:[1,0]
	v_pk_mul_f32 v[52:53], v[52:53], s[40:41] op_sel_hi:[1,0]
	v_pk_mul_f32 v[50:51], v[50:51], s[40:41] op_sel_hi:[1,0]
	v_pk_mul_f32 v[48:49], v[48:49], s[40:41] op_sel_hi:[1,0]
	v_pk_mul_f32 v[46:47], v[46:47], s[40:41] op_sel_hi:[1,0]
	v_pk_mul_f32 v[44:45], v[44:45], s[40:41] op_sel_hi:[1,0]
	v_pk_mul_f32 v[42:43], v[42:43], s[40:41] op_sel_hi:[1,0]
	v_pk_mul_f32 v[40:41], v[40:41], s[40:41] op_sel_hi:[1,0]
	v_pk_mul_f32 v[38:39], v[38:39], s[40:41] op_sel_hi:[1,0]
	v_pk_mul_f32 v[36:37], v[36:37], s[40:41] op_sel_hi:[1,0]
	v_pk_mul_f32 v[34:35], v[34:35], s[40:41] op_sel_hi:[1,0]
	v_pk_mul_f32 v[32:33], v[32:33], s[40:41] op_sel_hi:[1,0]
	v_pk_mul_f32 v[30:31], v[30:31], s[40:41] op_sel_hi:[1,0]
	v_pk_mul_f32 v[28:29], v[28:29], s[40:41] op_sel_hi:[1,0]
	v_pk_mul_f32 v[26:27], v[26:27], s[40:41] op_sel_hi:[1,0]
	v_pk_mul_f32 v[24:25], v[24:25], s[40:41] op_sel_hi:[1,0]
	v_pk_mul_f32 v[22:23], v[22:23], s[40:41] op_sel_hi:[1,0]
	v_pk_mul_f32 v[20:21], v[20:21], s[40:41] op_sel_hi:[1,0]
	v_pk_mul_f32 v[18:19], v[18:19], s[40:41] op_sel_hi:[1,0]
	v_pk_mul_f32 v[16:17], v[16:17], s[40:41] op_sel_hi:[1,0]
	v_pk_mul_f32 v[14:15], v[14:15], s[40:41] op_sel_hi:[1,0]
	v_pk_mul_f32 v[12:13], v[12:13], s[40:41] op_sel_hi:[1,0]
	v_pk_mul_f32 v[10:11], v[10:11], s[40:41] op_sel_hi:[1,0]
	v_pk_mul_f32 v[8:9], v[8:9], s[40:41] op_sel_hi:[1,0]
	v_pk_mul_f32 v[6:7], v[6:7], s[40:41] op_sel_hi:[1,0]
	v_pk_mul_f32 v[4:5], v[4:5], s[40:41] op_sel_hi:[1,0]
	v_pk_mul_f32 v[2:3], v[2:3], s[40:41] op_sel_hi:[1,0]
	v_pk_mul_f32 v[0:1], v[0:1], s[40:41] op_sel_hi:[1,0]
	v_readlane_b32 s78, v255, 11
	v_readlane_b32 s79, v255, 13
	s_and_b64 vcc, exec, s[38:39]
	s_cbranch_vccz .LBB0_1026

; __device__ __forceinline__ int lane_id() { int l; asm volatile("v_mbcnt_lo_u32_b32 %0, -1, 0\n\tv_mbcnt_hi_u32_b32 %0, -1, %0" : "=v"(l)); return l; }
; #define G_STAGE(bufoff, gbase, voff) do { _Pragma("unroll") for (int _i = 0; _i < 2; ++_i) \
;         __builtin_amdgcn_global_load_lds((const unsigned*)((const char*)(gbase) + (voff)[_i]), (LAS unsigned*)(lds + (bufoff) + ldsw + _i * 8192), 16, 0, 0); } while (0)
; #define G_LDA(dst, b, h) do { _Pragma("unroll") for (int m = 0; m < 4; ++m) G_LD8(dst[m], lds + G_SA(b, h) + aoff + m * 2048); } while (0)
; #define G_LDB(dst, b, h) do { _Pragma("unroll") for (int n = 0; n < 2; ++n) G_LD8(dst[n], lds + G_SB(b, h) + boff + n * 2048); } while (0)
; #define G_SCHED __builtin_amdgcn_sched_barrier(0)
;     ...
;         for (int t = 0; t < nt; t += 2) {
;             const bool last = (t == nt - 2);
;             { const int tz_ = wid * 64 + lane_id();
; #pragma unroll
;               for (int i = 0; i < 2; ++i) { int R, C; stage_rc(tz_ * 16 + i * 8192, R, C); const int Rb = Epi::PERM ? ((R & ~31) + perm32(R & 31)) : R;
;                   voffA[i] = (unsigned)(R * S.multA * S.pitchA + C) * 2u; voffB[i] = (unsigned)(Rb * S.multB * S.pitchB + C) * 2u; } }
;             if constexpr (GATHER) asm volatile("" : "+v"(gc0[0]), "+v"(gc0[1]), "+v"(gc1[0]), "+v"(gc1[1]));
;             if constexpr (PREF) { if (t == nt - 4) S.prefetch(nxt, lds); }
;             const char* a11 = cur.a1 + (size_t)(t + 1) * kstep;
;             const char* a02 = last ? nxt.a0 : cur.a0 + (size_t)(t + 2) * kstep; const char* a12 = last ? nxt.a1 : cur.a1 + (size_t)(t + 2) * kstep;
;             const char* b02 = last ? nxt.b0 : cur.b0 + (size_t)(t + 2) * kstep; const char* b12 = last ? nxt.b1 : cur.b1 + (size_t)(t + 2) * kstep;
;             G_LDB(B0, 0, 0); G_LDB(B1, 0, 1); G_SCHED; G_LDA(At, 0, 0); G_STAGE(G_SA(1, 1), a11, vA1);
;     ...
; #pragma unroll
;         for (int a = 0; a < 2; ++a)
; #pragma unroll
;             for (int b = 0; b < 2; ++b)
; #pragma unroll
;                 for (int m = 0; m < 4; ++m)
; #pragma unroll
;                     for (int n = 0; n < 2; ++n) acc[a][b][m][n] = (acc_t){0, 0, 0, 0};
;         cur = nxt; ++ui;
.LBB0_1057:
	s_add_u32 s5, s58, 0x100
	s_addc_u32 s41, s59, 0
	s_add_u32 s60, s56, 0x100
	s_addc_u32 s61, s57, 0
	s_add_u32 s77, s54, 0x100
	s_addc_u32 s78, s55, 0
	s_add_u32 s52, s52, 0x80
	v_mov_b32_e32 v0, 0
	s_addc_u32 s53, s53, 0
	s_mov_b32 s54, 0
	v_mov_b32_e32 v1, v0
	v_mov_b32_e32 v2, v0
	v_mov_b32_e32 v3, v0
	v_mov_b32_e32 v4, v0
	v_mov_b32_e32 v5, v0
	v_mov_b32_e32 v6, v0
	v_mov_b32_e32 v7, v0
	v_mov_b32_e32 v16, v0
	v_mov_b32_e32 v17, v0
	v_mov_b32_e32 v18, v0
	v_mov_b32_e32 v19, v0
	v_mov_b32_e32 v20, v0
	v_mov_b32_e32 v21, v0
	v_mov_b32_e32 v22, v0
	v_mov_b32_e32 v23, v0
	v_mov_b32_e32 v32, v0
	v_mov_b32_e32 v33, v0
	v_mov_b32_e32 v34, v0
	v_mov_b32_e32 v35, v0
	v_mov_b32_e32 v36, v0
	v_mov_b32_e32 v37, v0
	v_mov_b32_e32 v38, v0
	v_mov_b32_e32 v39, v0
	v_mov_b32_e32 v48, v0
	v_mov_b32_e32 v49, v0
	v_mov_b32_e32 v50, v0
	v_mov_b32_e32 v51, v0
	v_mov_b32_e32 v52, v0
	v_mov_b32_e32 v53, v0
	v_mov_b32_e32 v54, v0
	v_mov_b32_e32 v55, v0
	v_mov_b32_e32 v8, v0
	v_mov_b32_e32 v9, v0
	v_mov_b32_e32 v10, v0
	v_mov_b32_e32 v11, v0
	v_mov_b32_e32 v12, v0
	v_mov_b32_e32 v13, v0
	v_mov_b32_e32 v14, v0
	v_mov_b32_e32 v15, v0
	v_mov_b32_e32 v24, v0
	v_mov_b32_e32 v25, v0
	v_mov_b32_e32 v26, v0
	v_mov_b32_e32 v27, v0
	v_mov_b32_e32 v28, v0
	v_mov_b32_e32 v29, v0
	v_mov_b32_e32 v30, v0
	v_mov_b32_e32 v31, v0
	v_mov_b32_e32 v40, v0
	v_mov_b32_e32 v41, v0
	v_mov_b32_e32 v42, v0
	v_mov_b32_e32 v43, v0
	v_mov_b32_e32 v44, v0
	v_mov_b32_e32 v45, v0
	v_mov_b32_e32 v46, v0
	v_mov_b32_e32 v47, v0
	v_mov_b32_e32 v56, v0
	v_mov_b32_e32 v57, v0
	v_mov_b32_e32 v58, v0
	v_mov_b32_e32 v59, v0
	v_mov_b32_e32 v60, v0
	v_mov_b32_e32 v61, v0
	v_mov_b32_e32 v62, v0
	v_mov_b32_e32 v63, v0
	v_mov_b32_e32 v64, v0
	v_mov_b32_e32 v65, v0
	v_mov_b32_e32 v66, v0
	v_mov_b32_e32 v67, v0
	v_mov_b32_e32 v68, v0
	v_mov_b32_e32 v69, v0
	v_mov_b32_e32 v70, v0
	v_mov_b32_e32 v71, v0
	v_mov_b32_e32 v80, v0
	v_mov_b32_e32 v81, v0
	v_mov_b32_e32 v82, v0
	v_mov_b32_e32 v83, v0
	v_mov_b32_e32 v84, v0
	v_mov_b32_e32 v85, v0
	v_mov_b32_e32 v86, v0
	v_mov_b32_e32 v87, v0
	v_mov_b32_e32 v96, v0
	v_mov_b32_e32 v97, v0
	v_mov_b32_e32 v98, v0
	v_mov_b32_e32 v99, v0
	v_mov_b32_e32 v100, v0
	v_mov_b32_e32 v101, v0
	v_mov_b32_e32 v102, v0
	v_mov_b32_e32 v103, v0
	v_mov_b32_e32 v112, v0
	v_mov_b32_e32 v113, v0
	v_mov_b32_e32 v114, v0
	v_mov_b32_e32 v115, v0
	v_mov_b32_e32 v116, v0
	v_mov_b32_e32 v117, v0
	v_mov_b32_e32 v118, v0
	v_mov_b32_e32 v119, v0
	v_mov_b32_e32 v72, v0
	v_mov_b32_e32 v73, v0
	v_mov_b32_e32 v74, v0
	v_mov_b32_e32 v75, v0
	v_mov_b32_e32 v76, v0
	v_mov_b32_e32 v77, v0
	v_mov_b32_e32 v78, v0
	v_mov_b32_e32 v79, v0
	v_mov_b32_e32 v88, v0
	v_mov_b32_e32 v89, v0
	v_mov_b32_e32 v90, v0
	v_mov_b32_e32 v91, v0
	v_mov_b32_e32 v92, v0
	v_mov_b32_e32 v93, v0
	v_mov_b32_e32 v94, v0
	v_mov_b32_e32 v95, v0
	v_mov_b32_e32 v104, v0
	v_mov_b32_e32 v105, v0
	v_mov_b32_e32 v106, v0
	v_mov_b32_e32 v107, v0
	v_mov_b32_e32 v108, v0
	v_mov_b32_e32 v109, v0
	v_mov_b32_e32 v110, v0
	v_mov_b32_e32 v111, v0
	v_mov_b32_e32 v120, v0
	v_mov_b32_e32 v121, v0
	v_mov_b32_e32 v122, v0
	v_mov_b32_e32 v123, v0
	v_mov_b32_e32 v124, v0
	v_mov_b32_e32 v125, v0
	v_mov_b32_e32 v126, v0
	v_mov_b32_e32 v127, v0
	v_mbcnt_lo_u32_b32 v248, -1, 0
	v_mbcnt_hi_u32_b32 v248, -1, v248
	v_mov_b32_e32 v249, s88
	v_lshrrev_b32_e32 v249, 6, v249
	v_and_b32_e32 v250, 3, v248
	v_lshlrev_b32_e32 v250, 4, v250
	v_and_b32_e32 v251, 32, v248
	v_xor_b32_e32 v250, v250, v251
	v_and_b32_e32 v251, 1, v249
	v_lshl_add_u32 v250, v251, 6, v250
	v_lshrrev_b32_e32 v251, 1, v249
	v_lshrrev_b32_e32 v252, 2, v248
	v_lshl_add_u32 v251, v251, 4, v252
	v_mov_b32_e32 v253, 0x600
	v_mad_u32_u24 v240, v251, v253, v250
	v_add_u32_e32 v242, 0x18000, v240
	v_lshrrev_b32_e32 v251, 2, v249
	v_lshlrev_b32_e32 v251, 5, v251
	v_lshrrev_b32_e32 v252, 4, v248
	v_lshl_add_u32 v251, v252, 3, v251
	v_bfe_u32 v252, v249, 1, 1
	v_lshl_add_u32 v251, v252, 2, v251
	v_bfe_u32 v252, v248, 2, 2
	v_add_u32_e32 v251, v251, v252
	v_mov_b32_e32 v253, 0x600
	v_mad_u32_u24 v244, v251, v253, v250
	v_add_u32_e32 v246, 0x18000, v244
	v_mov_b32_e32 v241, 0
	v_mov_b32_e32 v243, 0
	v_mov_b32_e32 v245, 0
	v_mov_b32_e32 v247, 0
.LBB0_1058:
	s_add_i32 s79, s54, 2
	ds_read_b128 v[130:133], v138
	ds_read_b128 v[144:147], v138 offset:1024
	ds_read_b128 v[148:151], v138 offset:2048
	ds_read_b128 v[152:155], v138 offset:3072
	ds_read_b128 v[156:159], v139
	ds_read_b128 v[160:163], v139 offset:1024
	ds_read_b128 v[164:167], v139 offset:2048
	ds_read_b128 v[168:171], v139 offset:3072
	s_add_u32 s80, s52, 0x80
	s_addc_u32 s55, s53, 0
	s_add_i32 s83, s71, s20
	s_add_i32 m0, s33, 0xc000
	s_add_i32 s82, s33, 0xe000
	s_add_i32 s84, s83, 0x2000
	s_cmp_eq_u32 s69, s54
	s_cselect_b32 s54, s44, s80
	s_cselect_b32 s57, s43, s78
	s_cselect_b32 s56, s42, s77
	s_cselect_b32 s59, s47, s41
	s_cselect_b32 s58, s46, s5
	s_cselect_b32 s55, s45, s55
	ds_read_b128 v[172:175], v140
	ds_read_b128 v[176:179], v140 offset:1024
	ds_read_b128 v[180:183], v140 offset:2048
	ds_read_b128 v[184:187], v140 offset:3072
	ds_read_b128 v[188:191], v140 offset:4096
	ds_read_b128 v[192:195], v140 offset:5120
	ds_read_b128 v[196:199], v140 offset:6144
	ds_read_b128 v[200:203], v140 offset:7168
	global_load_lds_dwordx4 v240, s[52:53]
	s_mov_b32 m0, s82
	v_mov_b32_e32 v207, v129
	global_load_lds_dwordx4 v242, s[52:53]
	s_waitcnt lgkmcnt(0)
	s_barrier
; #define G_STAGE(bufoff, gbase, voff) do { _Pragma("unroll") for (int _i = 0; _i < 2; ++_i) \
;         __builtin_amdgcn_global_load_lds((const unsigned*)((const char*)(gbase) + (voff)[_i]), (LAS unsigned*)(lds + (bufoff) + ldsw + _i * 8192), 16, 0, 0); } while (0)
; #define G_LDA(dst, b, h) do { _Pragma("unroll") for (int m = 0; m < 4; ++m) G_LD8(dst[m], lds + G_SA(b, h) + aoff + m * 2048); } while (0)
; #define G_LDB(dst, b, h) do { _Pragma("unroll") for (int n = 0; n < 2; ++n) G_LD8(dst[n], lds + G_SB(b, h) + boff + n * 2048); } while (0)
; #define G_WAIT_V(n) asm volatile("s_waitcnt vmcnt(" #n ")" ::: "memory")
; #define G_WAIT_L(n) asm volatile("s_waitcnt lgkmcnt(" #n ")" ::: "memory")
; #define G_BAR __builtin_amdgcn_s_barrier()
; #define G_SCHED __builtin_amdgcn_sched_barrier(0)
;     __device__ __forceinline__ unsigned row_off(const Unit& u, int r, LAS unsigned char* lds) const { return (unsigned)((const LAS int*)(lds + LDS_STAGE + u.q * 4096))[r] * (unsigned)rowbytes; }
;     ...
;             G_LDB(B0, 0, 0); G_LDB(B1, 0, 1); G_SCHED; G_LDA(At, 0, 0); G_STAGE(G_SA(1, 1), a11, vA1);
;             if constexpr (GATHER) { if (last) { int tz = tid; asm volatile("" : "+v"(tz));
; #pragma unroll
;                 for (int i = 0; i < 2; ++i) { int R, C; stage_rc(tz * 16 + i * 8192, R, C); gc0[i] = S.row_off(nxt, R, lds) + (unsigned)C * 2u; gc1[i] = S.row_off(nxt, 128 + R, lds) + (unsigned)C * 2u; } } }
;             G_WAIT_L(0); G_BAR; G_MMA(0, 0, At, B0); G_MMA(0, 1, At, B1); G_WAIT_V(8); G_BAR; G_SCHED;
;             G_LDA(At, 0, 1); G_STAGE(G_SB(0, 0), b02, voffB); G_STAGE(G_SB(0, 1), b12, voffB); G_STAGE(G_SA(0, 0), a02, vA0);
;             G_WAIT_L(0); G_BAR; G_MMA(1, 0, At, B0); G_MMA(1, 1, At, B1); G_WAIT_V(8); G_BAR; G_SCHED;
	s_setprio 1
	s_waitcnt lgkmcnt(0)
	v_mfma_f32_16x16x32_bf16 v[124:127], v[130:133], v[172:175], v[124:127]
	v_mfma_f32_16x16x32_bf16 v[120:123], v[148:151], v[172:175], v[120:123]
	v_mfma_f32_16x16x32_bf16 v[108:111], v[130:133], v[180:183], v[108:111]
	v_mfma_f32_16x16x32_bf16 v[104:107], v[148:151], v[180:183], v[104:107]
	v_mfma_f32_16x16x32_bf16 v[92:95], v[130:133], v[188:191], v[92:95]
	v_mfma_f32_16x16x32_bf16 v[88:91], v[148:151], v[188:191], v[88:91]
	v_mfma_f32_16x16x32_bf16 v[76:79], v[130:133], v[196:199], v[76:79]
	v_mfma_f32_16x16x32_bf16 v[72:75], v[148:151], v[196:199], v[72:75]
	v_mfma_f32_16x16x32_bf16 v[124:127], v[144:147], v[176:179], v[124:127]
	v_mfma_f32_16x16x32_bf16 v[120:123], v[152:155], v[176:179], v[120:123]
	v_mfma_f32_16x16x32_bf16 v[108:111], v[144:147], v[184:187], v[108:111]
	v_mfma_f32_16x16x32_bf16 v[104:107], v[152:155], v[184:187], v[104:107]
	v_mfma_f32_16x16x32_bf16 v[92:95], v[144:147], v[192:195], v[92:95]
	v_mfma_f32_16x16x32_bf16 v[88:91], v[152:155], v[192:195], v[88:91]
	v_mfma_f32_16x16x32_bf16 v[76:79], v[144:147], v[200:203], v[76:79]
	v_mfma_f32_16x16x32_bf16 v[72:75], v[152:155], v[200:203], v[72:75]
	s_setprio 0
	s_setprio 1
	v_mfma_f32_16x16x32_bf16 v[116:119], v[156:159], v[172:175], v[116:119]
	v_mfma_f32_16x16x32_bf16 v[112:115], v[164:167], v[172:175], v[112:115]
	v_mfma_f32_16x16x32_bf16 v[100:103], v[156:159], v[180:183], v[100:103]
	v_mfma_f32_16x16x32_bf16 v[96:99], v[164:167], v[180:183], v[96:99]
	v_mfma_f32_16x16x32_bf16 v[84:87], v[156:159], v[188:191], v[84:87]
	v_mfma_f32_16x16x32_bf16 v[80:83], v[164:167], v[188:191], v[80:83]
	v_mfma_f32_16x16x32_bf16 v[68:71], v[156:159], v[196:199], v[68:71]
	v_mfma_f32_16x16x32_bf16 v[64:67], v[164:167], v[196:199], v[64:67]
	v_mfma_f32_16x16x32_bf16 v[116:119], v[160:163], v[176:179], v[116:119]
	v_mfma_f32_16x16x32_bf16 v[112:115], v[168:171], v[176:179], v[112:115]
	v_mfma_f32_16x16x32_bf16 v[100:103], v[160:163], v[184:187], v[100:103]
	v_mfma_f32_16x16x32_bf16 v[96:99], v[168:171], v[184:187], v[96:99]
	v_mfma_f32_16x16x32_bf16 v[84:87], v[160:163], v[192:195], v[84:87]
	v_mfma_f32_16x16x32_bf16 v[80:83], v[168:171], v[192:195], v[80:83]
	v_mfma_f32_16x16x32_bf16 v[68:71], v[160:163], v[200:203], v[68:71]
	v_mfma_f32_16x16x32_bf16 v[64:67], v[168:171], v[200:203], v[64:67]
	s_setprio 0
	s_waitcnt vmcnt(8)
	s_barrier
	s_mov_b32 m0, s83
	ds_read_b128 v[172:175], v140 offset:16384
	ds_read_b128 v[176:179], v140 offset:17408
	ds_read_b128 v[180:183], v140 offset:18432
	ds_read_b128 v[184:187], v140 offset:19456
	ds_read_b128 v[188:191], v140 offset:20480
	ds_read_b128 v[192:195], v140 offset:21504
	ds_read_b128 v[196:199], v140 offset:22528
	ds_read_b128 v[200:203], v140 offset:23552
	global_load_lds_dwordx4 v244, s[58:59]
	s_mov_b32 m0, s84
	s_cselect_b32 s81, s49, s61
	s_cselect_b32 s80, s48, s60
	s_add_i32 s82, s72, s20
	global_load_lds_dwordx4 v246, s[58:59]
	s_mov_b32 m0, s82
	v_mov_b32_e32 v205, v129
	global_load_lds_dwordx4 v244, s[80:81]
	s_add_i32 m0, s82, 0x2000
	v_mov_b32_e32 v209, v129
	global_load_lds_dwordx4 v246, s[80:81]
	s_mov_b32 m0, s33
	v_lshl_add_u64 v[210:211], s[58:59], 0, v[244:245]
	global_load_lds_dwordx4 v240, s[56:57]
	s_mov_b32 m0, s62
	v_lshl_add_u64 v[212:213], s[58:59], 0, v[246:247]
	global_load_lds_dwordx4 v242, s[56:57]
	s_waitcnt lgkmcnt(0)
	v_lshl_add_u64 v[204:205], s[80:81], 0, v[244:245]
	v_lshl_add_u64 v[208:209], s[80:81], 0, v[246:247]
	v_lshl_add_u64 v[214:215], s[56:57], 0, v[240:241]
	v_lshl_add_u64 v[216:217], s[56:57], 0, v[242:243]
	s_barrier
	s_setprio 1
	s_waitcnt lgkmcnt(0)
	v_mfma_f32_16x16x32_bf16 v[60:63], v[130:133], v[172:175], v[60:63]
	v_mfma_f32_16x16x32_bf16 v[56:59], v[148:151], v[172:175], v[56:59]
	v_mfma_f32_16x16x32_bf16 v[44:47], v[130:133], v[180:183], v[44:47]
	v_mfma_f32_16x16x32_bf16 v[40:43], v[148:151], v[180:183], v[40:43]
	v_mfma_f32_16x16x32_bf16 v[28:31], v[130:133], v[188:191], v[28:31]
	v_mfma_f32_16x16x32_bf16 v[24:27], v[148:151], v[188:191], v[24:27]
	v_mfma_f32_16x16x32_bf16 v[12:15], v[130:133], v[196:199], v[12:15]
	v_mfma_f32_16x16x32_bf16 v[8:11], v[148:151], v[196:199], v[8:11]
	v_mfma_f32_16x16x32_bf16 v[60:63], v[144:147], v[176:179], v[60:63]
	v_mfma_f32_16x16x32_bf16 v[56:59], v[152:155], v[176:179], v[56:59]
	v_mfma_f32_16x16x32_bf16 v[44:47], v[144:147], v[184:187], v[44:47]
	v_mfma_f32_16x16x32_bf16 v[40:43], v[152:155], v[184:187], v[40:43]
	v_mfma_f32_16x16x32_bf16 v[28:31], v[144:147], v[192:195], v[28:31]
	v_mfma_f32_16x16x32_bf16 v[24:27], v[152:155], v[192:195], v[24:27]
	v_mfma_f32_16x16x32_bf16 v[12:15], v[144:147], v[200:203], v[12:15]
	v_mfma_f32_16x16x32_bf16 v[8:11], v[152:155], v[200:203], v[8:11]
	s_setprio 0
	s_setprio 1
	v_mfma_f32_16x16x32_bf16 v[52:55], v[156:159], v[172:175], v[52:55]
	v_mfma_f32_16x16x32_bf16 v[48:51], v[164:167], v[172:175], v[48:51]
	v_mfma_f32_16x16x32_bf16 v[36:39], v[156:159], v[180:183], v[36:39]
	v_mfma_f32_16x16x32_bf16 v[32:35], v[164:167], v[180:183], v[32:35]
	v_mfma_f32_16x16x32_bf16 v[20:23], v[156:159], v[188:191], v[20:23]
	v_mfma_f32_16x16x32_bf16 v[16:19], v[164:167], v[188:191], v[16:19]
	v_mfma_f32_16x16x32_bf16 v[4:7], v[156:159], v[196:199], v[4:7]
	v_mfma_f32_16x16x32_bf16 v[0:3], v[164:167], v[196:199], v[0:3]
	v_mfma_f32_16x16x32_bf16 v[52:55], v[160:163], v[176:179], v[52:55]
	v_mfma_f32_16x16x32_bf16 v[48:51], v[168:171], v[176:179], v[48:51]
	v_mfma_f32_16x16x32_bf16 v[36:39], v[160:163], v[184:187], v[36:39]
	v_mfma_f32_16x16x32_bf16 v[32:35], v[168:171], v[184:187], v[32:35]
	v_mfma_f32_16x16x32_bf16 v[20:23], v[160:163], v[192:195], v[20:23]
	v_mfma_f32_16x16x32_bf16 v[16:19], v[168:171], v[192:195], v[16:19]
	v_mfma_f32_16x16x32_bf16 v[4:7], v[160:163], v[200:203], v[4:7]
	v_mfma_f32_16x16x32_bf16 v[0:3], v[168:171], v[200:203], v[0:3]
	s_setprio 0
	s_waitcnt vmcnt(8)
	s_barrier
; #define G_STAGE(bufoff, gbase, voff) do { _Pragma("unroll") for (int _i = 0; _i < 2; ++_i) \
;         __builtin_amdgcn_global_load_lds((const unsigned*)((const char*)(gbase) + (voff)[_i]), (LAS unsigned*)(lds + (bufoff) + ldsw + _i * 8192), 16, 0, 0); } while (0)
; #define G_LDA(dst, b, h) do { _Pragma("unroll") for (int m = 0; m < 4; ++m) G_LD8(dst[m], lds + G_SA(b, h) + aoff + m * 2048); } while (0)
; #define G_LDB(dst, b, h) do { _Pragma("unroll") for (int n = 0; n < 2; ++n) G_LD8(dst[n], lds + G_SB(b, h) + boff + n * 2048); } while (0)
; #define G_WAIT_V(n) asm volatile("s_waitcnt vmcnt(" #n ")" ::: "memory")
; #define G_WAIT_L(n) asm volatile("s_waitcnt lgkmcnt(" #n ")" ::: "memory")
; #define G_BAR __builtin_amdgcn_s_barrier()
; #define G_SCHED __builtin_amdgcn_sched_barrier(0)
;     ...
;             G_LDB(B0, 1, 0); G_LDB(B1, 1, 1); G_SCHED; G_LDA(At, 1, 0); G_STAGE(G_SA(0, 1), a12, vA1);
;             G_WAIT_L(0); G_BAR; G_MMA(0, 0, At, B0); G_MMA(0, 1, At, B1); G_WAIT_V(8); G_BAR; G_SCHED;
	s_add_i32 s56, 0, 0x18000
	s_add_i32 s57, 0, 0x1c000
	v_add_u32_e32 v152, s56, v137
	v_add_u32_e32 v168, s57, v137
	ds_read_b128 v[130:133], v152
	ds_read_b128 v[144:147], v152 offset:1024
	ds_read_b128 v[148:151], v152 offset:2048
	ds_read_b128 v[152:155], v152 offset:3072
	ds_read_b128 v[156:159], v168
	ds_read_b128 v[160:163], v168 offset:1024
	ds_read_b128 v[164:167], v168 offset:2048
	ds_read_b128 v[168:171], v168 offset:3072
	s_mov_b32 m0, s63
	ds_read_b128 v[172:175], v140 offset:32768
	ds_read_b128 v[176:179], v140 offset:33792
	ds_read_b128 v[180:183], v140 offset:34816
	ds_read_b128 v[184:187], v140 offset:35840
	ds_read_b128 v[188:191], v140 offset:36864
	ds_read_b128 v[192:195], v140 offset:37888
	ds_read_b128 v[196:199], v140 offset:38912
	ds_read_b128 v[200:203], v140 offset:39936
	global_load_lds_dwordx4 v240, s[54:55]
	s_mov_b32 m0, s64
	s_nop 0
	global_load_lds_dwordx4 v242, s[54:55]
	s_waitcnt lgkmcnt(0)
	s_barrier
	s_setprio 1
	s_waitcnt lgkmcnt(0)
	v_mfma_f32_16x16x32_bf16 v[124:127], v[130:133], v[172:175], v[124:127]
	v_mfma_f32_16x16x32_bf16 v[120:123], v[148:151], v[172:175], v[120:123]
	v_mfma_f32_16x16x32_bf16 v[108:111], v[130:133], v[180:183], v[108:111]
	v_mfma_f32_16x16x32_bf16 v[104:107], v[148:151], v[180:183], v[104:107]
	v_mfma_f32_16x16x32_bf16 v[92:95], v[130:133], v[188:191], v[92:95]
	v_mfma_f32_16x16x32_bf16 v[88:91], v[148:151], v[188:191], v[88:91]
	v_mfma_f32_16x16x32_bf16 v[76:79], v[130:133], v[196:199], v[76:79]
	v_mfma_f32_16x16x32_bf16 v[72:75], v[148:151], v[196:199], v[72:75]
	v_mfma_f32_16x16x32_bf16 v[124:127], v[144:147], v[176:179], v[124:127]
	v_mfma_f32_16x16x32_bf16 v[120:123], v[152:155], v[176:179], v[120:123]
	v_mfma_f32_16x16x32_bf16 v[108:111], v[144:147], v[184:187], v[108:111]
	v_mfma_f32_16x16x32_bf16 v[104:107], v[152:155], v[184:187], v[104:107]
	v_mfma_f32_16x16x32_bf16 v[92:95], v[144:147], v[192:195], v[92:95]
	v_mfma_f32_16x16x32_bf16 v[88:91], v[152:155], v[192:195], v[88:91]
	v_mfma_f32_16x16x32_bf16 v[76:79], v[144:147], v[200:203], v[76:79]
	v_mfma_f32_16x16x32_bf16 v[72:75], v[152:155], v[200:203], v[72:75]
	s_setprio 0
	s_setprio 1
	v_mfma_f32_16x16x32_bf16 v[116:119], v[156:159], v[172:175], v[116:119]
	v_mfma_f32_16x16x32_bf16 v[112:115], v[164:167], v[172:175], v[112:115]
	v_mfma_f32_16x16x32_bf16 v[100:103], v[156:159], v[180:183], v[100:103]
	v_mfma_f32_16x16x32_bf16 v[96:99], v[164:167], v[180:183], v[96:99]
	v_mfma_f32_16x16x32_bf16 v[84:87], v[156:159], v[188:191], v[84:87]
	v_mfma_f32_16x16x32_bf16 v[80:83], v[164:167], v[188:191], v[80:83]
	v_mfma_f32_16x16x32_bf16 v[68:71], v[156:159], v[196:199], v[68:71]
	v_mfma_f32_16x16x32_bf16 v[64:67], v[164:167], v[196:199], v[64:67]
	v_mfma_f32_16x16x32_bf16 v[116:119], v[160:163], v[176:179], v[116:119]
	v_mfma_f32_16x16x32_bf16 v[112:115], v[168:171], v[176:179], v[112:115]
	v_mfma_f32_16x16x32_bf16 v[100:103], v[160:163], v[184:187], v[100:103]
	v_mfma_f32_16x16x32_bf16 v[96:99], v[168:171], v[184:187], v[96:99]
	v_mfma_f32_16x16x32_bf16 v[84:87], v[160:163], v[192:195], v[84:87]
	v_mfma_f32_16x16x32_bf16 v[80:83], v[168:171], v[192:195], v[80:83]
	v_mfma_f32_16x16x32_bf16 v[68:71], v[160:163], v[200:203], v[68:71]
	v_mfma_f32_16x16x32_bf16 v[64:67], v[168:171], v[200:203], v[64:67]
	s_setprio 0
	s_waitcnt vmcnt(8)
	s_barrier
; #define G_STAGE(bufoff, gbase, voff) do { _Pragma("unroll") for (int _i = 0; _i < 2; ++_i) \
;         __builtin_amdgcn_global_load_lds((const unsigned*)((const char*)(gbase) + (voff)[_i]), (LAS unsigned*)(lds + (bufoff) + ldsw + _i * 8192), 16, 0, 0); } while (0)
; #define G_LDA(dst, b, h) do { _Pragma("unroll") for (int m = 0; m < 4; ++m) G_LD8(dst[m], lds + G_SA(b, h) + aoff + m * 2048); } while (0)
; #define G_WAIT_V(n) asm volatile("s_waitcnt vmcnt(" #n ")" ::: "memory")
; #define G_WAIT_L(n) asm volatile("s_waitcnt lgkmcnt(" #n ")" ::: "memory")
; #define G_BAR __builtin_amdgcn_s_barrier()
; #define G_SCHED __builtin_amdgcn_sched_barrier(0)
;     ...
;             G_LDA(At, 1, 1); G_STAGE(G_SB(1, 0), b02 + kstep, voffB); G_STAGE(G_SB(1, 1), b12 + kstep, voffB); G_STAGE(G_SA(1, 0), a02 + kstep, vA0);
;             G_WAIT_L(0); G_BAR; G_MMA(1, 0, At, B0); G_MMA(1, 1, At, B1); G_WAIT_V(8); G_BAR; G_SCHED;
;         }
	s_add_i32 s54, s56, s20
	v_lshl_add_u64 v[206:207], v[210:211], 0, s[34:35]
	s_mov_b32 m0, s54
	ds_read_b128 v[172:175], v140 offset:49152
	ds_read_b128 v[176:179], v140 offset:50176
	ds_read_b128 v[180:183], v140 offset:51200
	ds_read_b128 v[184:187], v140 offset:52224
	ds_read_b128 v[188:191], v140 offset:53248
	ds_read_b128 v[192:195], v140 offset:54272
	ds_read_b128 v[196:199], v140 offset:55296
	ds_read_b128 v[200:203], v140 offset:56320
	global_load_lds_dwordx4 v[206:207], off
	v_lshl_add_u64 v[206:207], v[212:213], 0, s[34:35]
	s_add_i32 m0, s54, 0x2000
	s_add_i32 s54, s57, s20
	global_load_lds_dwordx4 v[206:207], off
	v_lshl_add_u64 v[204:205], v[204:205], 0, s[34:35]
	s_mov_b32 m0, s54
	s_nop 0
	global_load_lds_dwordx4 v[204:205], off
	v_lshl_add_u64 v[204:205], v[208:209], 0, s[34:35]
	s_add_i32 m0, s54, 0x2000
	s_nop 0
	global_load_lds_dwordx4 v[204:205], off
	v_lshl_add_u64 v[204:205], v[214:215], 0, s[34:35]
	s_mov_b32 m0, s66
	s_nop 0
	global_load_lds_dwordx4 v[204:205], off
	v_lshl_add_u64 v[204:205], v[216:217], 0, s[34:35]
	s_mov_b32 m0, s67
	s_nop 0
	global_load_lds_dwordx4 v[204:205], off
	s_waitcnt lgkmcnt(0)
	s_barrier
	s_setprio 1
	s_waitcnt lgkmcnt(0)
	v_mfma_f32_16x16x32_bf16 v[60:63], v[130:133], v[172:175], v[60:63]
	v_mfma_f32_16x16x32_bf16 v[56:59], v[148:151], v[172:175], v[56:59]
	v_mfma_f32_16x16x32_bf16 v[44:47], v[130:133], v[180:183], v[44:47]
	v_mfma_f32_16x16x32_bf16 v[40:43], v[148:151], v[180:183], v[40:43]
	v_mfma_f32_16x16x32_bf16 v[28:31], v[130:133], v[188:191], v[28:31]
	v_mfma_f32_16x16x32_bf16 v[24:27], v[148:151], v[188:191], v[24:27]
	v_mfma_f32_16x16x32_bf16 v[12:15], v[130:133], v[196:199], v[12:15]
	v_mfma_f32_16x16x32_bf16 v[8:11], v[148:151], v[196:199], v[8:11]
	v_mfma_f32_16x16x32_bf16 v[60:63], v[144:147], v[176:179], v[60:63]
	v_mfma_f32_16x16x32_bf16 v[56:59], v[152:155], v[176:179], v[56:59]
	v_mfma_f32_16x16x32_bf16 v[44:47], v[144:147], v[184:187], v[44:47]
	v_mfma_f32_16x16x32_bf16 v[40:43], v[152:155], v[184:187], v[40:43]
	v_mfma_f32_16x16x32_bf16 v[28:31], v[144:147], v[192:195], v[28:31]
	v_mfma_f32_16x16x32_bf16 v[24:27], v[152:155], v[192:195], v[24:27]
	v_mfma_f32_16x16x32_bf16 v[12:15], v[144:147], v[200:203], v[12:15]
	v_mfma_f32_16x16x32_bf16 v[8:11], v[152:155], v[200:203], v[8:11]
	s_setprio 0
	s_setprio 1
	v_mfma_f32_16x16x32_bf16 v[52:55], v[156:159], v[172:175], v[52:55]
	v_mfma_f32_16x16x32_bf16 v[48:51], v[164:167], v[172:175], v[48:51]
	v_mfma_f32_16x16x32_bf16 v[36:39], v[156:159], v[180:183], v[36:39]
	v_mfma_f32_16x16x32_bf16 v[32:35], v[164:167], v[180:183], v[32:35]
	v_mfma_f32_16x16x32_bf16 v[20:23], v[156:159], v[188:191], v[20:23]
	v_mfma_f32_16x16x32_bf16 v[16:19], v[164:167], v[188:191], v[16:19]
	v_mfma_f32_16x16x32_bf16 v[4:7], v[156:159], v[196:199], v[4:7]
	v_mfma_f32_16x16x32_bf16 v[0:3], v[164:167], v[196:199], v[0:3]
	v_mfma_f32_16x16x32_bf16 v[52:55], v[160:163], v[176:179], v[52:55]
	v_mfma_f32_16x16x32_bf16 v[48:51], v[168:171], v[176:179], v[48:51]
	v_mfma_f32_16x16x32_bf16 v[36:39], v[160:163], v[184:187], v[36:39]
	v_mfma_f32_16x16x32_bf16 v[32:35], v[168:171], v[184:187], v[32:35]
	v_mfma_f32_16x16x32_bf16 v[20:23], v[160:163], v[192:195], v[20:23]
	v_mfma_f32_16x16x32_bf16 v[16:19], v[168:171], v[192:195], v[16:19]
	v_mfma_f32_16x16x32_bf16 v[4:7], v[160:163], v[200:203], v[4:7]
	v_mfma_f32_16x16x32_bf16 v[0:3], v[168:171], v[200:203], v[0:3]
	s_setprio 0
	s_waitcnt vmcnt(8)
	s_barrier
	s_add_u32 s5, s5, 0x100
	s_addc_u32 s41, s41, 0
	s_add_u32 s60, s60, 0x100
	s_addc_u32 s61, s61, 0
	s_add_u32 s77, s77, 0x100
	s_addc_u32 s78, s78, 0
	s_add_u32 s52, s52, 0x100
	s_addc_u32 s53, s53, 0
	s_cmp_ge_i32 s79, s24
	s_mov_b32 s54, s79
	s_cbranch_scc0 .LBB0_1058
	v_readlane_b32 s78, v255, 11
	v_readlane_b32 s79, v255, 13
	s_and_b64 vcc, exec, s[38:39]
	s_cbranch_vccz .LBB0_1061

; __device__ __forceinline__ int lane_id() { int l; asm volatile("v_mbcnt_lo_u32_b32 %0, -1, 0\n\tv_mbcnt_hi_u32_b32 %0, -1, %0" : "=v"(l)); return l; }
;     ...
;         for (int t = 0; t < nt; t += 2) {
;             const bool last = (t == nt - 2);
;             { const int tz_ = wid * 64 + lane_id();
; #pragma unroll
;               for (int i = 0; i < 2; ++i) { int R, C; stage_rc(tz_ * 16 + i * 8192, R, C); const int Rb = Epi::PERM ? ((R & ~31) + perm32(R & 31)) : R;
;                   voffA[i] = (unsigned)(R * S.multA * S.pitchA + C) * 2u; voffB[i] = (unsigned)(Rb * S.multB * S.pitchB + C) * 2u; } }
;     ...
; #pragma unroll
;         for (int a = 0; a < 2; ++a)
; #pragma unroll
;             for (int b = 0; b < 2; ++b)
; #pragma unroll
;                 for (int m = 0; m < 4; ++m)
; #pragma unroll
;                     for (int n = 0; n < 2; ++n) acc[a][b][m][n] = (acc_t){0, 0, 0, 0};
;         cur = nxt; ++ui;
.LBB0_1320:
	s_andn2_b64 vcc, exec, s[6:7]
	s_cbranch_vccnz .LBB0_1328
	s_add_u32 s9, s70, 0x100
	s_addc_u32 s93, s71, 0
	s_add_u32 s94, s68, 0x100
	s_addc_u32 s95, s69, 0
	s_add_u32 s96, s66, 0x100
	s_waitcnt lgkmcnt(0)
	s_addc_u32 s97, s67, 0
	s_add_u32 s64, s64, 0x80
	v_mov_b32_e32 v0, 0
	s_addc_u32 s65, s65, 0
	s_mov_b32 s66, 0
	v_mov_b32_e32 v1, v0
	v_mov_b32_e32 v2, v0
	v_mov_b32_e32 v3, v0
	v_mov_b32_e32 v4, v0
	v_mov_b32_e32 v5, v0
	v_mov_b32_e32 v6, v0
	v_mov_b32_e32 v7, v0
	v_mov_b32_e32 v8, v0
	v_mov_b32_e32 v9, v0
	v_mov_b32_e32 v10, v0
	v_mov_b32_e32 v11, v0
	v_mov_b32_e32 v12, v0
	v_mov_b32_e32 v13, v0
	v_mov_b32_e32 v14, v0
	v_mov_b32_e32 v15, v0
	v_mov_b32_e32 v16, v0
	v_mov_b32_e32 v17, v0
	v_mov_b32_e32 v18, v0
	v_mov_b32_e32 v19, v0
	v_mov_b32_e32 v20, v0
	v_mov_b32_e32 v21, v0
	v_mov_b32_e32 v22, v0
	v_mov_b32_e32 v23, v0
	v_mov_b32_e32 v24, v0
	v_mov_b32_e32 v25, v0
	v_mov_b32_e32 v26, v0
	v_mov_b32_e32 v27, v0
	v_mov_b32_e32 v28, v0
	v_mov_b32_e32 v29, v0
	v_mov_b32_e32 v30, v0
	v_mov_b32_e32 v31, v0
	v_mov_b32_e32 v56, v0
	v_mov_b32_e32 v57, v0
	v_mov_b32_e32 v58, v0
	v_mov_b32_e32 v59, v0
	v_mov_b32_e32 v64, v0
	v_mov_b32_e32 v65, v0
	v_mov_b32_e32 v66, v0
	v_mov_b32_e32 v67, v0
	v_mov_b32_e32 v72, v0
	v_mov_b32_e32 v73, v0
	v_mov_b32_e32 v74, v0
	v_mov_b32_e32 v75, v0
	v_mov_b32_e32 v76, v0
	v_mov_b32_e32 v77, v0
	v_mov_b32_e32 v78, v0
	v_mov_b32_e32 v79, v0
	v_mov_b32_e32 v80, v0
	v_mov_b32_e32 v81, v0
	v_mov_b32_e32 v82, v0
	v_mov_b32_e32 v83, v0
	v_mov_b32_e32 v84, v0
	v_mov_b32_e32 v85, v0
	v_mov_b32_e32 v86, v0
	v_mov_b32_e32 v87, v0
	v_mov_b32_e32 v88, v0
	v_mov_b32_e32 v89, v0
	v_mov_b32_e32 v90, v0
	v_mov_b32_e32 v91, v0
	v_mov_b32_e32 v92, v0
	v_mov_b32_e32 v93, v0
	v_mov_b32_e32 v94, v0
	v_mov_b32_e32 v95, v0
	v_mov_b32_e32 v32, v0
	v_mov_b32_e32 v33, v0
	v_mov_b32_e32 v34, v0
	v_mov_b32_e32 v35, v0
	v_mov_b32_e32 v36, v0
	v_mov_b32_e32 v37, v0
	v_mov_b32_e32 v38, v0
	v_mov_b32_e32 v39, v0
	v_mov_b32_e32 v40, v0
	v_mov_b32_e32 v41, v0
	v_mov_b32_e32 v42, v0
	v_mov_b32_e32 v43, v0
	v_mov_b32_e32 v44, v0
	v_mov_b32_e32 v45, v0
	v_mov_b32_e32 v46, v0
	v_mov_b32_e32 v47, v0
	v_mov_b32_e32 v48, v0
	v_mov_b32_e32 v49, v0
	v_mov_b32_e32 v50, v0
	v_mov_b32_e32 v51, v0
	v_mov_b32_e32 v52, v0
	v_mov_b32_e32 v53, v0
	v_mov_b32_e32 v54, v0
	v_mov_b32_e32 v55, v0
	v_mov_b32_e32 v60, v0
	v_mov_b32_e32 v61, v0
	v_mov_b32_e32 v62, v0
	v_mov_b32_e32 v63, v0
	v_mov_b32_e32 v68, v0
	v_mov_b32_e32 v69, v0
	v_mov_b32_e32 v70, v0
	v_mov_b32_e32 v71, v0
	v_mov_b32_e32 v96, v0
	v_mov_b32_e32 v97, v0
	v_mov_b32_e32 v98, v0
	v_mov_b32_e32 v99, v0
	v_mov_b32_e32 v100, v0
	v_mov_b32_e32 v101, v0
	v_mov_b32_e32 v102, v0
	v_mov_b32_e32 v103, v0
	v_mov_b32_e32 v104, v0
	v_mov_b32_e32 v105, v0
	v_mov_b32_e32 v106, v0
	v_mov_b32_e32 v107, v0
	v_mov_b32_e32 v108, v0
	v_mov_b32_e32 v109, v0
	v_mov_b32_e32 v110, v0
	v_mov_b32_e32 v111, v0
	v_mov_b32_e32 v112, v0
	v_mov_b32_e32 v113, v0
	v_mov_b32_e32 v114, v0
	v_mov_b32_e32 v115, v0
	v_mov_b32_e32 v116, v0
	v_mov_b32_e32 v117, v0
	v_mov_b32_e32 v118, v0
	v_mov_b32_e32 v119, v0
	v_mov_b32_e32 v120, v0
	v_mov_b32_e32 v121, v0
	v_mov_b32_e32 v122, v0
	v_mov_b32_e32 v123, v0
	v_mov_b32_e32 v124, v0
	v_mov_b32_e32 v125, v0
	v_mov_b32_e32 v126, v0
	v_mov_b32_e32 v127, v0
	v_mbcnt_lo_u32_b32 v248, -1, 0
	v_mbcnt_hi_u32_b32 v248, -1, v248
	v_mov_b32_e32 v249, s88
	v_lshrrev_b32_e32 v249, 6, v249
	v_and_b32_e32 v250, 3, v248
	v_lshlrev_b32_e32 v250, 4, v250
	v_and_b32_e32 v251, 32, v248
	v_xor_b32_e32 v250, v250, v251
	v_and_b32_e32 v251, 1, v249
	v_lshl_add_u32 v250, v251, 6, v250
	v_lshrrev_b32_e32 v251, 1, v249
	v_lshrrev_b32_e32 v252, 2, v248
	v_lshl_add_u32 v251, v251, 4, v252
	v_mov_b32_e32 v253, 0x1000
	v_mad_u32_u24 v240, v251, v253, v250
	v_add_u32_e32 v242, 0x40000, v240
	v_lshrrev_b32_e32 v251, 2, v249
	v_lshlrev_b32_e32 v251, 5, v251
	v_lshrrev_b32_e32 v252, 4, v248
	v_lshl_add_u32 v251, v252, 3, v251
	v_bfe_u32 v252, v249, 1, 1
	v_lshl_add_u32 v251, v252, 2, v251
	v_bfe_u32 v252, v248, 2, 2
	v_add_u32_e32 v251, v251, v252
	v_mov_b32_e32 v253, 0x1000
	v_mad_u32_u24 v244, v251, v253, v250
	v_add_u32_e32 v246, 0x40000, v244
	v_mov_b32_e32 v241, 0
	v_mov_b32_e32 v243, 0
	v_mov_b32_e32 v245, 0
	v_mov_b32_e32 v247, 0
; __device__ __forceinline__ int lane_id() { int l; asm volatile("v_mbcnt_lo_u32_b32 %0, -1, 0\n\tv_mbcnt_hi_u32_b32 %0, -1, %0" : "=v"(l)); return l; }
; #define G_STAGE(bufoff, gbase, voff) do { _Pragma("unroll") for (int _i = 0; _i < 2; ++_i) \
;         __builtin_amdgcn_global_load_lds((const unsigned*)((const char*)(gbase) + (voff)[_i]), (LAS unsigned*)(lds + (bufoff) + ldsw + _i * 8192), 16, 0, 0); } while (0)
; #define G_LDA(dst, b, h) do { _Pragma("unroll") for (int m = 0; m < 4; ++m) G_LD8(dst[m], lds + G_SA(b, h) + aoff + m * 2048); } while (0)
; #define G_BAR __builtin_amdgcn_s_barrier()
;     ...
;         for (int t = 0; t < nt; t += 2) {
;             const bool last = (t == nt - 2);
;             { const int tz_ = wid * 64 + lane_id();
; #pragma unroll
;               for (int i = 0; i < 2; ++i) { int R, C; stage_rc(tz_ * 16 + i * 8192, R, C); const int Rb = Epi::PERM ? ((R & ~31) + perm32(R & 31)) : R;
;                   voffA[i] = (unsigned)(R * S.multA * S.pitchA + C) * 2u; voffB[i] = (unsigned)(Rb * S.multB * S.pitchB + C) * 2u; } }
;             if constexpr (GATHER) asm volatile("" : "+v"(gc0[0]), "+v"(gc0[1]), "+v"(gc1[0]), "+v"(gc1[1]));
;             if constexpr (PREF) { if (t == nt - 4) S.prefetch(nxt, lds); }
;             const char* a11 = cur.a1 + (size_t)(t + 1) * kstep;
;             const char* a02 = last ? nxt.a0 : cur.a0 + (size_t)(t + 2) * kstep; const char* a12 = last ? nxt.a1 : cur.a1 + (size_t)(t + 2) * kstep;
;             const char* b02 = last ? nxt.b0 : cur.b0 + (size_t)(t + 2) * kstep; const char* b12 = last ? nxt.b1 : cur.b1 + (size_t)(t + 2) * kstep;
;             G_LDB(B0, 0, 0); G_LDB(B1, 0, 1); G_SCHED; G_LDA(At, 0, 0); G_STAGE(G_SA(1, 1), a11, vA1);
;             if constexpr (GATHER) { if (last) { int tz = tid; asm volatile("" : "+v"(tz));
; #pragma unroll
;                 for (int i = 0; i < 2; ++i) { int R, C; stage_rc(tz * 16 + i * 8192, R, C); gc0[i] = S.row_off(nxt, R, lds) + (unsigned)C * 2u; gc1[i] = S.row_off(nxt, 128 + R, lds) + (unsigned)C * 2u; } } }
;             G_WAIT_L(0); G_BAR; G_MMA(0, 0, At, B0); G_MMA(0, 1, At, B1); G_WAIT_V(8); G_BAR; G_SCHED;
;             G_LDA(At, 0, 1); G_STAGE(G_SB(0, 0), b02, voffB); G_STAGE(G_SB(0, 1), b12, voffB); G_STAGE(G_SA(0, 0), a02, vA0);
;             G_WAIT_L(0); G_BAR; G_MMA(1, 0, At, B0); G_MMA(1, 1, At, B1); G_WAIT_V(8); G_BAR; G_SCHED;
.LBB0_1322:
	s_add_i32 vcc_lo, s66, 2
	s_add_u32 vcc_hi, s64, 0x80
	s_addc_u32 s67, s65, 0
	s_add_i32 s68, 0, 0x10000
	s_add_i32 s1, 0, 0x14000
	v_add_u32_e32 v146, s68, v172
	v_add_u32_e32 v162, s1, v172
	ds_read_b128 v[130:133], v146
	ds_read_b128 v[134:137], v146 offset:1024
	ds_read_b128 v[138:141], v146 offset:2048
	ds_read_b128 v[146:149], v146 offset:3072
	ds_read_b128 v[150:153], v162
	ds_read_b128 v[154:157], v162 offset:1024
	ds_read_b128 v[158:161], v162 offset:2048
	ds_read_b128 v[162:165], v162 offset:3072
	s_add_i32 s11, s68, s77
	s_add_i32 m0, s10, 0xc000
	s_add_i32 s33, s10, 0xe000
	s_add_i32 s21, s11, 0x2000
	s_cmp_eq_u32 s89, s66
	s_cselect_b32 s66, s54, vcc_hi
	s_cselect_b32 s69, s53, s97
	s_cselect_b32 s68, s52, s96
	s_cselect_b32 s71, s57, s93
	s_cselect_b32 s70, s56, s9
	s_cselect_b32 s67, s55, s67
	ds_read_b128 v[174:177], v173
	ds_read_b128 v[178:181], v173 offset:1024
	ds_read_b128 v[182:185], v173 offset:2048
	ds_read_b128 v[186:189], v173 offset:3072
	ds_read_b128 v[190:193], v173 offset:4096
	ds_read_b128 v[194:197], v173 offset:5120
	ds_read_b128 v[198:201], v173 offset:6144
	ds_read_b128 v[202:205], v173 offset:7168
	global_load_lds_dwordx4 v240, s[64:65]
	s_mov_b32 m0, s33
	s_nop 0
	global_load_lds_dwordx4 v242, s[64:65]
	s_waitcnt lgkmcnt(0)
	v_mov_b32_e32 v129, v145
	s_barrier
	s_setprio 1
	s_waitcnt lgkmcnt(0)
	v_mfma_f32_16x16x32_bf16 v[124:127], v[130:133], v[174:177], v[124:127]
	v_mfma_f32_16x16x32_bf16 v[120:123], v[138:141], v[174:177], v[120:123]
	v_mfma_f32_16x16x32_bf16 v[116:119], v[130:133], v[182:185], v[116:119]
	v_mfma_f32_16x16x32_bf16 v[112:115], v[138:141], v[182:185], v[112:115]
	v_mfma_f32_16x16x32_bf16 v[108:111], v[130:133], v[190:193], v[108:111]
	v_mfma_f32_16x16x32_bf16 v[104:107], v[138:141], v[190:193], v[104:107]
	v_mfma_f32_16x16x32_bf16 v[100:103], v[130:133], v[198:201], v[100:103]
	v_mfma_f32_16x16x32_bf16 v[96:99], v[138:141], v[198:201], v[96:99]
	v_mfma_f32_16x16x32_bf16 v[124:127], v[134:137], v[178:181], v[124:127]
	v_mfma_f32_16x16x32_bf16 v[120:123], v[146:149], v[178:181], v[120:123]
	v_mfma_f32_16x16x32_bf16 v[116:119], v[134:137], v[186:189], v[116:119]
	v_mfma_f32_16x16x32_bf16 v[112:115], v[146:149], v[186:189], v[112:115]
	v_mfma_f32_16x16x32_bf16 v[108:111], v[134:137], v[194:197], v[108:111]
	v_mfma_f32_16x16x32_bf16 v[104:107], v[146:149], v[194:197], v[104:107]
	v_mfma_f32_16x16x32_bf16 v[100:103], v[134:137], v[202:205], v[100:103]
	v_mfma_f32_16x16x32_bf16 v[96:99], v[146:149], v[202:205], v[96:99]
	s_setprio 0
	s_setprio 1
	v_mfma_f32_16x16x32_bf16 v[68:71], v[150:153], v[174:177], v[68:71]
	v_mfma_f32_16x16x32_bf16 v[60:63], v[158:161], v[174:177], v[60:63]
	v_mfma_f32_16x16x32_bf16 v[52:55], v[150:153], v[182:185], v[52:55]
	v_mfma_f32_16x16x32_bf16 v[48:51], v[158:161], v[182:185], v[48:51]
	v_mfma_f32_16x16x32_bf16 v[44:47], v[150:153], v[190:193], v[44:47]
	v_mfma_f32_16x16x32_bf16 v[40:43], v[158:161], v[190:193], v[40:43]
	v_mfma_f32_16x16x32_bf16 v[36:39], v[150:153], v[198:201], v[36:39]
	v_mfma_f32_16x16x32_bf16 v[32:35], v[158:161], v[198:201], v[32:35]
	v_mfma_f32_16x16x32_bf16 v[68:71], v[154:157], v[178:181], v[68:71]
	v_mfma_f32_16x16x32_bf16 v[60:63], v[162:165], v[178:181], v[60:63]
	v_mfma_f32_16x16x32_bf16 v[52:55], v[154:157], v[186:189], v[52:55]
	v_mfma_f32_16x16x32_bf16 v[48:51], v[162:165], v[186:189], v[48:51]
	v_mfma_f32_16x16x32_bf16 v[44:47], v[154:157], v[194:197], v[44:47]
	v_mfma_f32_16x16x32_bf16 v[40:43], v[162:165], v[194:197], v[40:43]
	v_mfma_f32_16x16x32_bf16 v[36:39], v[154:157], v[202:205], v[36:39]
	v_mfma_f32_16x16x32_bf16 v[32:35], v[162:165], v[202:205], v[32:35]
	s_setprio 0
	s_waitcnt vmcnt(8)
	s_barrier
	s_mov_b32 m0, s11
	ds_read_b128 v[174:177], v173 offset:16384
	ds_read_b128 v[178:181], v173 offset:17408
	ds_read_b128 v[182:185], v173 offset:18432
	ds_read_b128 v[186:189], v173 offset:19456
	ds_read_b128 v[190:193], v173 offset:20480
	ds_read_b128 v[194:197], v173 offset:21504
	ds_read_b128 v[198:201], v173 offset:22528
	ds_read_b128 v[202:205], v173 offset:23552
	v_mov_b32_e32 v143, v145
	global_load_lds_dwordx4 v244, s[70:71]
	v_mov_b32_e32 v207, v145
	s_mov_b32 m0, s21
	v_lshl_add_u64 v[208:209], s[70:71], 0, v[244:245]
	v_lshl_add_u64 v[210:211], s[70:71], 0, v[246:247]
	global_load_lds_dwordx4 v246, s[70:71]
	s_cselect_b32 s71, s59, s95
	s_cselect_b32 s70, s58, s94
	s_add_i32 s1, s1, s77
	s_mov_b32 m0, s1
	v_lshl_add_u64 v[212:213], s[70:71], 0, v[244:245]
	global_load_lds_dwordx4 v244, s[70:71]
	s_add_i32 m0, s1, 0x2000
	v_lshl_add_u64 v[142:143], s[70:71], 0, v[246:247]
	global_load_lds_dwordx4 v246, s[70:71]
	s_mov_b32 m0, s10
	v_lshl_add_u64 v[206:207], s[68:69], 0, v[240:241]
	global_load_lds_dwordx4 v240, s[68:69]
	s_mov_b32 m0, s63
	v_lshl_add_u64 v[214:215], s[68:69], 0, v[242:243]
	global_load_lds_dwordx4 v242, s[68:69]
	s_waitcnt lgkmcnt(0)
	s_barrier
; #define G_STAGE(bufoff, gbase, voff) do { _Pragma("unroll") for (int _i = 0; _i < 2; ++_i) \
;         __builtin_amdgcn_global_load_lds((const unsigned*)((const char*)(gbase) + (voff)[_i]), (LAS unsigned*)(lds + (bufoff) + ldsw + _i * 8192), 16, 0, 0); } while (0)
; #define G_LDA(dst, b, h) do { _Pragma("unroll") for (int m = 0; m < 4; ++m) G_LD8(dst[m], lds + G_SA(b, h) + aoff + m * 2048); } while (0)
; #define G_LDB(dst, b, h) do { _Pragma("unroll") for (int n = 0; n < 2; ++n) G_LD8(dst[n], lds + G_SB(b, h) + boff + n * 2048); } while (0)
; #define G_WAIT_V(n) asm volatile("s_waitcnt vmcnt(" #n ")" ::: "memory")
; #define G_WAIT_L(n) asm volatile("s_waitcnt lgkmcnt(" #n ")" ::: "memory")
; #define G_BAR __builtin_amdgcn_s_barrier()
; #define G_SCHED __builtin_amdgcn_sched_barrier(0)
;     ...
;             G_WAIT_L(0); G_BAR; G_MMA(1, 0, At, B0); G_MMA(1, 1, At, B1); G_WAIT_V(8); G_BAR; G_SCHED;
;             G_LDB(B0, 1, 0); G_LDB(B1, 1, 1); G_SCHED; G_LDA(At, 1, 0); G_STAGE(G_SA(0, 1), a12, vA1);
;             G_WAIT_L(0); G_BAR; G_MMA(0, 0, At, B0); G_MMA(0, 1, At, B1); G_WAIT_V(8); G_BAR; G_SCHED;
	s_setprio 1
	s_waitcnt lgkmcnt(0)
	v_mfma_f32_16x16x32_bf16 v[92:95], v[130:133], v[174:177], v[92:95]
	v_mfma_f32_16x16x32_bf16 v[88:91], v[138:141], v[174:177], v[88:91]
	v_mfma_f32_16x16x32_bf16 v[84:87], v[130:133], v[182:185], v[84:87]
	v_mfma_f32_16x16x32_bf16 v[80:83], v[138:141], v[182:185], v[80:83]
	v_mfma_f32_16x16x32_bf16 v[76:79], v[130:133], v[190:193], v[76:79]
	v_mfma_f32_16x16x32_bf16 v[72:75], v[138:141], v[190:193], v[72:75]
	v_mfma_f32_16x16x32_bf16 v[64:67], v[130:133], v[198:201], v[64:67]
	v_mfma_f32_16x16x32_bf16 v[56:59], v[138:141], v[198:201], v[56:59]
	v_mfma_f32_16x16x32_bf16 v[92:95], v[134:137], v[178:181], v[92:95]
	v_mfma_f32_16x16x32_bf16 v[88:91], v[146:149], v[178:181], v[88:91]
	v_mfma_f32_16x16x32_bf16 v[84:87], v[134:137], v[186:189], v[84:87]
	v_mfma_f32_16x16x32_bf16 v[80:83], v[146:149], v[186:189], v[80:83]
	v_mfma_f32_16x16x32_bf16 v[76:79], v[134:137], v[194:197], v[76:79]
	v_mfma_f32_16x16x32_bf16 v[72:75], v[146:149], v[194:197], v[72:75]
	v_mfma_f32_16x16x32_bf16 v[64:67], v[134:137], v[202:205], v[64:67]
	v_mfma_f32_16x16x32_bf16 v[56:59], v[146:149], v[202:205], v[56:59]
	s_setprio 0
	s_setprio 1
	v_mfma_f32_16x16x32_bf16 v[28:31], v[150:153], v[174:177], v[28:31]
	v_mfma_f32_16x16x32_bf16 v[24:27], v[158:161], v[174:177], v[24:27]
	v_mfma_f32_16x16x32_bf16 v[20:23], v[150:153], v[182:185], v[20:23]
	v_mfma_f32_16x16x32_bf16 v[16:19], v[158:161], v[182:185], v[16:19]
	v_mfma_f32_16x16x32_bf16 v[12:15], v[150:153], v[190:193], v[12:15]
	v_mfma_f32_16x16x32_bf16 v[8:11], v[158:161], v[190:193], v[8:11]
	v_mfma_f32_16x16x32_bf16 v[4:7], v[150:153], v[198:201], v[4:7]
	v_mfma_f32_16x16x32_bf16 v[0:3], v[158:161], v[198:201], v[0:3]
	v_mfma_f32_16x16x32_bf16 v[28:31], v[154:157], v[178:181], v[28:31]
	v_mfma_f32_16x16x32_bf16 v[24:27], v[162:165], v[178:181], v[24:27]
	v_mfma_f32_16x16x32_bf16 v[20:23], v[154:157], v[186:189], v[20:23]
	v_mfma_f32_16x16x32_bf16 v[16:19], v[162:165], v[186:189], v[16:19]
	v_mfma_f32_16x16x32_bf16 v[12:15], v[154:157], v[194:197], v[12:15]
	v_mfma_f32_16x16x32_bf16 v[8:11], v[162:165], v[194:197], v[8:11]
	v_mfma_f32_16x16x32_bf16 v[4:7], v[154:157], v[202:205], v[4:7]
	v_mfma_f32_16x16x32_bf16 v[0:3], v[162:165], v[202:205], v[0:3]
	s_setprio 0
	s_waitcnt vmcnt(8)
	s_barrier
	s_add_i32 s1, 0, 0x18000
	v_add_u32_e32 v129, s1, v172
	s_add_i32 s11, 0, 0x1c000
	ds_read_b128 v[130:133], v129
	ds_read_b128 v[134:137], v129 offset:1024
	ds_read_b128 v[138:141], v129 offset:2048
	ds_read_b128 v[146:149], v129 offset:3072
	v_add_u32_e32 v129, s11, v172
	ds_read_b128 v[150:153], v129
	ds_read_b128 v[154:157], v129 offset:1024
	ds_read_b128 v[158:161], v129 offset:2048
	ds_read_b128 v[162:165], v129 offset:3072
	s_mov_b32 m0, s72
	ds_read_b128 v[174:177], v173 offset:32768
	ds_read_b128 v[178:181], v173 offset:33792
	ds_read_b128 v[182:185], v173 offset:34816
	ds_read_b128 v[186:189], v173 offset:35840
	ds_read_b128 v[190:193], v173 offset:36864
	ds_read_b128 v[194:197], v173 offset:37888
	ds_read_b128 v[198:201], v173 offset:38912
	ds_read_b128 v[202:205], v173 offset:39936
	global_load_lds_dwordx4 v240, s[66:67]
	s_mov_b32 m0, s73
	s_nop 0
	global_load_lds_dwordx4 v242, s[66:67]
	s_waitcnt lgkmcnt(0)
	s_barrier
	s_setprio 1
	s_waitcnt lgkmcnt(0)
	v_mfma_f32_16x16x32_bf16 v[124:127], v[130:133], v[174:177], v[124:127]
	v_mfma_f32_16x16x32_bf16 v[120:123], v[138:141], v[174:177], v[120:123]
	v_mfma_f32_16x16x32_bf16 v[116:119], v[130:133], v[182:185], v[116:119]
	v_mfma_f32_16x16x32_bf16 v[112:115], v[138:141], v[182:185], v[112:115]
	v_mfma_f32_16x16x32_bf16 v[108:111], v[130:133], v[190:193], v[108:111]
	v_mfma_f32_16x16x32_bf16 v[104:107], v[138:141], v[190:193], v[104:107]
	v_mfma_f32_16x16x32_bf16 v[100:103], v[130:133], v[198:201], v[100:103]
	v_mfma_f32_16x16x32_bf16 v[96:99], v[138:141], v[198:201], v[96:99]
	v_mfma_f32_16x16x32_bf16 v[124:127], v[134:137], v[178:181], v[124:127]
	v_mfma_f32_16x16x32_bf16 v[120:123], v[146:149], v[178:181], v[120:123]
	v_mfma_f32_16x16x32_bf16 v[116:119], v[134:137], v[186:189], v[116:119]
	v_mfma_f32_16x16x32_bf16 v[112:115], v[146:149], v[186:189], v[112:115]
	v_mfma_f32_16x16x32_bf16 v[108:111], v[134:137], v[194:197], v[108:111]
	v_mfma_f32_16x16x32_bf16 v[104:107], v[146:149], v[194:197], v[104:107]
	v_mfma_f32_16x16x32_bf16 v[100:103], v[134:137], v[202:205], v[100:103]
	v_mfma_f32_16x16x32_bf16 v[96:99], v[146:149], v[202:205], v[96:99]
	s_setprio 0
	s_setprio 1
	v_mfma_f32_16x16x32_bf16 v[68:71], v[150:153], v[174:177], v[68:71]
	v_mfma_f32_16x16x32_bf16 v[60:63], v[158:161], v[174:177], v[60:63]
	v_mfma_f32_16x16x32_bf16 v[52:55], v[150:153], v[182:185], v[52:55]
	v_mfma_f32_16x16x32_bf16 v[48:51], v[158:161], v[182:185], v[48:51]
	v_mfma_f32_16x16x32_bf16 v[44:47], v[150:153], v[190:193], v[44:47]
	v_mfma_f32_16x16x32_bf16 v[40:43], v[158:161], v[190:193], v[40:43]
	v_mfma_f32_16x16x32_bf16 v[36:39], v[150:153], v[198:201], v[36:39]
	v_mfma_f32_16x16x32_bf16 v[32:35], v[158:161], v[198:201], v[32:35]
	v_mfma_f32_16x16x32_bf16 v[68:71], v[154:157], v[178:181], v[68:71]
	v_mfma_f32_16x16x32_bf16 v[60:63], v[162:165], v[178:181], v[60:63]
	v_mfma_f32_16x16x32_bf16 v[52:55], v[154:157], v[186:189], v[52:55]
	v_mfma_f32_16x16x32_bf16 v[48:51], v[162:165], v[186:189], v[48:51]
	v_mfma_f32_16x16x32_bf16 v[44:47], v[154:157], v[194:197], v[44:47]
	v_mfma_f32_16x16x32_bf16 v[40:43], v[162:165], v[194:197], v[40:43]
	v_mfma_f32_16x16x32_bf16 v[36:39], v[154:157], v[202:205], v[36:39]
	v_mfma_f32_16x16x32_bf16 v[32:35], v[162:165], v[202:205], v[32:35]
	s_setprio 0
	s_waitcnt vmcnt(8)
	s_barrier
; #define G_STAGE(bufoff, gbase, voff) do { _Pragma("unroll") for (int _i = 0; _i < 2; ++_i) \
;         __builtin_amdgcn_global_load_lds((const unsigned*)((const char*)(gbase) + (voff)[_i]), (LAS unsigned*)(lds + (bufoff) + ldsw + _i * 8192), 16, 0, 0); } while (0)
; #define G_LDA(dst, b, h) do { _Pragma("unroll") for (int m = 0; m < 4; ++m) G_LD8(dst[m], lds + G_SA(b, h) + aoff + m * 2048); } while (0)
; #define G_WAIT_V(n) asm volatile("s_waitcnt vmcnt(" #n ")" ::: "memory")
; #define G_WAIT_L(n) asm volatile("s_waitcnt lgkmcnt(" #n ")" ::: "memory")
; #define G_BAR __builtin_amdgcn_s_barrier()
; #define G_SCHED __builtin_amdgcn_sched_barrier(0)
;     ...
;             G_LDA(At, 1, 1); G_STAGE(G_SB(1, 0), b02 + kstep, voffB); G_STAGE(G_SB(1, 1), b12 + kstep, voffB); G_STAGE(G_SA(1, 0), a02 + kstep, vA0);
;             G_WAIT_L(0); G_BAR; G_MMA(1, 0, At, B0); G_MMA(1, 1, At, B1); G_WAIT_V(8); G_BAR; G_SCHED;
;         }
;         if (wr == 0) G_BAR;
	s_add_i32 s1, s1, s77
	v_lshl_add_u64 v[128:129], v[208:209], 0, s[48:49]
	s_mov_b32 m0, s1
	ds_read_b128 v[174:177], v173 offset:49152
	ds_read_b128 v[178:181], v173 offset:50176
	ds_read_b128 v[182:185], v173 offset:51200
	ds_read_b128 v[186:189], v173 offset:52224
	ds_read_b128 v[190:193], v173 offset:53248
	ds_read_b128 v[194:197], v173 offset:54272
	ds_read_b128 v[198:201], v173 offset:55296
	ds_read_b128 v[202:205], v173 offset:56320
	global_load_lds_dwordx4 v[128:129], off
	v_lshl_add_u64 v[128:129], v[210:211], 0, s[48:49]
	s_add_i32 m0, s1, 0x2000
	s_add_i32 s1, s11, s77
	global_load_lds_dwordx4 v[128:129], off
	v_lshl_add_u64 v[128:129], v[212:213], 0, s[48:49]
	s_mov_b32 m0, s1
	s_nop 0
	global_load_lds_dwordx4 v[128:129], off
	v_lshl_add_u64 v[128:129], v[142:143], 0, s[48:49]
	s_add_i32 m0, s1, 0x2000
	s_nop 0
	global_load_lds_dwordx4 v[128:129], off
	v_lshl_add_u64 v[128:129], v[206:207], 0, s[48:49]
	s_mov_b32 m0, s75
	s_nop 0
	global_load_lds_dwordx4 v[128:129], off
	v_lshl_add_u64 v[128:129], v[214:215], 0, s[48:49]
	s_mov_b32 m0, s76
	s_nop 0
	global_load_lds_dwordx4 v[128:129], off
	s_waitcnt lgkmcnt(0)
	s_barrier
	s_setprio 1
	s_waitcnt lgkmcnt(0)
	v_mfma_f32_16x16x32_bf16 v[92:95], v[130:133], v[174:177], v[92:95]
	v_mfma_f32_16x16x32_bf16 v[88:91], v[138:141], v[174:177], v[88:91]
	v_mfma_f32_16x16x32_bf16 v[84:87], v[130:133], v[182:185], v[84:87]
	v_mfma_f32_16x16x32_bf16 v[80:83], v[138:141], v[182:185], v[80:83]
	v_mfma_f32_16x16x32_bf16 v[76:79], v[130:133], v[190:193], v[76:79]
	v_mfma_f32_16x16x32_bf16 v[72:75], v[138:141], v[190:193], v[72:75]
	v_mfma_f32_16x16x32_bf16 v[64:67], v[130:133], v[198:201], v[64:67]
	v_mfma_f32_16x16x32_bf16 v[56:59], v[138:141], v[198:201], v[56:59]
	v_mfma_f32_16x16x32_bf16 v[92:95], v[134:137], v[178:181], v[92:95]
	v_mfma_f32_16x16x32_bf16 v[88:91], v[146:149], v[178:181], v[88:91]
	v_mfma_f32_16x16x32_bf16 v[84:87], v[134:137], v[186:189], v[84:87]
	v_mfma_f32_16x16x32_bf16 v[80:83], v[146:149], v[186:189], v[80:83]
	v_mfma_f32_16x16x32_bf16 v[76:79], v[134:137], v[194:197], v[76:79]
	v_mfma_f32_16x16x32_bf16 v[72:75], v[146:149], v[194:197], v[72:75]
	v_mfma_f32_16x16x32_bf16 v[64:67], v[134:137], v[202:205], v[64:67]
	v_mfma_f32_16x16x32_bf16 v[56:59], v[146:149], v[202:205], v[56:59]
	s_setprio 0
	s_setprio 1
	v_mfma_f32_16x16x32_bf16 v[28:31], v[150:153], v[174:177], v[28:31]
	v_mfma_f32_16x16x32_bf16 v[24:27], v[158:161], v[174:177], v[24:27]
	v_mfma_f32_16x16x32_bf16 v[20:23], v[150:153], v[182:185], v[20:23]
	v_mfma_f32_16x16x32_bf16 v[16:19], v[158:161], v[182:185], v[16:19]
	v_mfma_f32_16x16x32_bf16 v[12:15], v[150:153], v[190:193], v[12:15]
	v_mfma_f32_16x16x32_bf16 v[8:11], v[158:161], v[190:193], v[8:11]
	v_mfma_f32_16x16x32_bf16 v[4:7], v[150:153], v[198:201], v[4:7]
	v_mfma_f32_16x16x32_bf16 v[0:3], v[158:161], v[198:201], v[0:3]
	v_mfma_f32_16x16x32_bf16 v[28:31], v[154:157], v[178:181], v[28:31]
	v_mfma_f32_16x16x32_bf16 v[24:27], v[162:165], v[178:181], v[24:27]
	v_mfma_f32_16x16x32_bf16 v[20:23], v[154:157], v[186:189], v[20:23]
	v_mfma_f32_16x16x32_bf16 v[16:19], v[162:165], v[186:189], v[16:19]
	v_mfma_f32_16x16x32_bf16 v[12:15], v[154:157], v[194:197], v[12:15]
	v_mfma_f32_16x16x32_bf16 v[8:11], v[162:165], v[194:197], v[8:11]
	v_mfma_f32_16x16x32_bf16 v[4:7], v[154:157], v[202:205], v[4:7]
	v_mfma_f32_16x16x32_bf16 v[0:3], v[162:165], v[202:205], v[0:3]
	s_setprio 0
	s_waitcnt vmcnt(8)
	s_barrier
	s_add_u32 s9, s9, 0x100
	s_addc_u32 s93, s93, 0
	s_add_u32 s94, s94, 0x100
	s_addc_u32 s95, s95, 0
	s_add_u32 s96, s96, 0x100
	s_addc_u32 s97, s97, 0
	s_add_u32 s64, s64, 0x100
	s_addc_u32 s65, s65, 0
	s_cmp_ge_i32 vcc_lo, s2
	s_mov_b32 s66, vcc_lo
	s_cbranch_scc0 .LBB0_1322
	v_readlane_b32 s64, v255, 9
	v_readlane_b32 s65, v255, 10
	s_load_dword s97, s[64:65], 0xa8
	s_and_b64 vcc, exec, s[46:47]
	s_cbranch_vccz .LBB0_1325

; #define LAS __attribute__((address_space(3)))
; __device__ __forceinline__ int lane_id() { int l; asm volatile("v_mbcnt_lo_u32_b32 %0, -1, 0\n\tv_mbcnt_hi_u32_b32 %0, -1, %0" : "=v"(l)); return l; }
;     ...
; #pragma unroll
;         for (int a = 0; a < 2; ++a)
; #pragma unroll
;             for (int b = 0; b < 2; ++b)
; #pragma unroll
;                 for (int m = 0; m < 4; ++m)
; #pragma unroll
;                     for (int n = 0; n < 2; ++n) acc[a][b][m][n] = (acc_t){0, 0, 0, 0};
;         cur = nxt; ++ui;
;     __device__ __forceinline__ void prefetch(const Unit& u, LAS unsigned char* lds) const {
;         LAS unsigned char* blk = lds + LDS_STAGE + u.q * 4096;
;         const int wid = wv, e = u.p2; int lane = lane_id(); asm volatile("" : "+v"(lane));
;         const int n = (int)cnt[64 * e]; int pos = u.p3 + (wid & 3) * 64 + lane; pos = pos < n ? pos : n - 1;
;         if (wid < 4) __builtin_amdgcn_global_load_lds((const unsigned*)(row_tok + (size_t)e * T + pos), (LAS unsigned*)(blk + wid * 256), 4, 0, 0);
;         else __builtin_amdgcn_global_load_lds((const unsigned*)(rsc + (size_t)e * T + pos), (LAS unsigned*)(blk + 1024 + (wid - 4) * 256), 4, 0, 0);
;         if (wid == 0) __builtin_amdgcn_global_load_lds((const unsigned*)(swup + (size_t)e * 2 * DFF + u.p1 * 256 + lane * 4), (LAS unsigned*)(blk + 2048), 16, 0, 0);
;         if (wid == 1) __builtin_amdgcn_global_load_lds((const unsigned*)(b_up + (size_t)e * 2 * DFF + u.p1 * 128 + (lane & 31) * 4 + (lane >> 5) * DFF), (LAS unsigned*)(blk + 3072), 16, 0, 0);
.LBB0_1624:
	s_andn2_b64 vcc, exec, s[8:9]
	s_and_b32 s20, s43, 1
	s_cbranch_vccnz .LBB0_1638
	s_lshl_b32 s21, s20, 12
	s_lshl_b32 s26, s48, 6
	s_add_i32 s21, s21, 0
	s_ashr_i32 s27, s26, 31
	s_ashr_i32 s49, s48, 31
	s_lshl_b32 s70, s1, 7
	s_lshl_b32 s80, s1, 8
	s_add_i32 s21, s21, 0x20000
	s_lshl_b64 s[36:37], s[48:49], 16
	s_lshl_b64 s[72:73], s[48:49], 14
	s_ashr_i32 s71, s70, 31
	s_ashr_i32 s81, s80, 31
	s_lshl_b64 s[26:27], s[26:27], 2
	v_readlane_b32 s31, v255, 18
	s_add_u32 s64, s31, s26
	s_addc_u32 s65, s47, s27
	s_add_i32 s49, s24, s10
	s_add_u32 s66, s84, s36
	s_addc_u32 s67, s86, s37
	v_readlane_b32 s26, v255, 14
	s_add_u32 s68, s26, s36
	v_readlane_b32 s26, v255, 16
	s_addc_u32 s69, s26, s37
	s_add_u32 s31, s12, s72
	s_addc_u32 s36, s13, s73
	s_lshl_b64 s[26:27], s[70:71], 2
	s_add_u32 s70, s31, s26
	s_addc_u32 s71, s36, s27
	v_readlane_b32 s26, v255, 19
	s_add_u32 s31, s26, s72
	v_readlane_b32 s26, v255, 22
	s_addc_u32 s36, s26, s73
	s_lshl_b64 s[26:27], s[80:81], 2
	s_add_u32 s72, s31, s26
	s_addc_u32 s73, s36, s27
	s_add_u32 s36, s74, 0x100
	s_addc_u32 s37, s75, 0
	s_add_u32 s87, s76, 0x100
	s_addc_u32 s90, s77, 0
	s_add_u32 s26, s78, 0x100
	s_addc_u32 s27, s79, 0
	s_mov_b32 s31, 0
	s_mov_b64 s[74:75], 0
	v_mov_b32_e32 v0, 0
	v_mov_b32_e32 v1, 0
	v_mov_b32_e32 v2, 0
	v_mov_b32_e32 v3, 0
	v_mov_b32_e32 v8, 0
	v_mov_b32_e32 v9, 0
	v_mov_b32_e32 v10, 0
	v_mov_b32_e32 v11, 0
	v_mov_b32_e32 v16, 0
	v_mov_b32_e32 v17, 0
	v_mov_b32_e32 v18, 0
	v_mov_b32_e32 v19, 0
	v_mov_b32_e32 v24, 0
	v_mov_b32_e32 v25, 0
	v_mov_b32_e32 v26, 0
	v_mov_b32_e32 v27, 0
	v_mov_b32_e32 v32, 0
	v_mov_b32_e32 v33, 0
	v_mov_b32_e32 v34, 0
	v_mov_b32_e32 v35, 0
	v_mov_b32_e32 v40, 0
	v_mov_b32_e32 v41, 0
	v_mov_b32_e32 v42, 0
	v_mov_b32_e32 v43, 0
	v_mov_b32_e32 v48, 0
	v_mov_b32_e32 v49, 0
	v_mov_b32_e32 v50, 0
	v_mov_b32_e32 v51, 0
	v_mov_b32_e32 v56, 0
	v_mov_b32_e32 v57, 0
	v_mov_b32_e32 v58, 0
	v_mov_b32_e32 v59, 0
	v_mov_b32_e32 v4, 0
	v_mov_b32_e32 v5, 0
	v_mov_b32_e32 v6, 0
	v_mov_b32_e32 v7, 0
	v_mov_b32_e32 v12, 0
	v_mov_b32_e32 v13, 0
	v_mov_b32_e32 v14, 0
	v_mov_b32_e32 v15, 0
	v_mov_b32_e32 v20, 0
	v_mov_b32_e32 v21, 0
	v_mov_b32_e32 v22, 0
	v_mov_b32_e32 v23, 0
	v_mov_b32_e32 v28, 0
	v_mov_b32_e32 v29, 0
	v_mov_b32_e32 v30, 0
	v_mov_b32_e32 v31, 0
	v_mov_b32_e32 v36, 0
	v_mov_b32_e32 v37, 0
	v_mov_b32_e32 v38, 0
	v_mov_b32_e32 v39, 0
	v_mov_b32_e32 v44, 0
	v_mov_b32_e32 v45, 0
	v_mov_b32_e32 v46, 0
	v_mov_b32_e32 v47, 0
	v_mov_b32_e32 v52, 0
	v_mov_b32_e32 v53, 0
	v_mov_b32_e32 v54, 0
	v_mov_b32_e32 v55, 0
	v_mov_b32_e32 v60, 0
	v_mov_b32_e32 v61, 0
	v_mov_b32_e32 v62, 0
	v_mov_b32_e32 v63, 0
	v_mov_b32_e32 v80, 0
	v_mov_b32_e32 v81, 0
	v_mov_b32_e32 v82, 0
	v_mov_b32_e32 v83, 0
	v_mov_b32_e32 v104, 0
	v_mov_b32_e32 v105, 0
	v_mov_b32_e32 v106, 0
	v_mov_b32_e32 v107, 0
	v_mov_b32_e32 v112, 0
	v_mov_b32_e32 v113, 0
	v_mov_b32_e32 v114, 0
	v_mov_b32_e32 v115, 0
	v_mov_b32_e32 v120, 0
	v_mov_b32_e32 v121, 0
	v_mov_b32_e32 v122, 0
	v_mov_b32_e32 v123, 0
	v_mov_b32_e32 v128, 0
	v_mov_b32_e32 v129, 0
	v_mov_b32_e32 v130, 0
	v_mov_b32_e32 v131, 0
	v_mov_b32_e32 v136, 0
	v_mov_b32_e32 v137, 0
	v_mov_b32_e32 v138, 0
	v_mov_b32_e32 v139, 0
	v_mov_b32_e32 v144, 0
	v_mov_b32_e32 v145, 0
	v_mov_b32_e32 v146, 0
	v_mov_b32_e32 v147, 0
	v_mov_b32_e32 v152, 0
	v_mov_b32_e32 v153, 0
	v_mov_b32_e32 v154, 0
	v_mov_b32_e32 v155, 0
	v_mov_b32_e32 v84, 0
	v_mov_b32_e32 v85, 0
	v_mov_b32_e32 v86, 0
	v_mov_b32_e32 v87, 0
	v_mov_b32_e32 v108, 0
	v_mov_b32_e32 v109, 0
	v_mov_b32_e32 v110, 0
	v_mov_b32_e32 v111, 0
	v_mov_b32_e32 v116, 0
	v_mov_b32_e32 v117, 0
	v_mov_b32_e32 v118, 0
	v_mov_b32_e32 v119, 0
	v_mov_b32_e32 v124, 0
	v_mov_b32_e32 v125, 0
	v_mov_b32_e32 v126, 0
	v_mov_b32_e32 v127, 0
	v_mov_b32_e32 v132, 0
	v_mov_b32_e32 v133, 0
	v_mov_b32_e32 v134, 0
	v_mov_b32_e32 v135, 0
	v_mov_b32_e32 v140, 0
	v_mov_b32_e32 v141, 0
	v_mov_b32_e32 v142, 0
	v_mov_b32_e32 v143, 0
	v_mov_b32_e32 v148, 0
	v_mov_b32_e32 v149, 0
	v_mov_b32_e32 v150, 0
	v_mov_b32_e32 v151, 0
	v_mov_b32_e32 v156, 0
	v_mov_b32_e32 v157, 0
	v_mov_b32_e32 v158, 0
	v_mov_b32_e32 v159, 0
	v_mbcnt_lo_u32_b32 v248, -1, 0
	v_mbcnt_hi_u32_b32 v248, -1, v248
	v_mov_b32_e32 v249, s88
	v_lshrrev_b32_e32 v249, 6, v249
	v_and_b32_e32 v250, 3, v248
	v_lshlrev_b32_e32 v250, 4, v250
	v_and_b32_e32 v251, 32, v248
	v_xor_b32_e32 v250, v250, v251
	v_and_b32_e32 v251, 1, v249
	v_lshl_add_u32 v250, v251, 6, v250
	v_lshrrev_b32_e32 v251, 1, v249
	v_lshrrev_b32_e32 v252, 2, v248
	v_lshl_add_u32 v251, v251, 4, v252
	v_lshrrev_b32_e32 v251, 2, v249
	v_lshlrev_b32_e32 v251, 5, v251
	v_lshrrev_b32_e32 v252, 4, v248
	v_lshl_add_u32 v251, v252, 3, v251
	v_bfe_u32 v252, v249, 1, 1
	v_lshl_add_u32 v251, v252, 2, v251
	v_bfe_u32 v252, v248, 2, 2
	v_add_u32_e32 v251, v251, v252
	v_mov_b32_e32 v253, 0x800
	v_mad_u32_u24 v244, v251, v253, v250
	v_add_u32_e32 v246, 0x20000, v244
	v_mov_b32_e32 v245, 0
	v_mov_b32_e32 v247, 0
	s_branch .LBB0_1627
; __device__ __forceinline__ int lane_id() { int l; asm volatile("v_mbcnt_lo_u32_b32 %0, -1, 0\n\tv_mbcnt_hi_u32_b32 %0, -1, %0" : "=v"(l)); return l; }
; #define G_STAGE(bufoff, gbase, voff) do { _Pragma("unroll") for (int _i = 0; _i < 2; ++_i) \
;         __builtin_amdgcn_global_load_lds((const unsigned*)((const char*)(gbase) + (voff)[_i]), (LAS unsigned*)(lds + (bufoff) + ldsw + _i * 8192), 16, 0, 0); } while (0)
; #define G_LDA(dst, b, h) do { _Pragma("unroll") for (int m = 0; m < 4; ++m) G_LD8(dst[m], lds + G_SA(b, h) + aoff + m * 2048); } while (0)
; #define G_LDB(dst, b, h) do { _Pragma("unroll") for (int n = 0; n < 2; ++n) G_LD8(dst[n], lds + G_SB(b, h) + boff + n * 2048); } while (0)
;     ...
;             { const int tz_ = wid * 64 + lane_id();
; #pragma unroll
;               for (int i = 0; i < 2; ++i) { int R, C; stage_rc(tz_ * 16 + i * 8192, R, C); const int Rb = Epi::PERM ? ((R & ~31) + perm32(R & 31)) : R;
;                   voffA[i] = (unsigned)(R * S.multA * S.pitchA + C) * 2u; voffB[i] = (unsigned)(Rb * S.multB * S.pitchB + C) * 2u; } }
;             if constexpr (GATHER) asm volatile("" : "+v"(gc0[0]), "+v"(gc0[1]), "+v"(gc1[0]), "+v"(gc1[1]));
;             if constexpr (PREF) { if (t == nt - 4) S.prefetch(nxt, lds); }
;             const char* a11 = cur.a1 + (size_t)(t + 1) * kstep;
;             const char* a02 = last ? nxt.a0 : cur.a0 + (size_t)(t + 2) * kstep; const char* a12 = last ? nxt.a1 : cur.a1 + (size_t)(t + 2) * kstep;
;             const char* b02 = last ? nxt.b0 : cur.b0 + (size_t)(t + 2) * kstep; const char* b12 = last ? nxt.b1 : cur.b1 + (size_t)(t + 2) * kstep;
;             G_LDB(B0, 0, 0); G_LDB(B1, 0, 1); G_SCHED; G_LDA(At, 0, 0); G_STAGE(G_SA(1, 1), a11, vA1);
;             if constexpr (GATHER) { if (last) { int tz = tid; asm volatile("" : "+v"(tz));
; #pragma unroll
;                 for (int i = 0; i < 2; ++i) { int R, C; stage_rc(tz * 16 + i * 8192, R, C); gc0[i] = S.row_off(nxt, R, lds) + (unsigned)C * 2u; gc1[i] = S.row_off(nxt, 128 + R, lds) + (unsigned)C * 2u; } } }
;             G_WAIT_L(0); G_BAR; G_MMA(0, 0, At, B0); G_MMA(0, 1, At, B1); G_WAIT_V(8); G_BAR; G_SCHED;
;             G_LDA(At, 0, 1); G_STAGE(G_SB(0, 0), b02, voffB); G_STAGE(G_SB(0, 1), b12, voffB); G_STAGE(G_SA(0, 0), a02, vA0);
;             G_WAIT_L(0); G_BAR; G_MMA(1, 0, At, B0); G_MMA(1, 1, At, B1); G_WAIT_V(8); G_BAR; G_SCHED;
.LBB0_1626:
	s_add_i32 s31, s31, 2
	s_add_u32 s78, s26, s74
	s_addc_u32 s79, s27, s75
	s_add_u32 s80, s62, s74
	s_addc_u32 s81, s63, s75
	s_add_u32 s82, s80, 0x100
	s_addc_u32 s83, s81, 0
	s_add_u32 s80, s36, s74
	s_addc_u32 s81, s37, s75
	s_add_u32 vcc_lo, s87, s74
	s_waitcnt lgkmcnt(0)
	s_addc_u32 vcc_hi, s90, s75
	s_and_b64 s[76:77], s[76:77], exec
	s_cselect_b32 s79, s57, s79
	s_cselect_b32 s78, s56, s78
	s_cselect_b32 s81, s51, s81
	s_cselect_b32 s80, s50, s80
	s_cselect_b32 s77, s55, s83
	s_cselect_b32 s76, s54, s82
	s_cselect_b32 s83, s53, vcc_hi
	s_cselect_b32 s82, s52, vcc_lo
	s_barrier
	s_setprio 1
	s_waitcnt lgkmcnt(0)
	v_mfma_i32_16x16x64_i8 v[156:159], v[88:91], v[184:187], v[156:159]
	v_mfma_i32_16x16x64_i8 v[148:151], v[96:99], v[184:187], v[148:151]
	v_mfma_i32_16x16x64_i8 v[140:143], v[88:91], v[176:179], v[140:143]
	v_mfma_i32_16x16x64_i8 v[132:135], v[96:99], v[176:179], v[132:135]
	v_mfma_i32_16x16x64_i8 v[124:127], v[88:91], v[168:171], v[124:127]
	v_mfma_i32_16x16x64_i8 v[116:119], v[96:99], v[168:171], v[116:119]
	v_mfma_i32_16x16x64_i8 v[108:111], v[88:91], v[160:163], v[108:111]
	v_mfma_i32_16x16x64_i8 v[84:87], v[96:99], v[160:163], v[84:87]
	v_mfma_i32_16x16x64_i8 v[156:159], v[92:95], v[188:191], v[156:159]
	v_mfma_i32_16x16x64_i8 v[148:151], v[100:103], v[188:191], v[148:151]
	v_mfma_i32_16x16x64_i8 v[140:143], v[92:95], v[180:183], v[140:143]
	v_mfma_i32_16x16x64_i8 v[132:135], v[100:103], v[180:183], v[132:135]
	v_mfma_i32_16x16x64_i8 v[124:127], v[92:95], v[172:175], v[124:127]
	v_mfma_i32_16x16x64_i8 v[116:119], v[100:103], v[172:175], v[116:119]
	v_mfma_i32_16x16x64_i8 v[108:111], v[92:95], v[164:167], v[108:111]
	v_mfma_i32_16x16x64_i8 v[84:87], v[100:103], v[164:167], v[84:87]
	s_setprio 0
	s_setprio 1
	v_mfma_i32_16x16x64_i8 v[152:155], v[64:67], v[184:187], v[152:155]
	v_mfma_i32_16x16x64_i8 v[144:147], v[72:75], v[184:187], v[144:147]
	v_mfma_i32_16x16x64_i8 v[136:139], v[64:67], v[176:179], v[136:139]
	v_mfma_i32_16x16x64_i8 v[128:131], v[72:75], v[176:179], v[128:131]
	v_mfma_i32_16x16x64_i8 v[120:123], v[64:67], v[168:171], v[120:123]
	v_mfma_i32_16x16x64_i8 v[112:115], v[72:75], v[168:171], v[112:115]
	v_mfma_i32_16x16x64_i8 v[104:107], v[64:67], v[160:163], v[104:107]
	v_mfma_i32_16x16x64_i8 v[80:83], v[72:75], v[160:163], v[80:83]
	v_mfma_i32_16x16x64_i8 v[152:155], v[68:71], v[188:191], v[152:155]
	v_mfma_i32_16x16x64_i8 v[144:147], v[76:79], v[188:191], v[144:147]
	v_mfma_i32_16x16x64_i8 v[136:139], v[68:71], v[180:183], v[136:139]
	v_mfma_i32_16x16x64_i8 v[128:131], v[76:79], v[180:183], v[128:131]
	v_mfma_i32_16x16x64_i8 v[120:123], v[68:71], v[172:175], v[120:123]
	v_mfma_i32_16x16x64_i8 v[112:115], v[76:79], v[172:175], v[112:115]
	v_mfma_i32_16x16x64_i8 v[104:107], v[68:71], v[164:167], v[104:107]
	v_mfma_i32_16x16x64_i8 v[80:83], v[76:79], v[164:167], v[80:83]
	s_setprio 0
	s_waitcnt vmcnt(8)
	s_barrier
	s_mov_b32 m0, s34
	ds_read_b128 v[160:163], v208 offset:16384
	ds_read_b128 v[164:167], v208 offset:17408
	ds_read_b128 v[168:171], v208 offset:18432
	ds_read_b128 v[172:175], v208 offset:19456
	ds_read_b128 v[176:179], v208 offset:20480
	ds_read_b128 v[180:183], v208 offset:21504
	ds_read_b128 v[184:187], v208 offset:22528
	ds_read_b128 v[188:191], v208 offset:23552
	global_load_lds_dwordx4 v244, s[80:81]
	s_mov_b32 m0, s35
	v_mov_b32_e32 v211, v193
	global_load_lds_dwordx4 v246, s[80:81]
	s_mov_b32 m0, s30
	v_mov_b32_e32 v213, v193
	global_load_lds_dwordx4 v244, s[82:83]
	s_mov_b32 m0, s0
	v_mov_b32_e32 v195, v193
	global_load_lds_dwordx4 v246, s[82:83]
	s_mov_b32 m0, s3
	v_mov_b32_e32 v197, v193
	global_load_lds_dwordx4 v194, s[78:79]
	s_mov_b32 m0, s40
	v_lshl_add_u64 v[214:215], s[80:81], 0, v[244:245]
	global_load_lds_dwordx4 v196, s[78:79]
	s_waitcnt lgkmcnt(0)
	v_lshl_add_u64 v[216:217], s[80:81], 0, v[246:247]
	v_lshl_add_u64 v[210:211], s[82:83], 0, v[244:245]
	v_lshl_add_u64 v[212:213], s[82:83], 0, v[246:247]
	v_lshl_add_u64 v[218:219], s[78:79], 0, v[194:195]
	v_lshl_add_u64 v[220:221], s[78:79], 0, v[196:197]
	s_barrier
	s_setprio 1
	s_waitcnt lgkmcnt(0)
	v_mfma_i32_16x16x64_i8 v[60:63], v[88:91], v[160:163], v[60:63]
	v_mfma_i32_16x16x64_i8 v[52:55], v[96:99], v[160:163], v[52:55]
	v_mfma_i32_16x16x64_i8 v[44:47], v[88:91], v[168:171], v[44:47]
	v_mfma_i32_16x16x64_i8 v[36:39], v[96:99], v[168:171], v[36:39]
	v_mfma_i32_16x16x64_i8 v[28:31], v[88:91], v[176:179], v[28:31]
	v_mfma_i32_16x16x64_i8 v[20:23], v[96:99], v[176:179], v[20:23]
	v_mfma_i32_16x16x64_i8 v[12:15], v[88:91], v[184:187], v[12:15]
	v_mfma_i32_16x16x64_i8 v[4:7], v[96:99], v[184:187], v[4:7]
	v_mfma_i32_16x16x64_i8 v[60:63], v[92:95], v[164:167], v[60:63]
	v_mfma_i32_16x16x64_i8 v[52:55], v[100:103], v[164:167], v[52:55]
	v_mfma_i32_16x16x64_i8 v[44:47], v[92:95], v[172:175], v[44:47]
	v_mfma_i32_16x16x64_i8 v[36:39], v[100:103], v[172:175], v[36:39]
	v_mfma_i32_16x16x64_i8 v[28:31], v[92:95], v[180:183], v[28:31]
	v_mfma_i32_16x16x64_i8 v[20:23], v[100:103], v[180:183], v[20:23]
	v_mfma_i32_16x16x64_i8 v[12:15], v[92:95], v[188:191], v[12:15]
	v_mfma_i32_16x16x64_i8 v[4:7], v[100:103], v[188:191], v[4:7]
	s_setprio 0
	s_setprio 1
	v_mfma_i32_16x16x64_i8 v[56:59], v[64:67], v[160:163], v[56:59]
	v_mfma_i32_16x16x64_i8 v[48:51], v[72:75], v[160:163], v[48:51]
	v_mfma_i32_16x16x64_i8 v[40:43], v[64:67], v[168:171], v[40:43]
	v_mfma_i32_16x16x64_i8 v[32:35], v[72:75], v[168:171], v[32:35]
	v_mfma_i32_16x16x64_i8 v[24:27], v[64:67], v[176:179], v[24:27]
	v_mfma_i32_16x16x64_i8 v[16:19], v[72:75], v[176:179], v[16:19]
	v_mfma_i32_16x16x64_i8 v[8:11], v[64:67], v[184:187], v[8:11]
	v_mfma_i32_16x16x64_i8 v[0:3], v[72:75], v[184:187], v[0:3]
	v_mfma_i32_16x16x64_i8 v[56:59], v[68:71], v[164:167], v[56:59]
	v_mfma_i32_16x16x64_i8 v[48:51], v[76:79], v[164:167], v[48:51]
	v_mfma_i32_16x16x64_i8 v[40:43], v[68:71], v[172:175], v[40:43]
	v_mfma_i32_16x16x64_i8 v[32:35], v[76:79], v[172:175], v[32:35]
	v_mfma_i32_16x16x64_i8 v[24:27], v[68:71], v[180:183], v[24:27]
	v_mfma_i32_16x16x64_i8 v[16:19], v[76:79], v[180:183], v[16:19]
	v_mfma_i32_16x16x64_i8 v[8:11], v[68:71], v[188:191], v[8:11]
	v_mfma_i32_16x16x64_i8 v[0:3], v[76:79], v[188:191], v[0:3]
	s_setprio 0
	s_waitcnt vmcnt(8)
	s_barrier
; #define G_STAGE(bufoff, gbase, voff) do { _Pragma("unroll") for (int _i = 0; _i < 2; ++_i) \
;         __builtin_amdgcn_global_load_lds((const unsigned*)((const char*)(gbase) + (voff)[_i]), (LAS unsigned*)(lds + (bufoff) + ldsw + _i * 8192), 16, 0, 0); } while (0)
; #define G_LDA(dst, b, h) do { _Pragma("unroll") for (int m = 0; m < 4; ++m) G_LD8(dst[m], lds + G_SA(b, h) + aoff + m * 2048); } while (0)
; #define G_LDB(dst, b, h) do { _Pragma("unroll") for (int n = 0; n < 2; ++n) G_LD8(dst[n], lds + G_SB(b, h) + boff + n * 2048); } while (0)
; #define G_WAIT_V(n) asm volatile("s_waitcnt vmcnt(" #n ")" ::: "memory")
; #define G_WAIT_L(n) asm volatile("s_waitcnt lgkmcnt(" #n ")" ::: "memory")
; #define G_BAR __builtin_amdgcn_s_barrier()
; #define G_SCHED __builtin_amdgcn_sched_barrier(0)
;     ...
;             G_LDB(B0, 1, 0); G_LDB(B1, 1, 1); G_SCHED; G_LDA(At, 1, 0); G_STAGE(G_SA(0, 1), a12, vA1);
;             G_WAIT_L(0); G_BAR; G_MMA(0, 0, At, B0); G_MMA(0, 1, At, B1); G_WAIT_V(8); G_BAR; G_SCHED;
;             G_LDA(At, 1, 1); G_STAGE(G_SB(1, 0), b02 + kstep, voffB); G_STAGE(G_SB(1, 1), b12 + kstep, voffB); G_STAGE(G_SA(1, 0), a02 + kstep, vA0);
;             G_WAIT_L(0); G_BAR; G_MMA(1, 0, At, B0); G_MMA(1, 1, At, B1); G_WAIT_V(8); G_BAR; G_SCHED;
;         }
	s_add_i32 s78, 0, 0x18000
	s_add_i32 s79, 0, 0x1c000
	v_add_u32_e32 v76, s78, v203
	v_add_u32_e32 v100, s79, v203
	ds_read_b128 v[64:67], v76
	ds_read_b128 v[68:71], v76 offset:1024
	ds_read_b128 v[72:75], v76 offset:2048
	ds_read_b128 v[76:79], v76 offset:3072
	ds_read_b128 v[88:91], v100
	ds_read_b128 v[92:95], v100 offset:1024
	ds_read_b128 v[96:99], v100 offset:2048
	ds_read_b128 v[100:103], v100 offset:3072
	s_mov_b32 m0, s41
	v_lshl_add_u64 v[222:223], s[76:77], 0, v[192:193]
	ds_read_b128 v[160:163], v208 offset:32768
	ds_read_b128 v[164:167], v208 offset:33792
	ds_read_b128 v[168:171], v208 offset:34816
	ds_read_b128 v[172:175], v208 offset:35840
	ds_read_b128 v[176:179], v208 offset:36864
	ds_read_b128 v[180:183], v208 offset:37888
	ds_read_b128 v[184:187], v208 offset:38912
	ds_read_b128 v[188:191], v208 offset:39936
	global_load_lds_dwordx4 v[222:223], off
	v_lshl_add_u64 v[222:223], s[76:77], 0, v[198:199]
	s_mov_b32 m0, s18
	s_nop 0
	global_load_lds_dwordx4 v[222:223], off
	s_waitcnt lgkmcnt(0)
	s_barrier
	s_setprio 1
	s_waitcnt lgkmcnt(0)
	v_mfma_i32_16x16x64_i8 v[156:159], v[64:67], v[160:163], v[156:159]
	v_mfma_i32_16x16x64_i8 v[148:151], v[72:75], v[160:163], v[148:151]
	v_mfma_i32_16x16x64_i8 v[140:143], v[64:67], v[168:171], v[140:143]
	v_mfma_i32_16x16x64_i8 v[132:135], v[72:75], v[168:171], v[132:135]
	v_mfma_i32_16x16x64_i8 v[124:127], v[64:67], v[176:179], v[124:127]
	v_mfma_i32_16x16x64_i8 v[116:119], v[72:75], v[176:179], v[116:119]
	v_mfma_i32_16x16x64_i8 v[108:111], v[64:67], v[184:187], v[108:111]
	v_mfma_i32_16x16x64_i8 v[84:87], v[72:75], v[184:187], v[84:87]
	v_mfma_i32_16x16x64_i8 v[156:159], v[68:71], v[164:167], v[156:159]
	v_mfma_i32_16x16x64_i8 v[148:151], v[76:79], v[164:167], v[148:151]
	v_mfma_i32_16x16x64_i8 v[140:143], v[68:71], v[172:175], v[140:143]
	v_mfma_i32_16x16x64_i8 v[132:135], v[76:79], v[172:175], v[132:135]
	v_mfma_i32_16x16x64_i8 v[124:127], v[68:71], v[180:183], v[124:127]
	v_mfma_i32_16x16x64_i8 v[116:119], v[76:79], v[180:183], v[116:119]
	v_mfma_i32_16x16x64_i8 v[108:111], v[68:71], v[188:191], v[108:111]
	v_mfma_i32_16x16x64_i8 v[84:87], v[76:79], v[188:191], v[84:87]
	s_setprio 0
	s_setprio 1
	v_mfma_i32_16x16x64_i8 v[152:155], v[88:91], v[160:163], v[152:155]
	v_mfma_i32_16x16x64_i8 v[144:147], v[96:99], v[160:163], v[144:147]
	v_mfma_i32_16x16x64_i8 v[136:139], v[88:91], v[168:171], v[136:139]
	v_mfma_i32_16x16x64_i8 v[128:131], v[96:99], v[168:171], v[128:131]
	v_mfma_i32_16x16x64_i8 v[120:123], v[88:91], v[176:179], v[120:123]
	v_mfma_i32_16x16x64_i8 v[112:115], v[96:99], v[176:179], v[112:115]
	v_mfma_i32_16x16x64_i8 v[104:107], v[88:91], v[184:187], v[104:107]
	v_mfma_i32_16x16x64_i8 v[80:83], v[96:99], v[184:187], v[80:83]
	v_mfma_i32_16x16x64_i8 v[152:155], v[92:95], v[164:167], v[152:155]
	v_mfma_i32_16x16x64_i8 v[144:147], v[100:103], v[164:167], v[144:147]
	v_mfma_i32_16x16x64_i8 v[136:139], v[92:95], v[172:175], v[136:139]
	v_mfma_i32_16x16x64_i8 v[128:131], v[100:103], v[172:175], v[128:131]
	v_mfma_i32_16x16x64_i8 v[120:123], v[92:95], v[180:183], v[120:123]
	v_mfma_i32_16x16x64_i8 v[112:115], v[100:103], v[180:183], v[112:115]
	v_mfma_i32_16x16x64_i8 v[104:107], v[92:95], v[188:191], v[104:107]
	v_mfma_i32_16x16x64_i8 v[80:83], v[100:103], v[188:191], v[80:83]
	s_setprio 0
	s_waitcnt vmcnt(8)
	s_barrier
	s_add_i32 s76, s78, s93
	v_lshl_add_u64 v[214:215], v[214:215], 0, s[44:45]
	s_mov_b32 m0, s76
	ds_read_b128 v[160:163], v208 offset:49152
	ds_read_b128 v[164:167], v208 offset:50176
	ds_read_b128 v[168:171], v208 offset:51200
	ds_read_b128 v[172:175], v208 offset:52224
	ds_read_b128 v[176:179], v208 offset:53248
	ds_read_b128 v[180:183], v208 offset:54272
	ds_read_b128 v[184:187], v208 offset:55296
	ds_read_b128 v[188:191], v208 offset:56320
	global_load_lds_dwordx4 v[214:215], off
	v_lshl_add_u64 v[214:215], v[216:217], 0, s[44:45]
	s_add_i32 m0, s76, 0x2000
	s_add_i32 s76, s79, s93
	global_load_lds_dwordx4 v[214:215], off
	v_lshl_add_u64 v[210:211], v[210:211], 0, s[44:45]
	s_mov_b32 m0, s76
	s_nop 0
	global_load_lds_dwordx4 v[210:211], off
	v_lshl_add_u64 v[210:211], v[212:213], 0, s[44:45]
	s_add_i32 m0, s76, 0x2000
	s_nop 0
	global_load_lds_dwordx4 v[210:211], off
	v_lshl_add_u64 v[210:211], v[218:219], 0, s[44:45]
	s_mov_b32 m0, s19
	s_nop 0
	global_load_lds_dwordx4 v[210:211], off
	v_lshl_add_u64 v[210:211], v[220:221], 0, s[44:45]
	s_mov_b32 m0, s89
	s_nop 0
	global_load_lds_dwordx4 v[210:211], off
	s_waitcnt lgkmcnt(0)
	s_barrier
	s_setprio 1
	s_waitcnt lgkmcnt(0)
	v_mfma_i32_16x16x64_i8 v[60:63], v[64:67], v[160:163], v[60:63]
	v_mfma_i32_16x16x64_i8 v[52:55], v[72:75], v[160:163], v[52:55]
	v_mfma_i32_16x16x64_i8 v[44:47], v[64:67], v[168:171], v[44:47]
	v_mfma_i32_16x16x64_i8 v[36:39], v[72:75], v[168:171], v[36:39]
	v_mfma_i32_16x16x64_i8 v[28:31], v[64:67], v[176:179], v[28:31]
	v_mfma_i32_16x16x64_i8 v[20:23], v[72:75], v[176:179], v[20:23]
	v_mfma_i32_16x16x64_i8 v[12:15], v[64:67], v[184:187], v[12:15]
	v_mfma_i32_16x16x64_i8 v[4:7], v[72:75], v[184:187], v[4:7]
	v_mfma_i32_16x16x64_i8 v[60:63], v[68:71], v[164:167], v[60:63]
	v_mfma_i32_16x16x64_i8 v[52:55], v[76:79], v[164:167], v[52:55]
	v_mfma_i32_16x16x64_i8 v[44:47], v[68:71], v[172:175], v[44:47]
	v_mfma_i32_16x16x64_i8 v[36:39], v[76:79], v[172:175], v[36:39]
	v_mfma_i32_16x16x64_i8 v[28:31], v[68:71], v[180:183], v[28:31]
	v_mfma_i32_16x16x64_i8 v[20:23], v[76:79], v[180:183], v[20:23]
	v_mfma_i32_16x16x64_i8 v[12:15], v[68:71], v[188:191], v[12:15]
	v_mfma_i32_16x16x64_i8 v[4:7], v[76:79], v[188:191], v[4:7]
	s_setprio 0
	s_setprio 1
	v_mfma_i32_16x16x64_i8 v[56:59], v[88:91], v[160:163], v[56:59]
	v_mfma_i32_16x16x64_i8 v[48:51], v[96:99], v[160:163], v[48:51]
	v_mfma_i32_16x16x64_i8 v[40:43], v[88:91], v[168:171], v[40:43]
	v_mfma_i32_16x16x64_i8 v[32:35], v[96:99], v[168:171], v[32:35]
	v_mfma_i32_16x16x64_i8 v[24:27], v[88:91], v[176:179], v[24:27]
	v_mfma_i32_16x16x64_i8 v[16:19], v[96:99], v[176:179], v[16:19]
	v_mfma_i32_16x16x64_i8 v[8:11], v[88:91], v[184:187], v[8:11]
	v_mfma_i32_16x16x64_i8 v[0:3], v[96:99], v[184:187], v[0:3]
	v_mfma_i32_16x16x64_i8 v[56:59], v[92:95], v[164:167], v[56:59]
	v_mfma_i32_16x16x64_i8 v[48:51], v[100:103], v[164:167], v[48:51]
	v_mfma_i32_16x16x64_i8 v[40:43], v[92:95], v[172:175], v[40:43]
	v_mfma_i32_16x16x64_i8 v[32:35], v[100:103], v[172:175], v[32:35]
	v_mfma_i32_16x16x64_i8 v[24:27], v[92:95], v[180:183], v[24:27]
	v_mfma_i32_16x16x64_i8 v[16:19], v[100:103], v[180:183], v[16:19]
	v_mfma_i32_16x16x64_i8 v[8:11], v[92:95], v[188:191], v[8:11]
	v_mfma_i32_16x16x64_i8 v[0:3], v[100:103], v[188:191], v[0:3]
	s_setprio 0
	s_waitcnt vmcnt(8)
	s_barrier
	s_add_u32 s74, s74, 0x100
	s_addc_u32 s75, s75, 0
	s_cmp_ge_i32 s31, s33
	s_cbranch_scc1 .LBB0_1639
; #define LAS __attribute__((address_space(3)))
; __device__ __forceinline__ int lane_id() { int l; asm volatile("v_mbcnt_lo_u32_b32 %0, -1, 0\n\tv_mbcnt_hi_u32_b32 %0, -1, %0" : "=v"(l)); return l; }
;     ...
;         for (int t = 0; t < nt; t += 2) {
;             const bool last = (t == nt - 2);
;             { const int tz_ = wid * 64 + lane_id();
; #pragma unroll
;               for (int i = 0; i < 2; ++i) { int R, C; stage_rc(tz_ * 16 + i * 8192, R, C); const int Rb = Epi::PERM ? ((R & ~31) + perm32(R & 31)) : R;
;                   voffA[i] = (unsigned)(R * S.multA * S.pitchA + C) * 2u; voffB[i] = (unsigned)(Rb * S.multB * S.pitchB + C) * 2u; } }
;             if constexpr (GATHER) asm volatile("" : "+v"(gc0[0]), "+v"(gc0[1]), "+v"(gc1[0]), "+v"(gc1[1]));
;             if constexpr (PREF) { if (t == nt - 4) S.prefetch(nxt, lds); }
;     __device__ __forceinline__ void prefetch(const Unit& u, LAS unsigned char* lds) const {
;         LAS unsigned char* blk = lds + LDS_STAGE + u.q * 4096;
;         const int wid = wv, e = u.p2; int lane = lane_id(); asm volatile("" : "+v"(lane));
;         const int n = (int)cnt[64 * e]; int pos = u.p3 + (wid & 3) * 64 + lane; pos = pos < n ? pos : n - 1;
;         if (wid < 4) __builtin_amdgcn_global_load_lds((const unsigned*)(row_tok + (size_t)e * T + pos), (LAS unsigned*)(blk + wid * 256), 4, 0, 0);
;         else __builtin_amdgcn_global_load_lds((const unsigned*)(rsc + (size_t)e * T + pos), (LAS unsigned*)(blk + 1024 + (wid - 4) * 256), 4, 0, 0);
;         if (wid == 0) __builtin_amdgcn_global_load_lds((const unsigned*)(swup + (size_t)e * 2 * DFF + u.p1 * 256 + lane * 4), (LAS unsigned*)(blk + 2048), 16, 0, 0);
;         if (wid == 1) __builtin_amdgcn_global_load_lds((const unsigned*)(b_up + (size_t)e * 2 * DFF + u.p1 * 128 + (lane & 31) * 4 + (lane >> 5) * DFF), (LAS unsigned*)(blk + 3072), 16, 0, 0);
.LBB0_1627:
	s_cmp_lg_u32 s22, s31
	s_cbranch_scc1 .LBB0_1636
	v_mbcnt_lo_u32_b32 v67, -1, 0
	v_mbcnt_hi_u32_b32 v67, -1, v67
	v_add_u32_e32 v65, s21, v204
	global_load_dword v64, v193, s[64:65]
	v_readfirstlane_b32 s76, v65
	v_add_u32_e32 v65, s49, v67
	s_mov_b32 m0, s76
	s_cmp_lt_i32 s85, 1
	s_waitcnt vmcnt(0)
	v_add_u32_e32 v64, -1, v64
	v_min_i32_e32 v64, v65, v64
	v_ashrrev_i32_e32 v65, 31, v64
	v_lshlrev_b64 v[64:65], 2, v[64:65]
	v_lshl_add_u64 v[68:69], s[66:67], 0, v[64:65]
	v_lshl_add_u64 v[64:65], s[68:69], 0, v[64:65]
	v_cndmask_b32_e64 v65, v69, v65, s[4:5]
	v_cndmask_b32_e64 v64, v68, v64, s[4:5]
	global_load_lds_dword v[64:65], off
	s_cbranch_scc1 .LBB0_1633
	s_mov_b64 s[78:79], 0
	s_cmp_eq_u32 s85, 1
	s_mov_b64 s[76:77], 0
	s_cbranch_scc0 .LBB0_1631
	v_lshlrev_b32_e32 v64, 4, v67
	v_and_b32_e32 v64, 0x1f0, v64
	v_mov_b32_e32 v65, v193
	v_lshlrev_b32_e32 v66, 6, v67
	v_lshl_add_u64 v[64:65], s[70:71], 0, v[64:65]
	v_and_b32_e32 v66, 0xfffff800, v66
	s_mov_b64 s[76:77], -1
	s_movk_i32 s80, 0xc00
	s_and_b64 vcc, exec, s[78:79]
	s_cbranch_vccz .LBB0_1634
	s_branch .LBB0_1632
